# P12 down-weight conversion: hand-written 3-items-in-flight converter AND conversion slot = (bx>>3)&7 so each XCD has only 4 converting WGs at a time (was a whole XCD at once)
# baseline (speedup 1.0000x reference)
;     __device__ __forceinline__ void operator()(const f32x4 (&acc)[2][2][4][2], const Unit& u, int wr, int wc, int fr, int fq) const {
;         asm volatile("" : "+v"(fr), "+v"(fq));
;         const int e = blkE[u.z], c0 = u.pn * 128 + wc * 32 + 8 * fq, row0 = wr * 64 + fr;
;         const float* bg = bup + (size_t)e * 2 * FF + c0; const f32x4 g0 = *(const f32x4*)bg, g1 = *(const f32x4*)(bg + 4), l0 = *(const f32x4*)(bg + FF), l1 = *(const f32x4*)(bg + FF + 4);
;         float rsb[8];
; #pragma unroll
;         for (int q = 0; q < 8; ++q) rsb[q] = ssq[tokTab[u.pm * 256 + row0 + (q >> 2) * 128 + (q & 3) * 16]] * W8_INV;
; #pragma unroll
;         for (int ai = 0; ai < 2; ++ai)
; #pragma unroll
;             for (int m = 0; m < 4; ++m) { const int r = row0 + ai * 128 + m * 16; const float rs = rsb[ai * 4 + m];
;                 float a[8];
; #pragma unroll
;                 for (int j = 0; j < 8; ++j) { const float gb = j < 4 ? g0[j & 3] : g1[j & 3], lb = j < 4 ? l0[j & 3] : l1[j & 3];
;                     const float gl = fminf(acc[ai][0][m][j >> 2][j & 3] * rs + gb, 7.0f), ln = fminf(fmaxf(acc[ai][1][m][j >> 2][j & 3] * rs + lb, -7.0f), 7.0f);
;                     a[j] = gl * __builtin_amdgcn_rcpf(1.0f + __builtin_amdgcn_exp2f(-1.702f * 1.4426950408889634f * gl)) * (ln + 1.0f); }
;                 v2u w; w.x = pk4_fp8(a[0], a[1], a[2], a[3]); w.y = pk4_fp8(a[4], a[5], a[6], a[7]);
;                 *(v2u*)(ACT + ((size_t)u.z * 256 + r) * FF + c0) = w; }
;     __device__ __forceinline__ void done(const Unit& u) const { if (u.pm == (c & 7)) convert_share(); }
.LBB0_1534:
	s_lshl_b32 s4, s40, 7
	v_mov_b32_e32 v2, v218
	v_mov_b32_e32 v3, v219
	s_or_b32 s4, s4, s89
	v_mov_b32_e32 v0, s35
	v_lshl_add_u32 v16, v3, 3, s4
	v_readlane_b32 s0, v254, 2
	v_readlane_b32 s4, v254, 6
	s_lshl_b32 s4, s65, 10
	v_add_u32_e32 v18, s88, v2
	s_add_i32 s4, s4, 0
	v_lshl_add_u32 v2, v18, 2, s4
	v_add_u32_e32 v9, 0x20400, v2
	ds_read2_b32 v[4:5], v9 offset1:16
	ds_read_b32 v0, v0
	v_readlane_b32 s1, v254, 3
	v_ashrrev_i32_e32 v17, 31, v16
	ds_read2_b32 v[20:21], v9 offset0:160 offset1:176
	s_waitcnt lgkmcnt(0)
	v_ashrrev_i32_e32 v11, 31, v4
	v_mov_b32_e32 v10, v4
	v_lshl_add_u64 v[10:11], v[10:11], 2, s[14:15]
	global_load_dword v19, v[10:11], off
	ds_read2_b32 v[10:11], v9 offset0:32 offset1:48
	v_ashrrev_i32_e32 v13, 31, v5
	v_mov_b32_e32 v12, v5
	v_lshl_add_u64 v[4:5], v[12:13], 2, s[14:15]
	global_load_dword v24, v[4:5], off
	s_waitcnt lgkmcnt(0)
	v_ashrrev_i32_e32 v5, 31, v10
	v_mov_b32_e32 v4, v10
	v_lshl_add_u64 v[4:5], v[4:5], 2, s[14:15]
	global_load_dword v25, v[4:5], off
	ds_read2_b32 v[4:5], v9 offset0:128 offset1:144
	v_ashrrev_i32_e32 v13, 31, v11
	v_mov_b32_e32 v12, v11
	v_lshl_add_u64 v[10:11], v[12:13], 2, s[14:15]
	v_ashrrev_i32_e32 v1, 31, v0
	global_load_dword v26, v[10:11], off
	s_waitcnt lgkmcnt(0)
	v_ashrrev_i32_e32 v11, 31, v4
	v_mov_b32_e32 v10, v4
	v_lshlrev_b64 v[0:1], 14, v[0:1]
	v_lshl_add_u64 v[10:11], v[10:11], 2, s[14:15]
	v_lshl_add_u64 v[0:1], s[0:1], 0, v[0:1]
	global_load_dword v27, v[10:11], off
	v_ashrrev_i32_e32 v11, 31, v5
	v_mov_b32_e32 v10, v5
	v_lshl_add_u64 v[6:7], v[16:17], 2, v[0:1]
	v_lshl_add_u64 v[4:5], v[10:11], 2, s[14:15]
	global_load_dwordx4 v[0:3], v[6:7], off
	global_load_dword v28, v[4:5], off
	v_ashrrev_i32_e32 v5, 31, v20
	v_mov_b32_e32 v4, v20
	v_add_co_u32_e32 v8, vcc, s56, v6
	v_lshl_add_u64 v[4:5], v[4:5], 2, s[14:15]
	global_load_dword v29, v[4:5], off
	v_addc_co_u32_e32 v9, vcc, 0, v7, vcc
	global_load_dwordx4 v[8:11], v[8:9], off
	s_nop 0
	global_load_dwordx4 v[12:15], v[6:7], off offset:16
	v_readlane_b32 s5, v254, 7
	s_mov_b64 s[4:5], 0x2000
	v_ashrrev_i32_e32 v23, 31, v21
	v_lshl_add_u64 v[4:5], v[6:7], 0, s[4:5]
	global_load_dwordx4 v[4:7], v[4:5], off offset:16
	v_mov_b32_e32 v22, v21
	v_lshl_add_u64 v[20:21], v[22:23], 2, s[14:15]
	global_load_dword v20, v[20:21], off
	s_ashr_i32 s39, s38, 31
	s_lshl_b64 s[4:5], s[38:39], 19
	s_add_u32 s4, s93, s4
	s_addc_u32 s5, s87, s5
	s_bfe_u32 s0, s92, 0x30003
	s_cmp_lg_u32 s65, s0
	v_readlane_b32 s2, v254, 4
	v_readlane_b32 s3, v254, 5
	v_readlane_b32 s6, v254, 8
	v_readlane_b32 s7, v254, 9
	s_waitcnt vmcnt(0)
	v_mul_f32_e32 v19, 0x3b800000, v19
	v_mul_f32_e32 v30, 0x3b800000, v24
	v_mul_f32_e32 v25, 0x3b800000, v25
	v_mul_f32_e32 v24, 0x3b800000, v26
	v_mul_f32_e32 v23, 0x3b800000, v27
	v_fma_f32 v26, v192, v19, v0
	v_mul_f32_e32 v22, 0x3b800000, v28
	v_fma_f32 v28, v193, v19, v1
	v_min_f32_e32 v26, 0x40e00000, v26
	v_min_f32_e32 v28, 0x40e00000, v28
	v_fma_f32 v31, v194, v19, v2
	v_mul_f32_e32 v34, 0xc01d265f, v26
	v_mul_f32_e32 v35, 0xc01d265f, v28
	v_min_f32_e32 v31, 0x40e00000, v31
	v_exp_f32_e32 v34, v34
	v_exp_f32_e32 v35, v35
	v_mul_f32_e32 v36, 0xc01d265f, v31
	v_fma_f32 v33, v195, v19, v3
	v_exp_f32_e32 v36, v36
	v_min_f32_e32 v33, 0x40e00000, v33
	v_mul_f32_e32 v37, 0xc01d265f, v33
	v_add_f32_e32 v34, 1.0, v34
	v_add_f32_e32 v35, 1.0, v35
	v_exp_f32_e32 v37, v37
	v_rcp_f32_e32 v34, v34
	v_rcp_f32_e32 v35, v35
	v_add_f32_e32 v36, 1.0, v36
	v_mul_f32_e32 v21, 0x3b800000, v29
	v_fma_f32 v27, v188, v19, v8
	v_fma_f32 v29, v189, v19, v9
	v_rcp_f32_e32 v36, v36
	v_med3_f32 v27, v27, s23, v236
	v_med3_f32 v29, v29, s23, v236
	v_fma_f32 v32, v190, v19, v10
	v_add_f32_e32 v27, 1.0, v27
	v_add_f32_e32 v29, 1.0, v29
	v_add_f32_e32 v37, 1.0, v37
	v_mul_f32_e32 v26, v26, v34
	v_mul_f32_e32 v28, v28, v35
	v_med3_f32 v32, v32, s23, v236
	v_mul_f32_e32 v26, v27, v26
	v_mul_f32_e32 v27, v29, v28
	v_rcp_f32_e32 v28, v37
	v_add_f32_e32 v32, 1.0, v32
	v_mul_f32_e32 v31, v31, v36
	v_mul_f32_e32 v29, v32, v31
	v_fma_f32 v32, v184, v19, v12
	v_min_f32_e32 v32, 0x40e00000, v32
	v_mul_f32_e32 v28, v33, v28
	v_mul_f32_e32 v33, 0xc01d265f, v32
	v_exp_f32_e32 v33, v33
	v_fma_f32 v34, v185, v19, v13
	v_min_f32_e32 v34, 0x40e00000, v34
	v_mul_f32_e32 v35, 0xc01d265f, v34
	v_add_f32_e32 v33, 1.0, v33
	v_rcp_f32_e32 v33, v33
	v_exp_f32_e32 v35, v35
	v_fma_f32 v31, v191, v19, v11
	v_fma_f32 v36, v187, v19, v15
	v_mul_f32_e32 v32, v32, v33
	v_add_f32_e32 v33, 1.0, v35
	v_rcp_f32_e32 v33, v33
	v_med3_f32 v31, v31, s23, v236
	v_min_f32_e32 v36, 0x40e00000, v36
	v_add_f32_e32 v31, 1.0, v31
	v_mul_f32_e32 v33, v34, v33
	v_fma_f32 v34, v186, v19, v14
	v_min_f32_e32 v34, 0x40e00000, v34
	v_mul_f32_e32 v35, 0xc01d265f, v34
	v_exp_f32_e32 v35, v35
	v_mul_f32_e32 v37, 0xc01d265f, v36
	v_mul_f32_e32 v28, v31, v28
	v_fma_f32 v31, v180, v19, v4
	v_add_f32_e32 v35, 1.0, v35
	v_rcp_f32_e32 v35, v35
	v_exp_f32_e32 v37, v37
	v_med3_f32 v31, v31, s23, v236
	v_add_f32_e32 v31, 1.0, v31
	v_mul_f32_e32 v31, v31, v32
	v_fma_f32 v32, v181, v19, v5
	v_med3_f32 v32, v32, s23, v236
	v_mul_f32_e32 v34, v34, v35
	v_add_f32_e32 v35, 1.0, v37
	v_add_f32_e32 v32, 1.0, v32
	v_rcp_f32_e32 v35, v35
	v_mul_f32_e32 v32, v32, v33
	v_fma_f32 v33, v182, v19, v6
	v_med3_f32 v33, v33, s23, v236
	v_fma_f32 v19, v183, v19, v7
	v_add_f32_e32 v33, 1.0, v33
	v_med3_f32 v19, v19, s23, v236
	v_mul_f32_e32 v33, v33, v34
	v_mul_f32_e32 v34, v36, v35
	v_add_f32_e32 v19, 1.0, v19
	v_mul_f32_e32 v19, v19, v34
	v_med3_f32 v34, v26, s24, v237
	v_med3_f32 v27, v27, s24, v237
	v_mov_b32_e32 v26, v65
	v_cvt_pk_fp8_f32 v26, v34, v27
	v_med3_f32 v31, v31, s24, v237
	v_med3_f32 v32, v32, s24, v237
;     __device__ __forceinline__ void operator()(const f32x4 (&acc)[2][2][4][2], const Unit& u, int wr, int wc, int fr, int fq) const {
;     ...
; #pragma unroll
;         for (int ai = 0; ai < 2; ++ai)
; #pragma unroll
;             for (int m = 0; m < 4; ++m) { const int r = row0 + ai * 128 + m * 16; const float rs = rsb[ai * 4 + m];
;                 float a[8];
; #pragma unroll
;                 for (int j = 0; j < 8; ++j) { const float gb = j < 4 ? g0[j & 3] : g1[j & 3], lb = j < 4 ? l0[j & 3] : l1[j & 3];
;                     const float gl = fminf(acc[ai][0][m][j >> 2][j & 3] * rs + gb, 7.0f), ln = fminf(fmaxf(acc[ai][1][m][j >> 2][j & 3] * rs + lb, -7.0f), 7.0f);
;                     a[j] = gl * __builtin_amdgcn_rcpf(1.0f + __builtin_amdgcn_exp2f(-1.702f * 1.4426950408889634f * gl)) * (ln + 1.0f); }
;                 v2u w; w.x = pk4_fp8(a[0], a[1], a[2], a[3]); w.y = pk4_fp8(a[4], a[5], a[6], a[7]);
;                 *(v2u*)(ACT + ((size_t)u.z * 256 + r) * FF + c0) = w; }
	v_mov_b32_e32 v27, v65
	v_cvt_pk_fp8_f32 v27, v31, v32
	v_med3_f32 v29, v29, s24, v237
	v_med3_f32 v28, v28, s24, v237
	v_cvt_pk_fp8_f32 v26, v29, v28 op_sel:[0,0,1]
	v_med3_f32 v28, v33, s24, v237
	v_med3_f32 v19, v19, s24, v237
	v_cvt_pk_fp8_f32 v27, v28, v19 op_sel:[0,0,1]
	v_ashrrev_i32_e32 v19, 31, v18
	v_lshlrev_b64 v[18:19], 11, v[18:19]
	v_lshl_add_u64 v[18:19], s[4:5], 0, v[18:19]
	v_lshl_add_u64 v[16:17], v[18:19], 0, v[16:17]
	global_store_dwordx2 v[16:17], v[26:27], off
	v_fma_f32 v26, v177, v30, v1
	v_min_f32_e32 v26, 0x40e00000, v26
	v_fma_f32 v28, v176, v30, v0
	v_mul_f32_e32 v27, 0xc01d265f, v26
	v_min_f32_e32 v28, 0x40e00000, v28
	v_exp_f32_e32 v27, v27
	v_mul_f32_e32 v29, 0xc01d265f, v28
	v_exp_f32_e32 v29, v29
	v_fma_f32 v32, v169, v30, v13
	v_add_f32_e32 v27, 1.0, v27
	v_rcp_f32_e32 v27, v27
	v_add_f32_e32 v19, 1.0, v29
	v_rcp_f32_e32 v19, v19
	v_fma_f32 v29, v179, v30, v3
	v_mul_f32_e32 v26, v26, v27
	v_fma_f32 v27, v178, v30, v2
	v_min_f32_e32 v27, 0x40e00000, v27
	v_mul_f32_e32 v19, v28, v19
	v_mul_f32_e32 v28, 0xc01d265f, v27
	v_exp_f32_e32 v28, v28
	v_min_f32_e32 v29, 0x40e00000, v29
	v_mul_f32_e32 v31, 0xc01d265f, v29
	v_exp_f32_e32 v31, v31
	v_add_f32_e32 v28, 1.0, v28
	v_rcp_f32_e32 v28, v28
	v_min_f32_e32 v32, 0x40e00000, v32
	v_mul_f32_e32 v33, 0xc01d265f, v32
	v_exp_f32_e32 v33, v33
	v_mul_f32_e32 v27, v27, v28
	v_add_f32_e32 v28, 1.0, v31
	v_rcp_f32_e32 v28, v28
	v_fma_f32 v18, v172, v30, v8
	v_med3_f32 v18, v18, s23, v236
	v_add_f32_e32 v18, 1.0, v18
	v_mul_f32_e32 v28, v29, v28
	v_fma_f32 v29, v168, v30, v12
	v_min_f32_e32 v29, 0x40e00000, v29
	v_mul_f32_e32 v31, 0xc01d265f, v29
	v_exp_f32_e32 v31, v31
	v_mul_f32_e32 v18, v18, v19
	v_fma_f32 v19, v173, v30, v9
	v_med3_f32 v19, v19, s23, v236
	v_add_f32_e32 v31, 1.0, v31
	v_rcp_f32_e32 v31, v31
	v_add_f32_e32 v19, 1.0, v19
	v_mul_f32_e32 v19, v19, v26
	v_fma_f32 v26, v174, v30, v10
	v_mul_f32_e32 v29, v29, v31
	v_add_f32_e32 v31, 1.0, v33
	v_rcp_f32_e32 v31, v31
	v_med3_f32 v26, v26, s23, v236
	v_add_f32_e32 v26, 1.0, v26
	v_mul_f32_e32 v26, v26, v27
	v_mul_f32_e32 v31, v32, v31
	v_fma_f32 v32, v170, v30, v14
	v_min_f32_e32 v32, 0x40e00000, v32
	v_mul_f32_e32 v33, 0xc01d265f, v32
	v_exp_f32_e32 v33, v33
	v_fma_f32 v27, v175, v30, v11
	v_fma_f32 v34, v171, v30, v15
	v_med3_f32 v27, v27, s23, v236
	v_min_f32_e32 v34, 0x40e00000, v34
	v_add_f32_e32 v27, 1.0, v27
	v_add_f32_e32 v33, 1.0, v33
	v_mul_f32_e32 v35, 0xc01d265f, v34
	v_mul_f32_e32 v27, v27, v28
	v_fma_f32 v28, v164, v30, v4
	v_rcp_f32_e32 v33, v33
	v_exp_f32_e32 v35, v35
	v_med3_f32 v28, v28, s23, v236
	v_add_f32_e32 v28, 1.0, v28
	v_mul_f32_e32 v28, v28, v29
	v_fma_f32 v29, v165, v30, v5
	v_med3_f32 v29, v29, s23, v236
	v_mul_f32_e32 v32, v32, v33
	v_add_f32_e32 v33, 1.0, v35
	v_add_f32_e32 v29, 1.0, v29
	v_rcp_f32_e32 v33, v33
	v_mul_f32_e32 v29, v29, v31
	v_fma_f32 v31, v166, v30, v6
	v_med3_f32 v31, v31, s23, v236
	v_fma_f32 v30, v167, v30, v7
	v_add_f32_e32 v31, 1.0, v31
	v_med3_f32 v30, v30, s23, v236
	v_mul_f32_e32 v31, v31, v32
	v_mul_f32_e32 v32, v34, v33
	v_add_f32_e32 v30, 1.0, v30
	v_mul_f32_e32 v30, v30, v32
	v_med3_f32 v32, v18, s24, v237
	v_med3_f32 v19, v19, s24, v237
	v_mov_b32_e32 v18, v65
	v_cvt_pk_fp8_f32 v18, v32, v19
	v_med3_f32 v28, v28, s24, v237
	v_med3_f32 v29, v29, s24, v237
	v_mov_b32_e32 v19, v65
	v_cvt_pk_fp8_f32 v19, v28, v29
	v_med3_f32 v26, v26, s24, v237
	v_med3_f32 v27, v27, s24, v237
	v_cvt_pk_fp8_f32 v18, v26, v27 op_sel:[0,0,1]
	v_med3_f32 v26, v31, s24, v237
	v_med3_f32 v27, v30, s24, v237
	v_cvt_pk_fp8_f32 v19, v26, v27 op_sel:[0,0,1]
	v_fma_f32 v27, v160, v25, v0
	v_min_f32_e32 v28, 0x40e00000, v27
	v_add_co_u32_e32 v26, vcc, s73, v16
	v_mul_f32_e32 v27, 0xc01d265f, v28
	v_exp_f32_e32 v29, v27
	v_addc_co_u32_e32 v27, vcc, 0, v17, vcc
	global_store_dwordx2 v[26:27], v[18:19], off
	v_fma_f32 v26, v161, v25, v1
	v_min_f32_e32 v26, 0x40e00000, v26
	v_mul_f32_e32 v27, 0xc01d265f, v26
	v_exp_f32_e32 v27, v27
	v_add_f32_e32 v19, 1.0, v29
	v_rcp_f32_e32 v19, v19
	v_fma_f32 v29, v163, v25, v3
	v_add_f32_e32 v27, 1.0, v27
	v_rcp_f32_e32 v27, v27
	v_mul_f32_e32 v19, v28, v19
	v_min_f32_e32 v29, 0x40e00000, v29
	v_mul_f32_e32 v30, 0xc01d265f, v29
	v_mul_f32_e32 v26, v26, v27
	v_fma_f32 v27, v162, v25, v2
	v_min_f32_e32 v27, 0x40e00000, v27
	v_mul_f32_e32 v28, 0xc01d265f, v27
	v_exp_f32_e32 v28, v28
	v_exp_f32_e32 v30, v30
	v_fma_f32 v31, v153, v25, v13
	v_min_f32_e32 v31, 0x40e00000, v31
	v_add_f32_e32 v28, 1.0, v28
	v_rcp_f32_e32 v28, v28
	v_mul_f32_e32 v32, 0xc01d265f, v31
	v_exp_f32_e32 v32, v32
	v_fma_f32 v18, v156, v25, v8
	v_mul_f32_e32 v27, v27, v28
	v_add_f32_e32 v28, 1.0, v30
	v_rcp_f32_e32 v28, v28
	v_med3_f32 v18, v18, s23, v236
	v_add_f32_e32 v18, 1.0, v18
	v_mul_f32_e32 v18, v18, v19
	v_mul_f32_e32 v28, v29, v28
	v_fma_f32 v29, v152, v25, v12
	v_min_f32_e32 v29, 0x40e00000, v29
	v_mul_f32_e32 v30, 0xc01d265f, v29
	v_exp_f32_e32 v30, v30
	v_fma_f32 v19, v157, v25, v9
	v_med3_f32 v19, v19, s23, v236
	v_add_f32_e32 v19, 1.0, v19
	v_add_f32_e32 v30, 1.0, v30
	v_rcp_f32_e32 v30, v30
	v_mul_f32_e32 v19, v19, v26
	v_fma_f32 v26, v158, v25, v10
	v_med3_f32 v26, v26, s23, v236
	v_mul_f32_e32 v29, v29, v30
	v_add_f32_e32 v30, 1.0, v32
	v_rcp_f32_e32 v30, v30
	v_add_f32_e32 v26, 1.0, v26
	v_mul_f32_e32 v26, v26, v27
	v_fma_f32 v27, v159, v25, v11
	v_mul_f32_e32 v30, v31, v30
	v_fma_f32 v31, v154, v25, v14
	v_min_f32_e32 v31, 0x40e00000, v31
	v_mul_f32_e32 v32, 0xc01d265f, v31
	v_exp_f32_e32 v32, v32
	v_fma_f32 v33, v155, v25, v15
	v_med3_f32 v27, v27, s23, v236
	v_min_f32_e32 v33, 0x40e00000, v33
	v_add_f32_e32 v27, 1.0, v27
	v_add_f32_e32 v32, 1.0, v32
;     __device__ __forceinline__ void operator()(const f32x4 (&acc)[2][2][4][2], const Unit& u, int wr, int wc, int fr, int fq) const {
;     ...
; #pragma unroll
;         for (int ai = 0; ai < 2; ++ai)
; #pragma unroll
;             for (int m = 0; m < 4; ++m) { const int r = row0 + ai * 128 + m * 16; const float rs = rsb[ai * 4 + m];
;                 float a[8];
; #pragma unroll
;                 for (int j = 0; j < 8; ++j) { const float gb = j < 4 ? g0[j & 3] : g1[j & 3], lb = j < 4 ? l0[j & 3] : l1[j & 3];
;                     const float gl = fminf(acc[ai][0][m][j >> 2][j & 3] * rs + gb, 7.0f), ln = fminf(fmaxf(acc[ai][1][m][j >> 2][j & 3] * rs + lb, -7.0f), 7.0f);
;                     a[j] = gl * __builtin_amdgcn_rcpf(1.0f + __builtin_amdgcn_exp2f(-1.702f * 1.4426950408889634f * gl)) * (ln + 1.0f); }
;                 v2u w; w.x = pk4_fp8(a[0], a[1], a[2], a[3]); w.y = pk4_fp8(a[4], a[5], a[6], a[7]);
;                 *(v2u*)(ACT + ((size_t)u.z * 256 + r) * FF + c0) = w; }
	v_mul_f32_e32 v34, 0xc01d265f, v33
	v_mul_f32_e32 v27, v27, v28
	v_fma_f32 v28, v148, v25, v4
	v_rcp_f32_e32 v32, v32
	v_exp_f32_e32 v34, v34
	v_med3_f32 v28, v28, s23, v236
	v_add_f32_e32 v28, 1.0, v28
	v_mul_f32_e32 v28, v28, v29
	v_fma_f32 v29, v149, v25, v5
	v_med3_f32 v29, v29, s23, v236
	v_mul_f32_e32 v31, v31, v32
	v_add_f32_e32 v32, 1.0, v34
	v_add_f32_e32 v29, 1.0, v29
	v_rcp_f32_e32 v32, v32
	v_mul_f32_e32 v29, v29, v30
	v_fma_f32 v30, v150, v25, v6
	v_med3_f32 v30, v30, s23, v236
	v_fma_f32 v25, v151, v25, v7
	v_add_f32_e32 v30, 1.0, v30
	v_med3_f32 v25, v25, s23, v236
	v_mul_f32_e32 v30, v30, v31
	v_mul_f32_e32 v31, v33, v32
	v_add_f32_e32 v25, 1.0, v25
	v_mul_f32_e32 v25, v25, v31
	v_med3_f32 v31, v18, s24, v237
	v_med3_f32 v19, v19, s24, v237
	v_mov_b32_e32 v18, v65
	v_cvt_pk_fp8_f32 v18, v31, v19
	v_med3_f32 v28, v28, s24, v237
	v_med3_f32 v29, v29, s24, v237
	v_mov_b32_e32 v19, v65
	v_cvt_pk_fp8_f32 v19, v28, v29
	v_med3_f32 v26, v26, s24, v237
	v_med3_f32 v27, v27, s24, v237
	v_cvt_pk_fp8_f32 v18, v26, v27 op_sel:[0,0,1]
	v_med3_f32 v26, v30, s24, v237
	v_med3_f32 v25, v25, s24, v237
	v_cvt_pk_fp8_f32 v19, v26, v25 op_sel:[0,0,1]
	v_fma_f32 v25, v144, v24, v0
	v_min_f32_e32 v25, 0x40e00000, v25
	v_mul_f32_e32 v27, 0xc01d265f, v25
	v_add_co_u32_e32 v26, vcc, s57, v16
	v_exp_f32_e32 v28, v27
	s_nop 0
	v_addc_co_u32_e32 v27, vcc, 0, v17, vcc
	global_store_dwordx2 v[26:27], v[18:19], off
	v_fma_f32 v26, v145, v24, v1
	v_min_f32_e32 v26, 0x40e00000, v26
	v_add_f32_e32 v19, 1.0, v28
	v_mul_f32_e32 v27, 0xc01d265f, v26
	v_rcp_f32_e32 v19, v19
	v_exp_f32_e32 v27, v27
	v_fma_f32 v28, v147, v24, v3
	v_min_f32_e32 v28, 0x40e00000, v28
	v_mul_f32_e32 v19, v25, v19
	v_add_f32_e32 v25, 1.0, v27
	v_rcp_f32_e32 v25, v25
	v_mul_f32_e32 v29, 0xc01d265f, v28
	v_exp_f32_e32 v29, v29
	v_fma_f32 v30, v137, v24, v13
	v_mul_f32_e32 v25, v26, v25
	v_fma_f32 v26, v146, v24, v2
	v_min_f32_e32 v26, 0x40e00000, v26
	v_mul_f32_e32 v27, 0xc01d265f, v26
	v_exp_f32_e32 v27, v27
	v_min_f32_e32 v30, 0x40e00000, v30
	v_mul_f32_e32 v31, 0xc01d265f, v30
	v_exp_f32_e32 v31, v31
	v_add_f32_e32 v27, 1.0, v27
	v_rcp_f32_e32 v27, v27
	v_fma_f32 v18, v140, v24, v8
	v_med3_f32 v18, v18, s23, v236
	v_add_f32_e32 v18, 1.0, v18
	v_mul_f32_e32 v26, v26, v27
	v_add_f32_e32 v27, 1.0, v29
	v_rcp_f32_e32 v27, v27
	v_mul_f32_e32 v18, v18, v19
	v_fma_f32 v19, v141, v24, v9
	v_med3_f32 v19, v19, s23, v236
	v_mul_f32_e32 v27, v28, v27
	v_fma_f32 v28, v136, v24, v12
	v_min_f32_e32 v28, 0x40e00000, v28
	v_mul_f32_e32 v29, 0xc01d265f, v28
	v_exp_f32_e32 v29, v29
	v_add_f32_e32 v19, 1.0, v19
	v_mul_f32_e32 v19, v19, v25
	v_fma_f32 v25, v142, v24, v10
	v_add_f32_e32 v29, 1.0, v29
	v_rcp_f32_e32 v29, v29
	v_med3_f32 v25, v25, s23, v236
	v_add_f32_e32 v25, 1.0, v25
	v_mul_f32_e32 v25, v25, v26
	v_mul_f32_e32 v28, v28, v29
	v_add_f32_e32 v29, 1.0, v31
	v_rcp_f32_e32 v29, v29
	v_fma_f32 v26, v143, v24, v11
	v_fma_f32 v32, v139, v24, v15
	v_med3_f32 v26, v26, s23, v236
	v_mul_f32_e32 v29, v30, v29
	v_fma_f32 v30, v138, v24, v14
	v_min_f32_e32 v30, 0x40e00000, v30
	v_mul_f32_e32 v31, 0xc01d265f, v30
	v_exp_f32_e32 v31, v31
	v_min_f32_e32 v32, 0x40e00000, v32
	v_add_f32_e32 v26, 1.0, v26
	v_mul_f32_e32 v33, 0xc01d265f, v32
	v_add_f32_e32 v31, 1.0, v31
	v_mul_f32_e32 v26, v26, v27
	v_fma_f32 v27, v132, v24, v4
	v_rcp_f32_e32 v31, v31
	v_exp_f32_e32 v33, v33
	v_med3_f32 v27, v27, s23, v236
	v_add_f32_e32 v27, 1.0, v27
	v_mul_f32_e32 v27, v27, v28
	v_fma_f32 v28, v133, v24, v5
	v_med3_f32 v28, v28, s23, v236
	v_mul_f32_e32 v30, v30, v31
	v_add_f32_e32 v31, 1.0, v33
	v_add_f32_e32 v28, 1.0, v28
	v_rcp_f32_e32 v31, v31
	v_mul_f32_e32 v28, v28, v29
	v_fma_f32 v29, v134, v24, v6
	v_med3_f32 v29, v29, s23, v236
	v_fma_f32 v24, v135, v24, v7
	v_add_f32_e32 v29, 1.0, v29
	v_med3_f32 v24, v24, s23, v236
	v_mul_f32_e32 v29, v29, v30
	v_mul_f32_e32 v30, v32, v31
	v_add_f32_e32 v24, 1.0, v24
	v_mul_f32_e32 v24, v24, v30
	v_med3_f32 v30, v18, s24, v237
	v_med3_f32 v19, v19, s24, v237
	v_mov_b32_e32 v18, v65
	v_cvt_pk_fp8_f32 v18, v30, v19
	v_med3_f32 v27, v27, s24, v237
	v_med3_f32 v28, v28, s24, v237
	v_mov_b32_e32 v19, v65
	v_cvt_pk_fp8_f32 v19, v27, v28
	v_med3_f32 v25, v25, s24, v237
	v_med3_f32 v26, v26, s24, v237
	v_cvt_pk_fp8_f32 v18, v25, v26 op_sel:[0,0,1]
	v_med3_f32 v25, v29, s24, v237
	v_med3_f32 v24, v24, s24, v237
	v_cvt_pk_fp8_f32 v19, v25, v24 op_sel:[0,0,1]
	v_fma_f32 v25, v128, v23, v0
	v_min_f32_e32 v26, 0x40e00000, v25
	v_add_co_u32_e32 v24, vcc, s69, v16
	v_mul_f32_e32 v25, 0xc01d265f, v26
	v_exp_f32_e32 v27, v25
	v_addc_co_u32_e32 v25, vcc, 0, v17, vcc
	global_store_dwordx2 v[24:25], v[18:19], off
	v_fma_f32 v24, v129, v23, v1
	v_min_f32_e32 v24, 0x40e00000, v24
	v_mul_f32_e32 v25, 0xc01d265f, v24
	v_exp_f32_e32 v25, v25
	v_add_f32_e32 v19, 1.0, v27
	v_rcp_f32_e32 v19, v19
	v_fma_f32 v27, v131, v23, v3
	v_add_f32_e32 v25, 1.0, v25
	v_rcp_f32_e32 v25, v25
	v_mul_f32_e32 v19, v26, v19
	v_min_f32_e32 v27, 0x40e00000, v27
	v_mul_f32_e32 v28, 0xc01d265f, v27
	v_mul_f32_e32 v24, v24, v25
	v_fma_f32 v25, v130, v23, v2
	v_min_f32_e32 v25, 0x40e00000, v25
	v_mul_f32_e32 v26, 0xc01d265f, v25
	v_exp_f32_e32 v26, v26
	v_exp_f32_e32 v28, v28
	v_fma_f32 v29, v121, v23, v13
	v_min_f32_e32 v29, 0x40e00000, v29
	v_add_f32_e32 v26, 1.0, v26
	v_rcp_f32_e32 v26, v26
	v_mul_f32_e32 v30, 0xc01d265f, v29
	v_exp_f32_e32 v30, v30
	v_fma_f32 v18, v124, v23, v8
	v_mul_f32_e32 v25, v25, v26
	v_add_f32_e32 v26, 1.0, v28
	v_rcp_f32_e32 v26, v26
	v_med3_f32 v18, v18, s23, v236
	v_add_f32_e32 v18, 1.0, v18
	v_mul_f32_e32 v18, v18, v19
	v_mul_f32_e32 v26, v27, v26
	v_fma_f32 v27, v120, v23, v12
;     __device__ __forceinline__ void operator()(const f32x4 (&acc)[2][2][4][2], const Unit& u, int wr, int wc, int fr, int fq) const {
;     ...
; #pragma unroll
;         for (int ai = 0; ai < 2; ++ai)
; #pragma unroll
;             for (int m = 0; m < 4; ++m) { const int r = row0 + ai * 128 + m * 16; const float rs = rsb[ai * 4 + m];
;                 float a[8];
; #pragma unroll
;                 for (int j = 0; j < 8; ++j) { const float gb = j < 4 ? g0[j & 3] : g1[j & 3], lb = j < 4 ? l0[j & 3] : l1[j & 3];
;                     const float gl = fminf(acc[ai][0][m][j >> 2][j & 3] * rs + gb, 7.0f), ln = fminf(fmaxf(acc[ai][1][m][j >> 2][j & 3] * rs + lb, -7.0f), 7.0f);
;                     a[j] = gl * __builtin_amdgcn_rcpf(1.0f + __builtin_amdgcn_exp2f(-1.702f * 1.4426950408889634f * gl)) * (ln + 1.0f); }
;                 v2u w; w.x = pk4_fp8(a[0], a[1], a[2], a[3]); w.y = pk4_fp8(a[4], a[5], a[6], a[7]);
;                 *(v2u*)(ACT + ((size_t)u.z * 256 + r) * FF + c0) = w; }
	v_min_f32_e32 v27, 0x40e00000, v27
	v_mul_f32_e32 v28, 0xc01d265f, v27
	v_exp_f32_e32 v28, v28
	v_fma_f32 v19, v125, v23, v9
	v_med3_f32 v19, v19, s23, v236
	v_add_f32_e32 v19, 1.0, v19
	v_add_f32_e32 v28, 1.0, v28
	v_rcp_f32_e32 v28, v28
	v_mul_f32_e32 v19, v19, v24
	v_fma_f32 v24, v126, v23, v10
	v_med3_f32 v24, v24, s23, v236
	v_mul_f32_e32 v27, v27, v28
	v_add_f32_e32 v28, 1.0, v30
	v_rcp_f32_e32 v28, v28
	v_add_f32_e32 v24, 1.0, v24
	v_mul_f32_e32 v24, v24, v25
	v_fma_f32 v25, v127, v23, v11
	v_mul_f32_e32 v28, v29, v28
	v_fma_f32 v29, v122, v23, v14
	v_min_f32_e32 v29, 0x40e00000, v29
	v_mul_f32_e32 v30, 0xc01d265f, v29
	v_exp_f32_e32 v30, v30
	v_fma_f32 v31, v123, v23, v15
	v_med3_f32 v25, v25, s23, v236
	v_min_f32_e32 v31, 0x40e00000, v31
	v_add_f32_e32 v25, 1.0, v25
	v_add_f32_e32 v30, 1.0, v30
	v_mul_f32_e32 v32, 0xc01d265f, v31
	v_mul_f32_e32 v25, v25, v26
	v_fma_f32 v26, v116, v23, v4
	v_rcp_f32_e32 v30, v30
	v_exp_f32_e32 v32, v32
	v_med3_f32 v26, v26, s23, v236
	v_add_f32_e32 v26, 1.0, v26
	v_mul_f32_e32 v26, v26, v27
	v_fma_f32 v27, v117, v23, v5
	v_med3_f32 v27, v27, s23, v236
	v_mul_f32_e32 v29, v29, v30
	v_add_f32_e32 v30, 1.0, v32
	v_add_f32_e32 v27, 1.0, v27
	v_rcp_f32_e32 v30, v30
	v_mul_f32_e32 v27, v27, v28
	v_fma_f32 v28, v118, v23, v6
	v_med3_f32 v28, v28, s23, v236
	v_fma_f32 v23, v119, v23, v7
	v_add_f32_e32 v28, 1.0, v28
	v_med3_f32 v23, v23, s23, v236
	v_mul_f32_e32 v28, v28, v29
	v_mul_f32_e32 v29, v31, v30
	v_add_f32_e32 v23, 1.0, v23
	v_mul_f32_e32 v23, v23, v29
	v_med3_f32 v29, v18, s24, v237
	v_med3_f32 v19, v19, s24, v237
	v_mov_b32_e32 v18, v65
	v_cvt_pk_fp8_f32 v18, v29, v19
	v_med3_f32 v26, v26, s24, v237
	v_med3_f32 v27, v27, s24, v237
	v_mov_b32_e32 v19, v65
	v_cvt_pk_fp8_f32 v19, v26, v27
	v_med3_f32 v24, v24, s24, v237
	v_med3_f32 v25, v25, s24, v237
	v_cvt_pk_fp8_f32 v18, v24, v25 op_sel:[0,0,1]
	v_med3_f32 v24, v28, s24, v237
	v_med3_f32 v23, v23, s24, v237
	v_cvt_pk_fp8_f32 v19, v24, v23 op_sel:[0,0,1]
	v_fma_f32 v23, v112, v22, v0
	v_min_f32_e32 v23, 0x40e00000, v23
	s_mov_b32 s4, 0x40000
	v_mul_f32_e32 v25, 0xc01d265f, v23
	v_add_co_u32_e32 v24, vcc, s4, v16
	v_exp_f32_e32 v26, v25
	s_nop 0
	v_addc_co_u32_e32 v25, vcc, 0, v17, vcc
	global_store_dwordx2 v[24:25], v[18:19], off
	v_fma_f32 v24, v113, v22, v1
	v_min_f32_e32 v24, 0x40e00000, v24
	v_add_f32_e32 v19, 1.0, v26
	v_mul_f32_e32 v25, 0xc01d265f, v24
	v_rcp_f32_e32 v19, v19
	v_exp_f32_e32 v25, v25
	v_fma_f32 v26, v115, v22, v3
	v_min_f32_e32 v26, 0x40e00000, v26
	v_mul_f32_e32 v19, v23, v19
	v_add_f32_e32 v23, 1.0, v25
	v_rcp_f32_e32 v23, v23
	v_mul_f32_e32 v27, 0xc01d265f, v26
	v_exp_f32_e32 v27, v27
	v_fma_f32 v28, v105, v22, v13
	v_mul_f32_e32 v23, v24, v23
	v_fma_f32 v24, v114, v22, v2
	v_min_f32_e32 v24, 0x40e00000, v24
	v_mul_f32_e32 v25, 0xc01d265f, v24
	v_exp_f32_e32 v25, v25
	v_min_f32_e32 v28, 0x40e00000, v28
	v_mul_f32_e32 v29, 0xc01d265f, v28
	v_exp_f32_e32 v29, v29
	v_add_f32_e32 v25, 1.0, v25
	v_rcp_f32_e32 v25, v25
	v_fma_f32 v18, v108, v22, v8
	v_med3_f32 v18, v18, s23, v236
	v_add_f32_e32 v18, 1.0, v18
	v_mul_f32_e32 v24, v24, v25
	v_add_f32_e32 v25, 1.0, v27
	v_rcp_f32_e32 v25, v25
	v_mul_f32_e32 v18, v18, v19
	v_fma_f32 v19, v109, v22, v9
	v_med3_f32 v19, v19, s23, v236
	v_mul_f32_e32 v25, v26, v25
	v_fma_f32 v26, v104, v22, v12
	v_min_f32_e32 v26, 0x40e00000, v26
	v_mul_f32_e32 v27, 0xc01d265f, v26
	v_exp_f32_e32 v27, v27
	v_add_f32_e32 v19, 1.0, v19
	v_mul_f32_e32 v19, v19, v23
	v_fma_f32 v23, v110, v22, v10
	v_add_f32_e32 v27, 1.0, v27
	v_rcp_f32_e32 v27, v27
	v_med3_f32 v23, v23, s23, v236
	v_add_f32_e32 v23, 1.0, v23
	v_mul_f32_e32 v23, v23, v24
	v_mul_f32_e32 v26, v26, v27
	v_add_f32_e32 v27, 1.0, v29
	v_rcp_f32_e32 v27, v27
	v_fma_f32 v24, v111, v22, v11
	v_fma_f32 v30, v107, v22, v15
	v_med3_f32 v24, v24, s23, v236
	v_mul_f32_e32 v27, v28, v27
	v_fma_f32 v28, v106, v22, v14
	v_min_f32_e32 v28, 0x40e00000, v28
	v_mul_f32_e32 v29, 0xc01d265f, v28
	v_exp_f32_e32 v29, v29
	v_min_f32_e32 v30, 0x40e00000, v30
	v_add_f32_e32 v24, 1.0, v24
	v_mul_f32_e32 v31, 0xc01d265f, v30
	v_add_f32_e32 v29, 1.0, v29
	v_mul_f32_e32 v24, v24, v25
	v_fma_f32 v25, v100, v22, v4
	v_rcp_f32_e32 v29, v29
	v_exp_f32_e32 v31, v31
	v_med3_f32 v25, v25, s23, v236
	v_add_f32_e32 v25, 1.0, v25
	v_mul_f32_e32 v25, v25, v26
	v_fma_f32 v26, v101, v22, v5
	v_med3_f32 v26, v26, s23, v236
	v_mul_f32_e32 v28, v28, v29
	v_add_f32_e32 v29, 1.0, v31
	v_add_f32_e32 v26, 1.0, v26
	v_rcp_f32_e32 v29, v29
	v_mul_f32_e32 v26, v26, v27
	v_fma_f32 v27, v102, v22, v6
	v_med3_f32 v27, v27, s23, v236
	v_fma_f32 v22, v103, v22, v7
	v_add_f32_e32 v27, 1.0, v27
	v_med3_f32 v22, v22, s23, v236
	v_mul_f32_e32 v27, v27, v28
	v_mul_f32_e32 v28, v30, v29
	v_add_f32_e32 v22, 1.0, v22
	v_mul_f32_e32 v22, v22, v28
	v_med3_f32 v28, v18, s24, v237
	v_med3_f32 v19, v19, s24, v237
	v_mov_b32_e32 v18, v65
	v_cvt_pk_fp8_f32 v18, v28, v19
	v_med3_f32 v25, v25, s24, v237
	v_med3_f32 v26, v26, s24, v237
	v_mov_b32_e32 v19, v65
	v_cvt_pk_fp8_f32 v19, v25, v26
	v_med3_f32 v23, v23, s24, v237
	v_med3_f32 v24, v24, s24, v237
	v_cvt_pk_fp8_f32 v18, v23, v24 op_sel:[0,0,1]
	v_med3_f32 v23, v27, s24, v237
	v_med3_f32 v22, v22, s24, v237
	v_cvt_pk_fp8_f32 v19, v23, v22 op_sel:[0,0,1]
	v_fma_f32 v23, v96, v21, v0
	s_mov_b32 s4, 0x48000
	v_min_f32_e32 v24, 0x40e00000, v23
	v_add_co_u32_e32 v22, vcc, s4, v16
	v_mul_f32_e32 v23, 0xc01d265f, v24
	v_exp_f32_e32 v25, v23
	v_addc_co_u32_e32 v23, vcc, 0, v17, vcc
	global_store_dwordx2 v[22:23], v[18:19], off
	v_fma_f32 v22, v97, v21, v1
	v_min_f32_e32 v22, 0x40e00000, v22
	v_mul_f32_e32 v23, 0xc01d265f, v22
	v_exp_f32_e32 v23, v23
	v_add_f32_e32 v19, 1.0, v25
;     __device__ __forceinline__ void operator()(const f32x4 (&acc)[2][2][4][2], const Unit& u, int wr, int wc, int fr, int fq) const {
;     ...
;             for (int m = 0; m < 4; ++m) { const int r = row0 + ai * 128 + m * 16; const float rs = rsb[ai * 4 + m];
;                 float a[8];
; #pragma unroll
;                 for (int j = 0; j < 8; ++j) { const float gb = j < 4 ? g0[j & 3] : g1[j & 3], lb = j < 4 ? l0[j & 3] : l1[j & 3];
;                     const float gl = fminf(acc[ai][0][m][j >> 2][j & 3] * rs + gb, 7.0f), ln = fminf(fmaxf(acc[ai][1][m][j >> 2][j & 3] * rs + lb, -7.0f), 7.0f);
;                     a[j] = gl * __builtin_amdgcn_rcpf(1.0f + __builtin_amdgcn_exp2f(-1.702f * 1.4426950408889634f * gl)) * (ln + 1.0f); }
;                 v2u w; w.x = pk4_fp8(a[0], a[1], a[2], a[3]); w.y = pk4_fp8(a[4], a[5], a[6], a[7]);
;                 *(v2u*)(ACT + ((size_t)u.z * 256 + r) * FF + c0) = w; }
;     __device__ __forceinline__ void done(const Unit& u) const { if (u.pm == (c & 7)) convert_share(); }
	v_rcp_f32_e32 v19, v19
	v_fma_f32 v25, v99, v21, v3
	v_add_f32_e32 v23, 1.0, v23
	v_rcp_f32_e32 v23, v23
	v_mul_f32_e32 v19, v24, v19
	v_min_f32_e32 v25, 0x40e00000, v25
	v_mul_f32_e32 v26, 0xc01d265f, v25
	v_mul_f32_e32 v22, v22, v23
	v_fma_f32 v23, v98, v21, v2
	v_min_f32_e32 v23, 0x40e00000, v23
	v_mul_f32_e32 v24, 0xc01d265f, v23
	v_exp_f32_e32 v24, v24
	v_exp_f32_e32 v26, v26
	v_fma_f32 v27, v89, v21, v13
	v_min_f32_e32 v27, 0x40e00000, v27
	v_add_f32_e32 v24, 1.0, v24
	v_rcp_f32_e32 v24, v24
	v_mul_f32_e32 v28, 0xc01d265f, v27
	v_exp_f32_e32 v28, v28
	v_fma_f32 v18, v92, v21, v8
	v_mul_f32_e32 v23, v23, v24
	v_add_f32_e32 v24, 1.0, v26
	v_rcp_f32_e32 v24, v24
	v_med3_f32 v18, v18, s23, v236
	v_add_f32_e32 v18, 1.0, v18
	v_mul_f32_e32 v18, v18, v19
	v_mul_f32_e32 v24, v25, v24
	v_fma_f32 v25, v88, v21, v12
	v_min_f32_e32 v25, 0x40e00000, v25
	v_mul_f32_e32 v26, 0xc01d265f, v25
	v_exp_f32_e32 v26, v26
	v_fma_f32 v19, v93, v21, v9
	v_med3_f32 v19, v19, s23, v236
	v_add_f32_e32 v19, 1.0, v19
	v_add_f32_e32 v26, 1.0, v26
	v_rcp_f32_e32 v26, v26
	v_mul_f32_e32 v19, v19, v22
	v_fma_f32 v22, v94, v21, v10
	v_med3_f32 v22, v22, s23, v236
	v_mul_f32_e32 v25, v25, v26
	v_add_f32_e32 v26, 1.0, v28
	v_rcp_f32_e32 v26, v26
	v_add_f32_e32 v22, 1.0, v22
	v_mul_f32_e32 v22, v22, v23
	v_fma_f32 v23, v95, v21, v11
	v_mul_f32_e32 v26, v27, v26
	v_fma_f32 v27, v90, v21, v14
	v_min_f32_e32 v27, 0x40e00000, v27
	v_mul_f32_e32 v28, 0xc01d265f, v27
	v_exp_f32_e32 v28, v28
	v_fma_f32 v29, v91, v21, v15
	v_med3_f32 v23, v23, s23, v236
	v_min_f32_e32 v29, 0x40e00000, v29
	v_add_f32_e32 v23, 1.0, v23
	v_add_f32_e32 v28, 1.0, v28
	v_mul_f32_e32 v30, 0xc01d265f, v29
	v_mul_f32_e32 v23, v23, v24
	v_fma_f32 v24, v84, v21, v4
	v_rcp_f32_e32 v28, v28
	v_exp_f32_e32 v30, v30
	v_med3_f32 v24, v24, s23, v236
	v_add_f32_e32 v24, 1.0, v24
	v_mul_f32_e32 v24, v24, v25
	v_fma_f32 v25, v85, v21, v5
	v_med3_f32 v25, v25, s23, v236
	v_mul_f32_e32 v27, v27, v28
	v_add_f32_e32 v28, 1.0, v30
	v_add_f32_e32 v25, 1.0, v25
	v_rcp_f32_e32 v28, v28
	v_mul_f32_e32 v25, v25, v26
	v_fma_f32 v26, v86, v21, v6
	v_med3_f32 v26, v26, s23, v236
	v_fma_f32 v21, v87, v21, v7
	v_add_f32_e32 v26, 1.0, v26
	v_med3_f32 v21, v21, s23, v236
	v_mul_f32_e32 v26, v26, v27
	v_mul_f32_e32 v27, v29, v28
	v_add_f32_e32 v21, 1.0, v21
	v_mul_f32_e32 v21, v21, v27
	v_med3_f32 v27, v18, s24, v237
	v_med3_f32 v19, v19, s24, v237
	v_mov_b32_e32 v18, v65
	v_cvt_pk_fp8_f32 v18, v27, v19
	v_med3_f32 v24, v24, s24, v237
	v_med3_f32 v25, v25, s24, v237
	v_mov_b32_e32 v19, v65
	v_cvt_pk_fp8_f32 v19, v24, v25
	v_mul_f32_e32 v20, 0x3b800000, v20
	v_med3_f32 v22, v22, s24, v237
	v_med3_f32 v23, v23, s24, v237
	v_fma_f32 v14, v74, v20, v14
	v_cvt_pk_fp8_f32 v18, v22, v23 op_sel:[0,0,1]
	v_med3_f32 v22, v26, s24, v237
	v_med3_f32 v21, v21, s24, v237
	v_min_f32_e32 v14, 0x40e00000, v14
	v_cvt_pk_fp8_f32 v19, v22, v21 op_sel:[0,0,1]
	v_mul_f32_e32 v21, 0xc01d265f, v14
	v_exp_f32_e32 v21, v21
	s_mov_b32 s4, 0x50000
	v_add_co_u32_e32 v22, vcc, s4, v16
	v_fma_f32 v13, v73, v20, v13
	s_nop 0
	v_addc_co_u32_e32 v23, vcc, 0, v17, vcc
	global_store_dwordx2 v[22:23], v[18:19], off
	v_add_f32_e32 v18, 1.0, v21
	v_rcp_f32_e32 v18, v18
	v_min_f32_e32 v13, 0x40e00000, v13
	v_fma_f32 v6, v70, v20, v6
	v_med3_f32 v6, v6, s23, v236
	v_mul_f32_e32 v14, v14, v18
	v_mul_f32_e32 v18, 0xc01d265f, v13
	v_exp_f32_e32 v18, v18
	v_add_f32_e32 v6, 1.0, v6
	v_fma_f32 v12, v72, v20, v12
	v_mul_f32_e32 v6, v6, v14
	v_add_f32_e32 v14, 1.0, v18
	v_min_f32_e32 v12, 0x40e00000, v12
	v_rcp_f32_e32 v14, v14
	v_mul_f32_e32 v18, 0xc01d265f, v12
	v_exp_f32_e32 v18, v18
	v_fma_f32 v5, v69, v20, v5
	v_med3_f32 v5, v5, s23, v236
	v_add_f32_e32 v5, 1.0, v5
	v_mul_f32_e32 v13, v13, v14
	v_mul_f32_e32 v5, v5, v13
	v_add_f32_e32 v13, 1.0, v18
	v_rcp_f32_e32 v13, v13
	v_fma_f32 v3, v83, v20, v3
	v_min_f32_e32 v3, 0x40e00000, v3
	v_fma_f32 v4, v68, v20, v4
	v_mul_f32_e32 v12, v12, v13
	v_mul_f32_e32 v13, 0xc01d265f, v3
	v_exp_f32_e32 v13, v13
	v_med3_f32 v4, v4, s23, v236
	v_add_f32_e32 v4, 1.0, v4
	v_fma_f32 v2, v82, v20, v2
	v_mul_f32_e32 v4, v4, v12
	v_add_f32_e32 v12, 1.0, v13
	v_min_f32_e32 v2, 0x40e00000, v2
	v_rcp_f32_e32 v12, v12
	v_mul_f32_e32 v13, 0xc01d265f, v2
	v_exp_f32_e32 v13, v13
	v_fma_f32 v11, v79, v20, v11
	v_med3_f32 v11, v11, s23, v236
	v_add_f32_e32 v11, 1.0, v11
	v_mul_f32_e32 v3, v3, v12
	v_mul_f32_e32 v3, v11, v3
	v_add_f32_e32 v11, 1.0, v13
	v_rcp_f32_e32 v11, v11
	v_fma_f32 v10, v78, v20, v10
	v_med3_f32 v10, v10, s23, v236
	v_fma_f32 v1, v81, v20, v1
	v_add_f32_e32 v10, 1.0, v10
	v_mul_f32_e32 v2, v2, v11
	v_min_f32_e32 v1, 0x40e00000, v1
	v_mul_f32_e32 v2, v10, v2
	v_mul_f32_e32 v10, 0xc01d265f, v1
	v_exp_f32_e32 v10, v10
	v_fmac_f32_e32 v0, v80, v20
	v_min_f32_e32 v0, 0x40e00000, v0
	v_mul_f32_e32 v11, 0xc01d265f, v0
	v_add_f32_e32 v10, 1.0, v10
	v_rcp_f32_e32 v10, v10
	v_exp_f32_e32 v11, v11
	v_fma_f32 v9, v77, v20, v9
	v_med3_f32 v9, v9, s23, v236
	v_fmac_f32_e32 v15, v75, v20
	v_add_f32_e32 v9, 1.0, v9
	v_mul_f32_e32 v1, v1, v10
	v_min_f32_e32 v10, 0x40e00000, v15
	v_mul_f32_e32 v1, v9, v1
	v_add_f32_e32 v9, 1.0, v11
	v_mul_f32_e32 v11, 0xc01d265f, v10
	v_rcp_f32_e32 v9, v9
	v_exp_f32_e32 v11, v11
	v_fmac_f32_e32 v8, v76, v20
	v_med3_f32 v8, v8, s23, v236
	v_mul_f32_e32 v0, v0, v9
	v_add_f32_e32 v9, 1.0, v11
	v_rcp_f32_e32 v9, v9
	v_fmac_f32_e32 v7, v71, v20
	v_add_f32_e32 v8, 1.0, v8
	v_med3_f32 v7, v7, s23, v236
	v_mul_f32_e32 v0, v8, v0
	v_mul_f32_e32 v8, v10, v9
	v_add_f32_e32 v7, 1.0, v7
	v_mul_f32_e32 v7, v7, v8
	v_med3_f32 v8, v0, s24, v237
	v_med3_f32 v1, v1, s24, v237
	v_mov_b32_e32 v0, v65
	v_cvt_pk_fp8_f32 v0, v8, v1
	v_med3_f32 v4, v4, s24, v237
	v_med3_f32 v5, v5, s24, v237
	v_mov_b32_e32 v1, v65
	v_cvt_pk_fp8_f32 v1, v4, v5
	v_med3_f32 v2, v2, s24, v237
	v_med3_f32 v3, v3, s24, v237
	v_cvt_pk_fp8_f32 v0, v2, v3 op_sel:[0,0,1]
	v_med3_f32 v2, v6, s24, v237
	v_med3_f32 v3, v7, s24, v237
	v_cvt_pk_fp8_f32 v1, v2, v3 op_sel:[0,0,1]
	v_add_co_u32_e32 v2, vcc, 0x58000, v16
	s_nop 1
	v_addc_co_u32_e32 v3, vcc, 0, v17, vcc
	global_store_dwordx2 v[2:3], v[0:1], off
	s_cbranch_scc1 .LBB0_1541
; __device__ __forceinline__ int lane_id_now() { unsigned z = 0u; asm volatile("" : "+v"(z)); return (int)__builtin_amdgcn_mbcnt_hi(~0u, __builtin_amdgcn_mbcnt_lo(~0u, z)); }
; #define GAS __attribute__((address_space(1)))
; template <bool GAIN, bool NT = false> __device__ __forceinline__ void titem8_load(const TItem& d, int lane, f32x4 (&r)[16], f32x4 (&g)[4]) {
;     const int q = lane & 7, kg = lane >> 3; const unsigned lo = (unsigned)((16 * kg) * d.N + 4 * q) * 4u;
;     const GAS char* base = (const GAS char*)d.src;
; #pragma unroll
;     for (int j = 0; j < 16; ++j) { const GAS f32x4* p = (const GAS f32x4*)(base + (size_t)j * (size_t)d.N * 4 + lo); r[j] = NT ? __builtin_nontemporal_load(p) : *p; }
;     __device__ __forceinline__ void convert_share() const {
;         const int lane = lane_id_now(), gw = c * NWAVES + wave, NGW = G * NWAVES;
;         constexpr int NIT = E * (FF / 128) * (D / 32);
;         TSTREAM(NIT, dec_dn, TI8L_NT, TI8S_NT);
	v_readlane_b32 s0, v254, 26
	v_readlane_b32 s1, v254, 27
	v_mov_b32_e32 v0, v65
	s_andn2_b64 vcc, exec, s[0:1]
	s_cbranch_vccnz .LBB0_1541
	v_mbcnt_lo_u32_b32 v64, -1, 0
	v_mbcnt_hi_u32_b32 v64, -1, v64
	v_and_b32_e32 v194, 7, v64
	v_lshrrev_b32_e32 v195, 3, v64
	v_lshlrev_b32_e32 v246, 17, v195
	v_lshl_or_b32 v246, v194, 4, v246
	v_add_u32_e32 v247, 0x2000, v246
	v_add_u32_e32 v248, 0x4000, v246
	v_add_u32_e32 v249, 0x6000, v246
	v_lshlrev_b32_e32 v250, 13, v194
	v_lshl_or_b32 v250, v195, 4, v250
	v_add_u32_e32 v251, 0x1000, v250
	v_readlane_b32 s0, v254, 60
	v_readlane_b32 s4, v254, 4
	v_readlane_b32 s5, v254, 5
	s_nop 3
	s_lshl_b32 s1, s92, 3
	s_add_i32 s0, s0, s1
	s_lshr_b32 s1, s0, 10
	s_and_b32 s0, s0, 0x3ff
	s_lshr_b32 s2, s0, 6
	s_and_b32 s0, s0, 63
	s_lshl_b32 s35, s1, 24
	s_lshl_b32 s38, s2, 20
	s_add_i32 s35, s35, s38
	s_lshl_b32 s38, s0, 7
	s_add_i32 s35, s35, s38
	s_add_u32 s4, s4, s35
	s_addc_u32 s5, s5, 0
	s_add_u32 s6, s4, 0x8000
	s_addc_u32 s7, s5, 0
	s_add_u32 s8, s4, 0x10000
	s_addc_u32 s9, s5, 0
	s_add_u32 s38, s4, 0x18000
	s_addc_u32 s39, s5, 0
	s_lshl_b32 s35, s1, 22
	s_lshl_b32 s40, s0, 16
	s_add_i32 s35, s35, s40
	s_lshl_b32 s40, s2, 7
	s_add_i32 s35, s35, s40
	s_add_u32 s42, s78, 0x57dc8000
	s_addc_u32 s43, s79, 0
	s_add_u32 s42, s42, s35
	s_addc_u32 s43, s43, 0
	global_load_dwordx4 v[0:3], v246, s[4:5] nt
	global_load_dwordx4 v[4:7], v247, s[4:5] nt
	global_load_dwordx4 v[8:11], v248, s[4:5] nt
	global_load_dwordx4 v[12:15], v249, s[4:5] nt
	global_load_dwordx4 v[16:19], v246, s[6:7] nt
	global_load_dwordx4 v[20:23], v247, s[6:7] nt
	global_load_dwordx4 v[24:27], v248, s[6:7] nt
	global_load_dwordx4 v[28:31], v249, s[6:7] nt
	global_load_dwordx4 v[32:35], v246, s[8:9] nt
	global_load_dwordx4 v[36:39], v247, s[8:9] nt
	global_load_dwordx4 v[40:43], v248, s[8:9] nt
	global_load_dwordx4 v[44:47], v249, s[8:9] nt
	global_load_dwordx4 v[48:51], v246, s[38:39] nt
	global_load_dwordx4 v[52:55], v247, s[38:39] nt
	global_load_dwordx4 v[56:59], v248, s[38:39] nt
	global_load_dwordx4 v[60:63], v249, s[38:39] nt
	s_add_u32 s4, s4, 0x2000000
	s_addc_u32 s5, s5, 0
	s_add_u32 s6, s6, 0x2000000
	s_addc_u32 s7, s7, 0
	s_add_u32 s8, s8, 0x2000000
	s_addc_u32 s9, s9, 0
	s_add_u32 s38, s38, 0x2000000
	s_addc_u32 s39, s39, 0
	global_load_dwordx4 v[66:69], v246, s[4:5] nt
	global_load_dwordx4 v[70:73], v247, s[4:5] nt
	global_load_dwordx4 v[74:77], v248, s[4:5] nt
	global_load_dwordx4 v[78:81], v249, s[4:5] nt
	global_load_dwordx4 v[82:85], v246, s[6:7] nt
	global_load_dwordx4 v[86:89], v247, s[6:7] nt
	global_load_dwordx4 v[90:93], v248, s[6:7] nt
	global_load_dwordx4 v[94:97], v249, s[6:7] nt
	global_load_dwordx4 v[98:101], v246, s[8:9] nt
	global_load_dwordx4 v[102:105], v247, s[8:9] nt
	global_load_dwordx4 v[106:109], v248, s[8:9] nt
	global_load_dwordx4 v[110:113], v249, s[8:9] nt
	global_load_dwordx4 v[114:117], v246, s[38:39] nt
	global_load_dwordx4 v[118:121], v247, s[38:39] nt
	global_load_dwordx4 v[122:125], v248, s[38:39] nt
	global_load_dwordx4 v[126:129], v249, s[38:39] nt
	s_add_u32 s4, s4, 0x2000000
	s_addc_u32 s5, s5, 0
	s_add_u32 s6, s6, 0x2000000
	s_addc_u32 s7, s7, 0
	s_add_u32 s8, s8, 0x2000000
	s_addc_u32 s9, s9, 0
	s_add_u32 s38, s38, 0x2000000
	s_addc_u32 s39, s39, 0
	global_load_dwordx4 v[130:133], v246, s[4:5] nt
	global_load_dwordx4 v[134:137], v247, s[4:5] nt
	global_load_dwordx4 v[138:141], v248, s[4:5] nt
	global_load_dwordx4 v[142:145], v249, s[4:5] nt
	global_load_dwordx4 v[146:149], v246, s[6:7] nt
	global_load_dwordx4 v[150:153], v247, s[6:7] nt
	global_load_dwordx4 v[154:157], v248, s[6:7] nt
	global_load_dwordx4 v[158:161], v249, s[6:7] nt
	global_load_dwordx4 v[162:165], v246, s[8:9] nt
	global_load_dwordx4 v[166:169], v247, s[8:9] nt
	global_load_dwordx4 v[170:173], v248, s[8:9] nt
	global_load_dwordx4 v[174:177], v249, s[8:9] nt
	global_load_dwordx4 v[178:181], v246, s[38:39] nt
	global_load_dwordx4 v[182:185], v247, s[38:39] nt
	global_load_dwordx4 v[186:189], v248, s[38:39] nt
	global_load_dwordx4 v[190:193], v249, s[38:39] nt
	s_add_u32 s4, s4, 0x2000000
	s_addc_u32 s5, s5, 0
	s_add_u32 s6, s6, 0x2000000
	s_addc_u32 s7, s7, 0
	s_add_u32 s8, s8, 0x2000000
	s_addc_u32 s9, s9, 0
	s_add_u32 s38, s38, 0x2000000
	s_addc_u32 s39, s39, 0
	s_waitcnt vmcnt(32)
; #define GAS __attribute__((address_space(1)))
; template <bool GAIN, bool NT = false> __device__ __forceinline__ void titem8_load(const TItem& d, int lane, f32x4 (&r)[16], f32x4 (&g)[4]) {
;     const int q = lane & 7, kg = lane >> 3; const unsigned lo = (unsigned)((16 * kg) * d.N + 4 * q) * 4u;
;     const GAS char* base = (const GAS char*)d.src;
; #pragma unroll
;     for (int j = 0; j < 16; ++j) { const GAS f32x4* p = (const GAS f32x4*)(base + (size_t)j * (size_t)d.N * 4 + lo); r[j] = NT ? __builtin_nontemporal_load(p) : *p; }
; template <bool GAIN, bool NT = false> __device__ __forceinline__ void titem8_store(const TItem& d, int lane, const f32x4 (&r)[16], const f32x4 (&g)[4]) {
;     const int q = lane & 7, kg = lane >> 3; const unsigned lo = (unsigned)((4 * q) * d.ldk + 16 * kg);
;     GAS char* base = (GAS char*)d.dst;
;     f32x4 s[16];
; #pragma unroll
;     for (int j = 0; j < 16; ++j) s[j] = r[j] * ((GAIN ? g[j >> 2][j & 3] : 1.0f) * W8_SCALE);
; #pragma unroll
;     for (int i = 0; i < 4; ++i) { v4u w;
;         w.x = pk4_fp8w(s[0][i], s[1][i], s[2][i], s[3][i]); w.y = pk4_fp8w(s[4][i], s[5][i], s[6][i], s[7][i]);
;         w.z = pk4_fp8w(s[8][i], s[9][i], s[10][i], s[11][i]); w.w = pk4_fp8w(s[12][i], s[13][i], s[14][i], s[15][i]);
;         GAS v4u* p = (GAS v4u*)(base + (size_t)i * (size_t)d.ldk + lo);
;         if (NT) __builtin_nontemporal_store(w, p); else *p = w; }
	v_pk_mul_f32 v[0:1], v[0:1], s[30:31] op_sel_hi:[1,0]
	v_pk_mul_f32 v[2:3], v[2:3], s[30:31] op_sel_hi:[1,0]
	v_pk_mul_f32 v[4:5], v[4:5], s[30:31] op_sel_hi:[1,0]
	v_pk_mul_f32 v[6:7], v[6:7], s[30:31] op_sel_hi:[1,0]
	v_pk_mul_f32 v[8:9], v[8:9], s[30:31] op_sel_hi:[1,0]
	v_pk_mul_f32 v[10:11], v[10:11], s[30:31] op_sel_hi:[1,0]
	v_pk_mul_f32 v[12:13], v[12:13], s[30:31] op_sel_hi:[1,0]
	v_pk_mul_f32 v[14:15], v[14:15], s[30:31] op_sel_hi:[1,0]
	v_pk_mul_f32 v[16:17], v[16:17], s[30:31] op_sel_hi:[1,0]
	v_pk_mul_f32 v[18:19], v[18:19], s[30:31] op_sel_hi:[1,0]
	v_pk_mul_f32 v[20:21], v[20:21], s[30:31] op_sel_hi:[1,0]
	v_pk_mul_f32 v[22:23], v[22:23], s[30:31] op_sel_hi:[1,0]
	v_pk_mul_f32 v[24:25], v[24:25], s[30:31] op_sel_hi:[1,0]
	v_pk_mul_f32 v[26:27], v[26:27], s[30:31] op_sel_hi:[1,0]
	v_pk_mul_f32 v[28:29], v[28:29], s[30:31] op_sel_hi:[1,0]
	v_pk_mul_f32 v[30:31], v[30:31], s[30:31] op_sel_hi:[1,0]
	v_pk_mul_f32 v[32:33], v[32:33], s[30:31] op_sel_hi:[1,0]
	v_pk_mul_f32 v[34:35], v[34:35], s[30:31] op_sel_hi:[1,0]
	v_pk_mul_f32 v[36:37], v[36:37], s[30:31] op_sel_hi:[1,0]
	v_pk_mul_f32 v[38:39], v[38:39], s[30:31] op_sel_hi:[1,0]
	v_pk_mul_f32 v[40:41], v[40:41], s[30:31] op_sel_hi:[1,0]
	v_pk_mul_f32 v[42:43], v[42:43], s[30:31] op_sel_hi:[1,0]
	v_pk_mul_f32 v[44:45], v[44:45], s[30:31] op_sel_hi:[1,0]
	v_pk_mul_f32 v[46:47], v[46:47], s[30:31] op_sel_hi:[1,0]
	v_pk_mul_f32 v[48:49], v[48:49], s[30:31] op_sel_hi:[1,0]
	v_pk_mul_f32 v[50:51], v[50:51], s[30:31] op_sel_hi:[1,0]
	v_pk_mul_f32 v[52:53], v[52:53], s[30:31] op_sel_hi:[1,0]
	v_pk_mul_f32 v[54:55], v[54:55], s[30:31] op_sel_hi:[1,0]
	v_pk_mul_f32 v[56:57], v[56:57], s[30:31] op_sel_hi:[1,0]
	v_pk_mul_f32 v[58:59], v[58:59], s[30:31] op_sel_hi:[1,0]
	v_pk_mul_f32 v[60:61], v[60:61], s[30:31] op_sel_hi:[1,0]
	v_pk_mul_f32 v[62:63], v[62:63], s[30:31] op_sel_hi:[1,0]
	v_med3_f32 v0, v0, s24, v237
	v_med3_f32 v1, v1, s24, v237
	v_med3_f32 v2, v2, s24, v237
	v_med3_f32 v3, v3, s24, v237
	v_med3_f32 v4, v4, s24, v237
	v_med3_f32 v5, v5, s24, v237
	v_med3_f32 v6, v6, s24, v237
	v_med3_f32 v7, v7, s24, v237
	v_med3_f32 v8, v8, s24, v237
	v_med3_f32 v9, v9, s24, v237
	v_med3_f32 v10, v10, s24, v237
	v_med3_f32 v11, v11, s24, v237
	v_med3_f32 v12, v12, s24, v237
	v_med3_f32 v13, v13, s24, v237
	v_med3_f32 v14, v14, s24, v237
	v_med3_f32 v15, v15, s24, v237
	v_med3_f32 v16, v16, s24, v237
	v_med3_f32 v17, v17, s24, v237
	v_med3_f32 v18, v18, s24, v237
	v_med3_f32 v19, v19, s24, v237
	v_med3_f32 v20, v20, s24, v237
	v_med3_f32 v21, v21, s24, v237
	v_med3_f32 v22, v22, s24, v237
	v_med3_f32 v23, v23, s24, v237
	v_med3_f32 v24, v24, s24, v237
	v_med3_f32 v25, v25, s24, v237
	v_med3_f32 v26, v26, s24, v237
	v_med3_f32 v27, v27, s24, v237
	v_med3_f32 v28, v28, s24, v237
	v_med3_f32 v29, v29, s24, v237
	v_med3_f32 v30, v30, s24, v237
	v_med3_f32 v31, v31, s24, v237
	v_med3_f32 v32, v32, s24, v237
	v_med3_f32 v33, v33, s24, v237
	v_med3_f32 v34, v34, s24, v237
	v_med3_f32 v35, v35, s24, v237
	v_med3_f32 v36, v36, s24, v237
	v_med3_f32 v37, v37, s24, v237
	v_med3_f32 v38, v38, s24, v237
	v_med3_f32 v39, v39, s24, v237
	v_med3_f32 v40, v40, s24, v237
	v_med3_f32 v41, v41, s24, v237
	v_med3_f32 v42, v42, s24, v237
	v_med3_f32 v43, v43, s24, v237
	v_med3_f32 v44, v44, s24, v237
	v_med3_f32 v45, v45, s24, v237
	v_med3_f32 v46, v46, s24, v237
	v_med3_f32 v47, v47, s24, v237
	v_med3_f32 v48, v48, s24, v237
	v_med3_f32 v49, v49, s24, v237
	v_med3_f32 v50, v50, s24, v237
	v_med3_f32 v51, v51, s24, v237
	v_med3_f32 v52, v52, s24, v237
	v_med3_f32 v53, v53, s24, v237
	v_med3_f32 v54, v54, s24, v237
	v_med3_f32 v55, v55, s24, v237
	v_med3_f32 v56, v56, s24, v237
	v_med3_f32 v57, v57, s24, v237
	v_med3_f32 v58, v58, s24, v237
	v_med3_f32 v59, v59, s24, v237
	v_med3_f32 v60, v60, s24, v237
	v_med3_f32 v61, v61, s24, v237
	v_med3_f32 v62, v62, s24, v237
	v_med3_f32 v63, v63, s24, v237
	v_cvt_pk_fp8_f32 v0, v0, v4
	v_cvt_pk_fp8_f32 v0, v8, v12 op_sel:[0,0,1]
	v_cvt_pk_fp8_f32 v4, v1, v5
	v_cvt_pk_fp8_f32 v4, v9, v13 op_sel:[0,0,1]
	v_cvt_pk_fp8_f32 v8, v2, v6
	v_cvt_pk_fp8_f32 v8, v10, v14 op_sel:[0,0,1]
	v_cvt_pk_fp8_f32 v12, v3, v7
	v_cvt_pk_fp8_f32 v12, v11, v15 op_sel:[0,0,1]
	v_cvt_pk_fp8_f32 v1, v16, v20
	v_cvt_pk_fp8_f32 v1, v24, v28 op_sel:[0,0,1]
	v_cvt_pk_fp8_f32 v5, v17, v21
	v_cvt_pk_fp8_f32 v5, v25, v29 op_sel:[0,0,1]
	v_cvt_pk_fp8_f32 v9, v18, v22
	v_cvt_pk_fp8_f32 v9, v26, v30 op_sel:[0,0,1]
	v_cvt_pk_fp8_f32 v13, v19, v23
	v_cvt_pk_fp8_f32 v13, v27, v31 op_sel:[0,0,1]
	v_cvt_pk_fp8_f32 v2, v32, v36
	v_cvt_pk_fp8_f32 v2, v40, v44 op_sel:[0,0,1]
	v_cvt_pk_fp8_f32 v6, v33, v37
	v_cvt_pk_fp8_f32 v6, v41, v45 op_sel:[0,0,1]
	v_cvt_pk_fp8_f32 v10, v34, v38
	v_cvt_pk_fp8_f32 v10, v42, v46 op_sel:[0,0,1]
	v_cvt_pk_fp8_f32 v14, v35, v39
	v_cvt_pk_fp8_f32 v14, v43, v47 op_sel:[0,0,1]
	v_cvt_pk_fp8_f32 v3, v48, v52
	v_cvt_pk_fp8_f32 v3, v56, v60 op_sel:[0,0,1]
	v_cvt_pk_fp8_f32 v7, v49, v53
	v_cvt_pk_fp8_f32 v7, v57, v61 op_sel:[0,0,1]
	v_cvt_pk_fp8_f32 v11, v50, v54
	v_cvt_pk_fp8_f32 v11, v58, v62 op_sel:[0,0,1]
	v_cvt_pk_fp8_f32 v15, v51, v55
	v_cvt_pk_fp8_f32 v15, v59, v63 op_sel:[0,0,1]
	global_store_dwordx4 v250, v[0:3], s[42:43] nt
	global_store_dwordx4 v250, v[4:7], s[42:43] offset:2048 nt
	global_store_dwordx4 v251, v[8:11], s[42:43] nt
	global_store_dwordx4 v251, v[12:15], s[42:43] offset:2048 nt
	s_add_u32 s42, s42, 0x800000
	s_addc_u32 s43, s43, 0
	global_load_dwordx4 v[0:3], v246, s[4:5] nt
	global_load_dwordx4 v[4:7], v247, s[4:5] nt
	global_load_dwordx4 v[8:11], v248, s[4:5] nt
	global_load_dwordx4 v[12:15], v249, s[4:5] nt
	global_load_dwordx4 v[16:19], v246, s[6:7] nt
	global_load_dwordx4 v[20:23], v247, s[6:7] nt
	global_load_dwordx4 v[24:27], v248, s[6:7] nt
	global_load_dwordx4 v[28:31], v249, s[6:7] nt
	global_load_dwordx4 v[32:35], v246, s[8:9] nt
	global_load_dwordx4 v[36:39], v247, s[8:9] nt
	global_load_dwordx4 v[40:43], v248, s[8:9] nt
	global_load_dwordx4 v[44:47], v249, s[8:9] nt
	global_load_dwordx4 v[48:51], v246, s[38:39] nt
	global_load_dwordx4 v[52:55], v247, s[38:39] nt
	global_load_dwordx4 v[56:59], v248, s[38:39] nt
	global_load_dwordx4 v[60:63], v249, s[38:39] nt
	s_add_u32 s4, s4, 0x2000000
	s_addc_u32 s5, s5, 0
	s_add_u32 s6, s6, 0x2000000
	s_addc_u32 s7, s7, 0
	s_add_u32 s8, s8, 0x2000000
	s_addc_u32 s9, s9, 0
	s_add_u32 s38, s38, 0x2000000
	s_addc_u32 s39, s39, 0
	s_waitcnt vmcnt(36)
; #define GAS __attribute__((address_space(1)))
; template <bool GAIN, bool NT = false> __device__ __forceinline__ void titem8_load(const TItem& d, int lane, f32x4 (&r)[16], f32x4 (&g)[4]) {
;     const int q = lane & 7, kg = lane >> 3; const unsigned lo = (unsigned)((16 * kg) * d.N + 4 * q) * 4u;
;     const GAS char* base = (const GAS char*)d.src;
; #pragma unroll
;     for (int j = 0; j < 16; ++j) { const GAS f32x4* p = (const GAS f32x4*)(base + (size_t)j * (size_t)d.N * 4 + lo); r[j] = NT ? __builtin_nontemporal_load(p) : *p; }
; template <bool GAIN, bool NT = false> __device__ __forceinline__ void titem8_store(const TItem& d, int lane, const f32x4 (&r)[16], const f32x4 (&g)[4]) {
;     const int q = lane & 7, kg = lane >> 3; const unsigned lo = (unsigned)((4 * q) * d.ldk + 16 * kg);
;     GAS char* base = (GAS char*)d.dst;
;     f32x4 s[16];
; #pragma unroll
;     for (int j = 0; j < 16; ++j) s[j] = r[j] * ((GAIN ? g[j >> 2][j & 3] : 1.0f) * W8_SCALE);
; #pragma unroll
;     for (int i = 0; i < 4; ++i) { v4u w;
;         w.x = pk4_fp8w(s[0][i], s[1][i], s[2][i], s[3][i]); w.y = pk4_fp8w(s[4][i], s[5][i], s[6][i], s[7][i]);
;         w.z = pk4_fp8w(s[8][i], s[9][i], s[10][i], s[11][i]); w.w = pk4_fp8w(s[12][i], s[13][i], s[14][i], s[15][i]);
;         GAS v4u* p = (GAS v4u*)(base + (size_t)i * (size_t)d.ldk + lo);
;         if (NT) __builtin_nontemporal_store(w, p); else *p = w; }
	v_pk_mul_f32 v[66:67], v[66:67], s[30:31] op_sel_hi:[1,0]
	v_pk_mul_f32 v[68:69], v[68:69], s[30:31] op_sel_hi:[1,0]
	v_pk_mul_f32 v[70:71], v[70:71], s[30:31] op_sel_hi:[1,0]
	v_pk_mul_f32 v[72:73], v[72:73], s[30:31] op_sel_hi:[1,0]
	v_pk_mul_f32 v[74:75], v[74:75], s[30:31] op_sel_hi:[1,0]
	v_pk_mul_f32 v[76:77], v[76:77], s[30:31] op_sel_hi:[1,0]
	v_pk_mul_f32 v[78:79], v[78:79], s[30:31] op_sel_hi:[1,0]
	v_pk_mul_f32 v[80:81], v[80:81], s[30:31] op_sel_hi:[1,0]
	v_pk_mul_f32 v[82:83], v[82:83], s[30:31] op_sel_hi:[1,0]
	v_pk_mul_f32 v[84:85], v[84:85], s[30:31] op_sel_hi:[1,0]
	v_pk_mul_f32 v[86:87], v[86:87], s[30:31] op_sel_hi:[1,0]
	v_pk_mul_f32 v[88:89], v[88:89], s[30:31] op_sel_hi:[1,0]
	v_pk_mul_f32 v[90:91], v[90:91], s[30:31] op_sel_hi:[1,0]
	v_pk_mul_f32 v[92:93], v[92:93], s[30:31] op_sel_hi:[1,0]
	v_pk_mul_f32 v[94:95], v[94:95], s[30:31] op_sel_hi:[1,0]
	v_pk_mul_f32 v[96:97], v[96:97], s[30:31] op_sel_hi:[1,0]
	v_pk_mul_f32 v[98:99], v[98:99], s[30:31] op_sel_hi:[1,0]
	v_pk_mul_f32 v[100:101], v[100:101], s[30:31] op_sel_hi:[1,0]
	v_pk_mul_f32 v[102:103], v[102:103], s[30:31] op_sel_hi:[1,0]
	v_pk_mul_f32 v[104:105], v[104:105], s[30:31] op_sel_hi:[1,0]
	v_pk_mul_f32 v[106:107], v[106:107], s[30:31] op_sel_hi:[1,0]
	v_pk_mul_f32 v[108:109], v[108:109], s[30:31] op_sel_hi:[1,0]
	v_pk_mul_f32 v[110:111], v[110:111], s[30:31] op_sel_hi:[1,0]
	v_pk_mul_f32 v[112:113], v[112:113], s[30:31] op_sel_hi:[1,0]
	v_pk_mul_f32 v[114:115], v[114:115], s[30:31] op_sel_hi:[1,0]
	v_pk_mul_f32 v[116:117], v[116:117], s[30:31] op_sel_hi:[1,0]
	v_pk_mul_f32 v[118:119], v[118:119], s[30:31] op_sel_hi:[1,0]
	v_pk_mul_f32 v[120:121], v[120:121], s[30:31] op_sel_hi:[1,0]
	v_pk_mul_f32 v[122:123], v[122:123], s[30:31] op_sel_hi:[1,0]
	v_pk_mul_f32 v[124:125], v[124:125], s[30:31] op_sel_hi:[1,0]
	v_pk_mul_f32 v[126:127], v[126:127], s[30:31] op_sel_hi:[1,0]
	v_pk_mul_f32 v[128:129], v[128:129], s[30:31] op_sel_hi:[1,0]
	v_med3_f32 v66, v66, s24, v237
	v_med3_f32 v67, v67, s24, v237
	v_med3_f32 v68, v68, s24, v237
	v_med3_f32 v69, v69, s24, v237
	v_med3_f32 v70, v70, s24, v237
	v_med3_f32 v71, v71, s24, v237
	v_med3_f32 v72, v72, s24, v237
	v_med3_f32 v73, v73, s24, v237
	v_med3_f32 v74, v74, s24, v237
	v_med3_f32 v75, v75, s24, v237
	v_med3_f32 v76, v76, s24, v237
	v_med3_f32 v77, v77, s24, v237
	v_med3_f32 v78, v78, s24, v237
	v_med3_f32 v79, v79, s24, v237
	v_med3_f32 v80, v80, s24, v237
	v_med3_f32 v81, v81, s24, v237
	v_med3_f32 v82, v82, s24, v237
	v_med3_f32 v83, v83, s24, v237
	v_med3_f32 v84, v84, s24, v237
	v_med3_f32 v85, v85, s24, v237
	v_med3_f32 v86, v86, s24, v237
	v_med3_f32 v87, v87, s24, v237
	v_med3_f32 v88, v88, s24, v237
	v_med3_f32 v89, v89, s24, v237
	v_med3_f32 v90, v90, s24, v237
	v_med3_f32 v91, v91, s24, v237
	v_med3_f32 v92, v92, s24, v237
	v_med3_f32 v93, v93, s24, v237
	v_med3_f32 v94, v94, s24, v237
	v_med3_f32 v95, v95, s24, v237
	v_med3_f32 v96, v96, s24, v237
	v_med3_f32 v97, v97, s24, v237
	v_med3_f32 v98, v98, s24, v237
	v_med3_f32 v99, v99, s24, v237
	v_med3_f32 v100, v100, s24, v237
	v_med3_f32 v101, v101, s24, v237
	v_med3_f32 v102, v102, s24, v237
	v_med3_f32 v103, v103, s24, v237
	v_med3_f32 v104, v104, s24, v237
	v_med3_f32 v105, v105, s24, v237
	v_med3_f32 v106, v106, s24, v237
	v_med3_f32 v107, v107, s24, v237
	v_med3_f32 v108, v108, s24, v237
	v_med3_f32 v109, v109, s24, v237
	v_med3_f32 v110, v110, s24, v237
	v_med3_f32 v111, v111, s24, v237
	v_med3_f32 v112, v112, s24, v237
	v_med3_f32 v113, v113, s24, v237
	v_med3_f32 v114, v114, s24, v237
	v_med3_f32 v115, v115, s24, v237
	v_med3_f32 v116, v116, s24, v237
	v_med3_f32 v117, v117, s24, v237
	v_med3_f32 v118, v118, s24, v237
	v_med3_f32 v119, v119, s24, v237
	v_med3_f32 v120, v120, s24, v237
	v_med3_f32 v121, v121, s24, v237
	v_med3_f32 v122, v122, s24, v237
	v_med3_f32 v123, v123, s24, v237
	v_med3_f32 v124, v124, s24, v237
	v_med3_f32 v125, v125, s24, v237
	v_med3_f32 v126, v126, s24, v237
	v_med3_f32 v127, v127, s24, v237
	v_med3_f32 v128, v128, s24, v237
	v_med3_f32 v129, v129, s24, v237
	v_cvt_pk_fp8_f32 v66, v66, v70
	v_cvt_pk_fp8_f32 v66, v74, v78 op_sel:[0,0,1]
	v_cvt_pk_fp8_f32 v70, v67, v71
	v_cvt_pk_fp8_f32 v70, v75, v79 op_sel:[0,0,1]
	v_cvt_pk_fp8_f32 v74, v68, v72
	v_cvt_pk_fp8_f32 v74, v76, v80 op_sel:[0,0,1]
	v_cvt_pk_fp8_f32 v78, v69, v73
	v_cvt_pk_fp8_f32 v78, v77, v81 op_sel:[0,0,1]
	v_cvt_pk_fp8_f32 v67, v82, v86
	v_cvt_pk_fp8_f32 v67, v90, v94 op_sel:[0,0,1]
	v_cvt_pk_fp8_f32 v71, v83, v87
	v_cvt_pk_fp8_f32 v71, v91, v95 op_sel:[0,0,1]
	v_cvt_pk_fp8_f32 v75, v84, v88
	v_cvt_pk_fp8_f32 v75, v92, v96 op_sel:[0,0,1]
	v_cvt_pk_fp8_f32 v79, v85, v89
	v_cvt_pk_fp8_f32 v79, v93, v97 op_sel:[0,0,1]
	v_cvt_pk_fp8_f32 v68, v98, v102
	v_cvt_pk_fp8_f32 v68, v106, v110 op_sel:[0,0,1]
	v_cvt_pk_fp8_f32 v72, v99, v103
	v_cvt_pk_fp8_f32 v72, v107, v111 op_sel:[0,0,1]
	v_cvt_pk_fp8_f32 v76, v100, v104
	v_cvt_pk_fp8_f32 v76, v108, v112 op_sel:[0,0,1]
	v_cvt_pk_fp8_f32 v80, v101, v105
	v_cvt_pk_fp8_f32 v80, v109, v113 op_sel:[0,0,1]
	v_cvt_pk_fp8_f32 v69, v114, v118
	v_cvt_pk_fp8_f32 v69, v122, v126 op_sel:[0,0,1]
	v_cvt_pk_fp8_f32 v73, v115, v119
	v_cvt_pk_fp8_f32 v73, v123, v127 op_sel:[0,0,1]
	v_cvt_pk_fp8_f32 v77, v116, v120
	v_cvt_pk_fp8_f32 v77, v124, v128 op_sel:[0,0,1]
	v_cvt_pk_fp8_f32 v81, v117, v121
	v_cvt_pk_fp8_f32 v81, v125, v129 op_sel:[0,0,1]
	global_store_dwordx4 v250, v[66:69], s[42:43] nt
	global_store_dwordx4 v250, v[70:73], s[42:43] offset:2048 nt
	global_store_dwordx4 v251, v[74:77], s[42:43] nt
	global_store_dwordx4 v251, v[78:81], s[42:43] offset:2048 nt
	s_add_u32 s42, s42, 0x800000
	s_addc_u32 s43, s43, 0
	global_load_dwordx4 v[66:69], v246, s[4:5] nt
	global_load_dwordx4 v[70:73], v247, s[4:5] nt
	global_load_dwordx4 v[74:77], v248, s[4:5] nt
	global_load_dwordx4 v[78:81], v249, s[4:5] nt
	global_load_dwordx4 v[82:85], v246, s[6:7] nt
	global_load_dwordx4 v[86:89], v247, s[6:7] nt
	global_load_dwordx4 v[90:93], v248, s[6:7] nt
	global_load_dwordx4 v[94:97], v249, s[6:7] nt
	global_load_dwordx4 v[98:101], v246, s[8:9] nt
	global_load_dwordx4 v[102:105], v247, s[8:9] nt
	global_load_dwordx4 v[106:109], v248, s[8:9] nt
	global_load_dwordx4 v[110:113], v249, s[8:9] nt
	global_load_dwordx4 v[114:117], v246, s[38:39] nt
	global_load_dwordx4 v[118:121], v247, s[38:39] nt
	global_load_dwordx4 v[122:125], v248, s[38:39] nt
	global_load_dwordx4 v[126:129], v249, s[38:39] nt
	s_add_u32 s4, s4, 0x2000000
	s_addc_u32 s5, s5, 0
	s_add_u32 s6, s6, 0x2000000
	s_addc_u32 s7, s7, 0
	s_add_u32 s8, s8, 0x2000000
	s_addc_u32 s9, s9, 0
	s_add_u32 s38, s38, 0x2000000
	s_addc_u32 s39, s39, 0
	s_waitcnt vmcnt(40)
; #define GAS __attribute__((address_space(1)))
; template <bool GAIN, bool NT = false> __device__ __forceinline__ void titem8_load(const TItem& d, int lane, f32x4 (&r)[16], f32x4 (&g)[4]) {
;     const int q = lane & 7, kg = lane >> 3; const unsigned lo = (unsigned)((16 * kg) * d.N + 4 * q) * 4u;
;     const GAS char* base = (const GAS char*)d.src;
; #pragma unroll
;     for (int j = 0; j < 16; ++j) { const GAS f32x4* p = (const GAS f32x4*)(base + (size_t)j * (size_t)d.N * 4 + lo); r[j] = NT ? __builtin_nontemporal_load(p) : *p; }
; template <bool GAIN, bool NT = false> __device__ __forceinline__ void titem8_store(const TItem& d, int lane, const f32x4 (&r)[16], const f32x4 (&g)[4]) {
;     const int q = lane & 7, kg = lane >> 3; const unsigned lo = (unsigned)((4 * q) * d.ldk + 16 * kg);
;     GAS char* base = (GAS char*)d.dst;
;     f32x4 s[16];
; #pragma unroll
;     for (int j = 0; j < 16; ++j) s[j] = r[j] * ((GAIN ? g[j >> 2][j & 3] : 1.0f) * W8_SCALE);
; #pragma unroll
;     for (int i = 0; i < 4; ++i) { v4u w;
;         w.x = pk4_fp8w(s[0][i], s[1][i], s[2][i], s[3][i]); w.y = pk4_fp8w(s[4][i], s[5][i], s[6][i], s[7][i]);
;         w.z = pk4_fp8w(s[8][i], s[9][i], s[10][i], s[11][i]); w.w = pk4_fp8w(s[12][i], s[13][i], s[14][i], s[15][i]);
;         GAS v4u* p = (GAS v4u*)(base + (size_t)i * (size_t)d.ldk + lo);
;         if (NT) __builtin_nontemporal_store(w, p); else *p = w; }
	v_pk_mul_f32 v[130:131], v[130:131], s[30:31] op_sel_hi:[1,0]
	v_pk_mul_f32 v[132:133], v[132:133], s[30:31] op_sel_hi:[1,0]
	v_pk_mul_f32 v[134:135], v[134:135], s[30:31] op_sel_hi:[1,0]
	v_pk_mul_f32 v[136:137], v[136:137], s[30:31] op_sel_hi:[1,0]
	v_pk_mul_f32 v[138:139], v[138:139], s[30:31] op_sel_hi:[1,0]
	v_pk_mul_f32 v[140:141], v[140:141], s[30:31] op_sel_hi:[1,0]
	v_pk_mul_f32 v[142:143], v[142:143], s[30:31] op_sel_hi:[1,0]
	v_pk_mul_f32 v[144:145], v[144:145], s[30:31] op_sel_hi:[1,0]
	v_pk_mul_f32 v[146:147], v[146:147], s[30:31] op_sel_hi:[1,0]
	v_pk_mul_f32 v[148:149], v[148:149], s[30:31] op_sel_hi:[1,0]
	v_pk_mul_f32 v[150:151], v[150:151], s[30:31] op_sel_hi:[1,0]
	v_pk_mul_f32 v[152:153], v[152:153], s[30:31] op_sel_hi:[1,0]
	v_pk_mul_f32 v[154:155], v[154:155], s[30:31] op_sel_hi:[1,0]
	v_pk_mul_f32 v[156:157], v[156:157], s[30:31] op_sel_hi:[1,0]
	v_pk_mul_f32 v[158:159], v[158:159], s[30:31] op_sel_hi:[1,0]
	v_pk_mul_f32 v[160:161], v[160:161], s[30:31] op_sel_hi:[1,0]
	v_pk_mul_f32 v[162:163], v[162:163], s[30:31] op_sel_hi:[1,0]
	v_pk_mul_f32 v[164:165], v[164:165], s[30:31] op_sel_hi:[1,0]
	v_pk_mul_f32 v[166:167], v[166:167], s[30:31] op_sel_hi:[1,0]
	v_pk_mul_f32 v[168:169], v[168:169], s[30:31] op_sel_hi:[1,0]
	v_pk_mul_f32 v[170:171], v[170:171], s[30:31] op_sel_hi:[1,0]
	v_pk_mul_f32 v[172:173], v[172:173], s[30:31] op_sel_hi:[1,0]
	v_pk_mul_f32 v[174:175], v[174:175], s[30:31] op_sel_hi:[1,0]
	v_pk_mul_f32 v[176:177], v[176:177], s[30:31] op_sel_hi:[1,0]
	v_pk_mul_f32 v[178:179], v[178:179], s[30:31] op_sel_hi:[1,0]
	v_pk_mul_f32 v[180:181], v[180:181], s[30:31] op_sel_hi:[1,0]
	v_pk_mul_f32 v[182:183], v[182:183], s[30:31] op_sel_hi:[1,0]
	v_pk_mul_f32 v[184:185], v[184:185], s[30:31] op_sel_hi:[1,0]
	v_pk_mul_f32 v[186:187], v[186:187], s[30:31] op_sel_hi:[1,0]
	v_pk_mul_f32 v[188:189], v[188:189], s[30:31] op_sel_hi:[1,0]
	v_pk_mul_f32 v[190:191], v[190:191], s[30:31] op_sel_hi:[1,0]
	v_pk_mul_f32 v[192:193], v[192:193], s[30:31] op_sel_hi:[1,0]
	v_med3_f32 v130, v130, s24, v237
	v_med3_f32 v131, v131, s24, v237
	v_med3_f32 v132, v132, s24, v237
	v_med3_f32 v133, v133, s24, v237
	v_med3_f32 v134, v134, s24, v237
	v_med3_f32 v135, v135, s24, v237
	v_med3_f32 v136, v136, s24, v237
	v_med3_f32 v137, v137, s24, v237
	v_med3_f32 v138, v138, s24, v237
	v_med3_f32 v139, v139, s24, v237
	v_med3_f32 v140, v140, s24, v237
	v_med3_f32 v141, v141, s24, v237
	v_med3_f32 v142, v142, s24, v237
	v_med3_f32 v143, v143, s24, v237
	v_med3_f32 v144, v144, s24, v237
	v_med3_f32 v145, v145, s24, v237
	v_med3_f32 v146, v146, s24, v237
	v_med3_f32 v147, v147, s24, v237
	v_med3_f32 v148, v148, s24, v237
	v_med3_f32 v149, v149, s24, v237
	v_med3_f32 v150, v150, s24, v237
	v_med3_f32 v151, v151, s24, v237
	v_med3_f32 v152, v152, s24, v237
	v_med3_f32 v153, v153, s24, v237
	v_med3_f32 v154, v154, s24, v237
	v_med3_f32 v155, v155, s24, v237
	v_med3_f32 v156, v156, s24, v237
	v_med3_f32 v157, v157, s24, v237
	v_med3_f32 v158, v158, s24, v237
	v_med3_f32 v159, v159, s24, v237
	v_med3_f32 v160, v160, s24, v237
	v_med3_f32 v161, v161, s24, v237
	v_med3_f32 v162, v162, s24, v237
	v_med3_f32 v163, v163, s24, v237
	v_med3_f32 v164, v164, s24, v237
	v_med3_f32 v165, v165, s24, v237
	v_med3_f32 v166, v166, s24, v237
	v_med3_f32 v167, v167, s24, v237
	v_med3_f32 v168, v168, s24, v237
	v_med3_f32 v169, v169, s24, v237
	v_med3_f32 v170, v170, s24, v237
	v_med3_f32 v171, v171, s24, v237
	v_med3_f32 v172, v172, s24, v237
	v_med3_f32 v173, v173, s24, v237
	v_med3_f32 v174, v174, s24, v237
	v_med3_f32 v175, v175, s24, v237
	v_med3_f32 v176, v176, s24, v237
	v_med3_f32 v177, v177, s24, v237
	v_med3_f32 v178, v178, s24, v237
	v_med3_f32 v179, v179, s24, v237
	v_med3_f32 v180, v180, s24, v237
	v_med3_f32 v181, v181, s24, v237
	v_med3_f32 v182, v182, s24, v237
	v_med3_f32 v183, v183, s24, v237
	v_med3_f32 v184, v184, s24, v237
	v_med3_f32 v185, v185, s24, v237
	v_med3_f32 v186, v186, s24, v237
	v_med3_f32 v187, v187, s24, v237
	v_med3_f32 v188, v188, s24, v237
	v_med3_f32 v189, v189, s24, v237
	v_med3_f32 v190, v190, s24, v237
	v_med3_f32 v191, v191, s24, v237
	v_med3_f32 v192, v192, s24, v237
	v_med3_f32 v193, v193, s24, v237
	v_cvt_pk_fp8_f32 v130, v130, v134
	v_cvt_pk_fp8_f32 v130, v138, v142 op_sel:[0,0,1]
	v_cvt_pk_fp8_f32 v134, v131, v135
	v_cvt_pk_fp8_f32 v134, v139, v143 op_sel:[0,0,1]
	v_cvt_pk_fp8_f32 v138, v132, v136
	v_cvt_pk_fp8_f32 v138, v140, v144 op_sel:[0,0,1]
	v_cvt_pk_fp8_f32 v142, v133, v137
	v_cvt_pk_fp8_f32 v142, v141, v145 op_sel:[0,0,1]
	v_cvt_pk_fp8_f32 v131, v146, v150
	v_cvt_pk_fp8_f32 v131, v154, v158 op_sel:[0,0,1]
	v_cvt_pk_fp8_f32 v135, v147, v151
	v_cvt_pk_fp8_f32 v135, v155, v159 op_sel:[0,0,1]
	v_cvt_pk_fp8_f32 v139, v148, v152
	v_cvt_pk_fp8_f32 v139, v156, v160 op_sel:[0,0,1]
	v_cvt_pk_fp8_f32 v143, v149, v153
	v_cvt_pk_fp8_f32 v143, v157, v161 op_sel:[0,0,1]
	v_cvt_pk_fp8_f32 v132, v162, v166
	v_cvt_pk_fp8_f32 v132, v170, v174 op_sel:[0,0,1]
	v_cvt_pk_fp8_f32 v136, v163, v167
	v_cvt_pk_fp8_f32 v136, v171, v175 op_sel:[0,0,1]
	v_cvt_pk_fp8_f32 v140, v164, v168
	v_cvt_pk_fp8_f32 v140, v172, v176 op_sel:[0,0,1]
	v_cvt_pk_fp8_f32 v144, v165, v169
	v_cvt_pk_fp8_f32 v144, v173, v177 op_sel:[0,0,1]
	v_cvt_pk_fp8_f32 v133, v178, v182
	v_cvt_pk_fp8_f32 v133, v186, v190 op_sel:[0,0,1]
	v_cvt_pk_fp8_f32 v137, v179, v183
	v_cvt_pk_fp8_f32 v137, v187, v191 op_sel:[0,0,1]
	v_cvt_pk_fp8_f32 v141, v180, v184
	v_cvt_pk_fp8_f32 v141, v188, v192 op_sel:[0,0,1]
	v_cvt_pk_fp8_f32 v145, v181, v185
	v_cvt_pk_fp8_f32 v145, v189, v193 op_sel:[0,0,1]
	global_store_dwordx4 v250, v[130:133], s[42:43] nt
	global_store_dwordx4 v250, v[134:137], s[42:43] offset:2048 nt
	global_store_dwordx4 v251, v[138:141], s[42:43] nt
	global_store_dwordx4 v251, v[142:145], s[42:43] offset:2048 nt
	s_add_u32 s42, s42, 0x800000
	s_addc_u32 s43, s43, 0
	global_load_dwordx4 v[130:133], v246, s[4:5] nt
	global_load_dwordx4 v[134:137], v247, s[4:5] nt
	global_load_dwordx4 v[138:141], v248, s[4:5] nt
	global_load_dwordx4 v[142:145], v249, s[4:5] nt
	global_load_dwordx4 v[146:149], v246, s[6:7] nt
	global_load_dwordx4 v[150:153], v247, s[6:7] nt
	global_load_dwordx4 v[154:157], v248, s[6:7] nt
	global_load_dwordx4 v[158:161], v249, s[6:7] nt
	global_load_dwordx4 v[162:165], v246, s[8:9] nt
	global_load_dwordx4 v[166:169], v247, s[8:9] nt
	global_load_dwordx4 v[170:173], v248, s[8:9] nt
	global_load_dwordx4 v[174:177], v249, s[8:9] nt
	global_load_dwordx4 v[178:181], v246, s[38:39] nt
	global_load_dwordx4 v[182:185], v247, s[38:39] nt
	global_load_dwordx4 v[186:189], v248, s[38:39] nt
	global_load_dwordx4 v[190:193], v249, s[38:39] nt
	s_add_u32 s4, s4, 0x2000000
	s_addc_u32 s5, s5, 0
	s_add_u32 s6, s6, 0x2000000
	s_addc_u32 s7, s7, 0
	s_add_u32 s8, s8, 0x2000000
	s_addc_u32 s9, s9, 0
	s_add_u32 s38, s38, 0x2000000
	s_addc_u32 s39, s39, 0
	s_waitcnt vmcnt(40)
; #define GAS __attribute__((address_space(1)))
; template <bool GAIN, bool NT = false> __device__ __forceinline__ void titem8_load(const TItem& d, int lane, f32x4 (&r)[16], f32x4 (&g)[4]) {
;     const int q = lane & 7, kg = lane >> 3; const unsigned lo = (unsigned)((16 * kg) * d.N + 4 * q) * 4u;
;     const GAS char* base = (const GAS char*)d.src;
; #pragma unroll
;     for (int j = 0; j < 16; ++j) { const GAS f32x4* p = (const GAS f32x4*)(base + (size_t)j * (size_t)d.N * 4 + lo); r[j] = NT ? __builtin_nontemporal_load(p) : *p; }
; template <bool GAIN, bool NT = false> __device__ __forceinline__ void titem8_store(const TItem& d, int lane, const f32x4 (&r)[16], const f32x4 (&g)[4]) {
;     const int q = lane & 7, kg = lane >> 3; const unsigned lo = (unsigned)((4 * q) * d.ldk + 16 * kg);
;     GAS char* base = (GAS char*)d.dst;
;     f32x4 s[16];
; #pragma unroll
;     for (int j = 0; j < 16; ++j) s[j] = r[j] * ((GAIN ? g[j >> 2][j & 3] : 1.0f) * W8_SCALE);
; #pragma unroll
;     for (int i = 0; i < 4; ++i) { v4u w;
;         w.x = pk4_fp8w(s[0][i], s[1][i], s[2][i], s[3][i]); w.y = pk4_fp8w(s[4][i], s[5][i], s[6][i], s[7][i]);
;         w.z = pk4_fp8w(s[8][i], s[9][i], s[10][i], s[11][i]); w.w = pk4_fp8w(s[12][i], s[13][i], s[14][i], s[15][i]);
;         GAS v4u* p = (GAS v4u*)(base + (size_t)i * (size_t)d.ldk + lo);
;         if (NT) __builtin_nontemporal_store(w, p); else *p = w; }
	v_pk_mul_f32 v[0:1], v[0:1], s[30:31] op_sel_hi:[1,0]
	v_pk_mul_f32 v[2:3], v[2:3], s[30:31] op_sel_hi:[1,0]
	v_pk_mul_f32 v[4:5], v[4:5], s[30:31] op_sel_hi:[1,0]
	v_pk_mul_f32 v[6:7], v[6:7], s[30:31] op_sel_hi:[1,0]
	v_pk_mul_f32 v[8:9], v[8:9], s[30:31] op_sel_hi:[1,0]
	v_pk_mul_f32 v[10:11], v[10:11], s[30:31] op_sel_hi:[1,0]
	v_pk_mul_f32 v[12:13], v[12:13], s[30:31] op_sel_hi:[1,0]
	v_pk_mul_f32 v[14:15], v[14:15], s[30:31] op_sel_hi:[1,0]
	v_pk_mul_f32 v[16:17], v[16:17], s[30:31] op_sel_hi:[1,0]
	v_pk_mul_f32 v[18:19], v[18:19], s[30:31] op_sel_hi:[1,0]
	v_pk_mul_f32 v[20:21], v[20:21], s[30:31] op_sel_hi:[1,0]
	v_pk_mul_f32 v[22:23], v[22:23], s[30:31] op_sel_hi:[1,0]
	v_pk_mul_f32 v[24:25], v[24:25], s[30:31] op_sel_hi:[1,0]
	v_pk_mul_f32 v[26:27], v[26:27], s[30:31] op_sel_hi:[1,0]
	v_pk_mul_f32 v[28:29], v[28:29], s[30:31] op_sel_hi:[1,0]
	v_pk_mul_f32 v[30:31], v[30:31], s[30:31] op_sel_hi:[1,0]
	v_pk_mul_f32 v[32:33], v[32:33], s[30:31] op_sel_hi:[1,0]
	v_pk_mul_f32 v[34:35], v[34:35], s[30:31] op_sel_hi:[1,0]
	v_pk_mul_f32 v[36:37], v[36:37], s[30:31] op_sel_hi:[1,0]
	v_pk_mul_f32 v[38:39], v[38:39], s[30:31] op_sel_hi:[1,0]
	v_pk_mul_f32 v[40:41], v[40:41], s[30:31] op_sel_hi:[1,0]
	v_pk_mul_f32 v[42:43], v[42:43], s[30:31] op_sel_hi:[1,0]
	v_pk_mul_f32 v[44:45], v[44:45], s[30:31] op_sel_hi:[1,0]
	v_pk_mul_f32 v[46:47], v[46:47], s[30:31] op_sel_hi:[1,0]
	v_pk_mul_f32 v[48:49], v[48:49], s[30:31] op_sel_hi:[1,0]
	v_pk_mul_f32 v[50:51], v[50:51], s[30:31] op_sel_hi:[1,0]
	v_pk_mul_f32 v[52:53], v[52:53], s[30:31] op_sel_hi:[1,0]
	v_pk_mul_f32 v[54:55], v[54:55], s[30:31] op_sel_hi:[1,0]
	v_pk_mul_f32 v[56:57], v[56:57], s[30:31] op_sel_hi:[1,0]
	v_pk_mul_f32 v[58:59], v[58:59], s[30:31] op_sel_hi:[1,0]
	v_pk_mul_f32 v[60:61], v[60:61], s[30:31] op_sel_hi:[1,0]
	v_pk_mul_f32 v[62:63], v[62:63], s[30:31] op_sel_hi:[1,0]
	v_med3_f32 v0, v0, s24, v237
	v_med3_f32 v1, v1, s24, v237
	v_med3_f32 v2, v2, s24, v237
	v_med3_f32 v3, v3, s24, v237
	v_med3_f32 v4, v4, s24, v237
	v_med3_f32 v5, v5, s24, v237
	v_med3_f32 v6, v6, s24, v237
	v_med3_f32 v7, v7, s24, v237
	v_med3_f32 v8, v8, s24, v237
	v_med3_f32 v9, v9, s24, v237
	v_med3_f32 v10, v10, s24, v237
	v_med3_f32 v11, v11, s24, v237
	v_med3_f32 v12, v12, s24, v237
	v_med3_f32 v13, v13, s24, v237
	v_med3_f32 v14, v14, s24, v237
	v_med3_f32 v15, v15, s24, v237
	v_med3_f32 v16, v16, s24, v237
	v_med3_f32 v17, v17, s24, v237
	v_med3_f32 v18, v18, s24, v237
	v_med3_f32 v19, v19, s24, v237
	v_med3_f32 v20, v20, s24, v237
	v_med3_f32 v21, v21, s24, v237
	v_med3_f32 v22, v22, s24, v237
	v_med3_f32 v23, v23, s24, v237
	v_med3_f32 v24, v24, s24, v237
	v_med3_f32 v25, v25, s24, v237
	v_med3_f32 v26, v26, s24, v237
	v_med3_f32 v27, v27, s24, v237
	v_med3_f32 v28, v28, s24, v237
	v_med3_f32 v29, v29, s24, v237
	v_med3_f32 v30, v30, s24, v237
	v_med3_f32 v31, v31, s24, v237
	v_med3_f32 v32, v32, s24, v237
	v_med3_f32 v33, v33, s24, v237
	v_med3_f32 v34, v34, s24, v237
	v_med3_f32 v35, v35, s24, v237
	v_med3_f32 v36, v36, s24, v237
	v_med3_f32 v37, v37, s24, v237
	v_med3_f32 v38, v38, s24, v237
	v_med3_f32 v39, v39, s24, v237
	v_med3_f32 v40, v40, s24, v237
	v_med3_f32 v41, v41, s24, v237
	v_med3_f32 v42, v42, s24, v237
	v_med3_f32 v43, v43, s24, v237
	v_med3_f32 v44, v44, s24, v237
	v_med3_f32 v45, v45, s24, v237
	v_med3_f32 v46, v46, s24, v237
	v_med3_f32 v47, v47, s24, v237
	v_med3_f32 v48, v48, s24, v237
	v_med3_f32 v49, v49, s24, v237
	v_med3_f32 v50, v50, s24, v237
	v_med3_f32 v51, v51, s24, v237
	v_med3_f32 v52, v52, s24, v237
	v_med3_f32 v53, v53, s24, v237
	v_med3_f32 v54, v54, s24, v237
	v_med3_f32 v55, v55, s24, v237
	v_med3_f32 v56, v56, s24, v237
	v_med3_f32 v57, v57, s24, v237
	v_med3_f32 v58, v58, s24, v237
	v_med3_f32 v59, v59, s24, v237
	v_med3_f32 v60, v60, s24, v237
	v_med3_f32 v61, v61, s24, v237
	v_med3_f32 v62, v62, s24, v237
	v_med3_f32 v63, v63, s24, v237
	v_cvt_pk_fp8_f32 v0, v0, v4
	v_cvt_pk_fp8_f32 v0, v8, v12 op_sel:[0,0,1]
	v_cvt_pk_fp8_f32 v4, v1, v5
	v_cvt_pk_fp8_f32 v4, v9, v13 op_sel:[0,0,1]
	v_cvt_pk_fp8_f32 v8, v2, v6
	v_cvt_pk_fp8_f32 v8, v10, v14 op_sel:[0,0,1]
	v_cvt_pk_fp8_f32 v12, v3, v7
	v_cvt_pk_fp8_f32 v12, v11, v15 op_sel:[0,0,1]
	v_cvt_pk_fp8_f32 v1, v16, v20
	v_cvt_pk_fp8_f32 v1, v24, v28 op_sel:[0,0,1]
	v_cvt_pk_fp8_f32 v5, v17, v21
	v_cvt_pk_fp8_f32 v5, v25, v29 op_sel:[0,0,1]
	v_cvt_pk_fp8_f32 v9, v18, v22
	v_cvt_pk_fp8_f32 v9, v26, v30 op_sel:[0,0,1]
	v_cvt_pk_fp8_f32 v13, v19, v23
	v_cvt_pk_fp8_f32 v13, v27, v31 op_sel:[0,0,1]
	v_cvt_pk_fp8_f32 v2, v32, v36
	v_cvt_pk_fp8_f32 v2, v40, v44 op_sel:[0,0,1]
	v_cvt_pk_fp8_f32 v6, v33, v37
	v_cvt_pk_fp8_f32 v6, v41, v45 op_sel:[0,0,1]
	v_cvt_pk_fp8_f32 v10, v34, v38
	v_cvt_pk_fp8_f32 v10, v42, v46 op_sel:[0,0,1]
	v_cvt_pk_fp8_f32 v14, v35, v39
	v_cvt_pk_fp8_f32 v14, v43, v47 op_sel:[0,0,1]
	v_cvt_pk_fp8_f32 v3, v48, v52
	v_cvt_pk_fp8_f32 v3, v56, v60 op_sel:[0,0,1]
	v_cvt_pk_fp8_f32 v7, v49, v53
	v_cvt_pk_fp8_f32 v7, v57, v61 op_sel:[0,0,1]
	v_cvt_pk_fp8_f32 v11, v50, v54
	v_cvt_pk_fp8_f32 v11, v58, v62 op_sel:[0,0,1]
	v_cvt_pk_fp8_f32 v15, v51, v55
	v_cvt_pk_fp8_f32 v15, v59, v63 op_sel:[0,0,1]
	global_store_dwordx4 v250, v[0:3], s[42:43] nt
	global_store_dwordx4 v250, v[4:7], s[42:43] offset:2048 nt
	global_store_dwordx4 v251, v[8:11], s[42:43] nt
	global_store_dwordx4 v251, v[12:15], s[42:43] offset:2048 nt
	s_add_u32 s42, s42, 0x800000
	s_addc_u32 s43, s43, 0
	global_load_dwordx4 v[0:3], v246, s[4:5] nt
	global_load_dwordx4 v[4:7], v247, s[4:5] nt
	global_load_dwordx4 v[8:11], v248, s[4:5] nt
	global_load_dwordx4 v[12:15], v249, s[4:5] nt
	global_load_dwordx4 v[16:19], v246, s[6:7] nt
	global_load_dwordx4 v[20:23], v247, s[6:7] nt
	global_load_dwordx4 v[24:27], v248, s[6:7] nt
	global_load_dwordx4 v[28:31], v249, s[6:7] nt
	global_load_dwordx4 v[32:35], v246, s[8:9] nt
	global_load_dwordx4 v[36:39], v247, s[8:9] nt
	global_load_dwordx4 v[40:43], v248, s[8:9] nt
	global_load_dwordx4 v[44:47], v249, s[8:9] nt
	global_load_dwordx4 v[48:51], v246, s[38:39] nt
	global_load_dwordx4 v[52:55], v247, s[38:39] nt
	global_load_dwordx4 v[56:59], v248, s[38:39] nt
	global_load_dwordx4 v[60:63], v249, s[38:39] nt
	s_add_u32 s4, s4, 0x2000000
	s_addc_u32 s5, s5, 0
	s_add_u32 s6, s6, 0x2000000
	s_addc_u32 s7, s7, 0
	s_add_u32 s8, s8, 0x2000000
	s_addc_u32 s9, s9, 0
	s_add_u32 s38, s38, 0x2000000
	s_addc_u32 s39, s39, 0
	s_waitcnt vmcnt(40)
; #define GAS __attribute__((address_space(1)))
; template <bool GAIN, bool NT = false> __device__ __forceinline__ void titem8_load(const TItem& d, int lane, f32x4 (&r)[16], f32x4 (&g)[4]) {
;     const int q = lane & 7, kg = lane >> 3; const unsigned lo = (unsigned)((16 * kg) * d.N + 4 * q) * 4u;
;     const GAS char* base = (const GAS char*)d.src;
; #pragma unroll
;     for (int j = 0; j < 16; ++j) { const GAS f32x4* p = (const GAS f32x4*)(base + (size_t)j * (size_t)d.N * 4 + lo); r[j] = NT ? __builtin_nontemporal_load(p) : *p; }
; template <bool GAIN, bool NT = false> __device__ __forceinline__ void titem8_store(const TItem& d, int lane, const f32x4 (&r)[16], const f32x4 (&g)[4]) {
;     const int q = lane & 7, kg = lane >> 3; const unsigned lo = (unsigned)((4 * q) * d.ldk + 16 * kg);
;     GAS char* base = (GAS char*)d.dst;
;     f32x4 s[16];
; #pragma unroll
;     for (int j = 0; j < 16; ++j) s[j] = r[j] * ((GAIN ? g[j >> 2][j & 3] : 1.0f) * W8_SCALE);
; #pragma unroll
;     for (int i = 0; i < 4; ++i) { v4u w;
;         w.x = pk4_fp8w(s[0][i], s[1][i], s[2][i], s[3][i]); w.y = pk4_fp8w(s[4][i], s[5][i], s[6][i], s[7][i]);
;         w.z = pk4_fp8w(s[8][i], s[9][i], s[10][i], s[11][i]); w.w = pk4_fp8w(s[12][i], s[13][i], s[14][i], s[15][i]);
;         GAS v4u* p = (GAS v4u*)(base + (size_t)i * (size_t)d.ldk + lo);
;         if (NT) __builtin_nontemporal_store(w, p); else *p = w; }
	v_pk_mul_f32 v[66:67], v[66:67], s[30:31] op_sel_hi:[1,0]
	v_pk_mul_f32 v[68:69], v[68:69], s[30:31] op_sel_hi:[1,0]
	v_pk_mul_f32 v[70:71], v[70:71], s[30:31] op_sel_hi:[1,0]
	v_pk_mul_f32 v[72:73], v[72:73], s[30:31] op_sel_hi:[1,0]
	v_pk_mul_f32 v[74:75], v[74:75], s[30:31] op_sel_hi:[1,0]
	v_pk_mul_f32 v[76:77], v[76:77], s[30:31] op_sel_hi:[1,0]
	v_pk_mul_f32 v[78:79], v[78:79], s[30:31] op_sel_hi:[1,0]
	v_pk_mul_f32 v[80:81], v[80:81], s[30:31] op_sel_hi:[1,0]
	v_pk_mul_f32 v[82:83], v[82:83], s[30:31] op_sel_hi:[1,0]
	v_pk_mul_f32 v[84:85], v[84:85], s[30:31] op_sel_hi:[1,0]
	v_pk_mul_f32 v[86:87], v[86:87], s[30:31] op_sel_hi:[1,0]
	v_pk_mul_f32 v[88:89], v[88:89], s[30:31] op_sel_hi:[1,0]
	v_pk_mul_f32 v[90:91], v[90:91], s[30:31] op_sel_hi:[1,0]
	v_pk_mul_f32 v[92:93], v[92:93], s[30:31] op_sel_hi:[1,0]
	v_pk_mul_f32 v[94:95], v[94:95], s[30:31] op_sel_hi:[1,0]
	v_pk_mul_f32 v[96:97], v[96:97], s[30:31] op_sel_hi:[1,0]
	v_pk_mul_f32 v[98:99], v[98:99], s[30:31] op_sel_hi:[1,0]
	v_pk_mul_f32 v[100:101], v[100:101], s[30:31] op_sel_hi:[1,0]
	v_pk_mul_f32 v[102:103], v[102:103], s[30:31] op_sel_hi:[1,0]
	v_pk_mul_f32 v[104:105], v[104:105], s[30:31] op_sel_hi:[1,0]
	v_pk_mul_f32 v[106:107], v[106:107], s[30:31] op_sel_hi:[1,0]
	v_pk_mul_f32 v[108:109], v[108:109], s[30:31] op_sel_hi:[1,0]
	v_pk_mul_f32 v[110:111], v[110:111], s[30:31] op_sel_hi:[1,0]
	v_pk_mul_f32 v[112:113], v[112:113], s[30:31] op_sel_hi:[1,0]
	v_pk_mul_f32 v[114:115], v[114:115], s[30:31] op_sel_hi:[1,0]
	v_pk_mul_f32 v[116:117], v[116:117], s[30:31] op_sel_hi:[1,0]
	v_pk_mul_f32 v[118:119], v[118:119], s[30:31] op_sel_hi:[1,0]
	v_pk_mul_f32 v[120:121], v[120:121], s[30:31] op_sel_hi:[1,0]
	v_pk_mul_f32 v[122:123], v[122:123], s[30:31] op_sel_hi:[1,0]
	v_pk_mul_f32 v[124:125], v[124:125], s[30:31] op_sel_hi:[1,0]
	v_pk_mul_f32 v[126:127], v[126:127], s[30:31] op_sel_hi:[1,0]
	v_pk_mul_f32 v[128:129], v[128:129], s[30:31] op_sel_hi:[1,0]
	v_med3_f32 v66, v66, s24, v237
	v_med3_f32 v67, v67, s24, v237
	v_med3_f32 v68, v68, s24, v237
	v_med3_f32 v69, v69, s24, v237
	v_med3_f32 v70, v70, s24, v237
	v_med3_f32 v71, v71, s24, v237
	v_med3_f32 v72, v72, s24, v237
	v_med3_f32 v73, v73, s24, v237
	v_med3_f32 v74, v74, s24, v237
	v_med3_f32 v75, v75, s24, v237
	v_med3_f32 v76, v76, s24, v237
	v_med3_f32 v77, v77, s24, v237
	v_med3_f32 v78, v78, s24, v237
	v_med3_f32 v79, v79, s24, v237
	v_med3_f32 v80, v80, s24, v237
	v_med3_f32 v81, v81, s24, v237
	v_med3_f32 v82, v82, s24, v237
	v_med3_f32 v83, v83, s24, v237
	v_med3_f32 v84, v84, s24, v237
	v_med3_f32 v85, v85, s24, v237
	v_med3_f32 v86, v86, s24, v237
	v_med3_f32 v87, v87, s24, v237
	v_med3_f32 v88, v88, s24, v237
	v_med3_f32 v89, v89, s24, v237
	v_med3_f32 v90, v90, s24, v237
	v_med3_f32 v91, v91, s24, v237
	v_med3_f32 v92, v92, s24, v237
	v_med3_f32 v93, v93, s24, v237
	v_med3_f32 v94, v94, s24, v237
	v_med3_f32 v95, v95, s24, v237
	v_med3_f32 v96, v96, s24, v237
	v_med3_f32 v97, v97, s24, v237
	v_med3_f32 v98, v98, s24, v237
	v_med3_f32 v99, v99, s24, v237
	v_med3_f32 v100, v100, s24, v237
	v_med3_f32 v101, v101, s24, v237
	v_med3_f32 v102, v102, s24, v237
	v_med3_f32 v103, v103, s24, v237
	v_med3_f32 v104, v104, s24, v237
	v_med3_f32 v105, v105, s24, v237
	v_med3_f32 v106, v106, s24, v237
	v_med3_f32 v107, v107, s24, v237
	v_med3_f32 v108, v108, s24, v237
	v_med3_f32 v109, v109, s24, v237
	v_med3_f32 v110, v110, s24, v237
	v_med3_f32 v111, v111, s24, v237
	v_med3_f32 v112, v112, s24, v237
	v_med3_f32 v113, v113, s24, v237
	v_med3_f32 v114, v114, s24, v237
	v_med3_f32 v115, v115, s24, v237
	v_med3_f32 v116, v116, s24, v237
	v_med3_f32 v117, v117, s24, v237
	v_med3_f32 v118, v118, s24, v237
	v_med3_f32 v119, v119, s24, v237
	v_med3_f32 v120, v120, s24, v237
	v_med3_f32 v121, v121, s24, v237
	v_med3_f32 v122, v122, s24, v237
	v_med3_f32 v123, v123, s24, v237
	v_med3_f32 v124, v124, s24, v237
	v_med3_f32 v125, v125, s24, v237
	v_med3_f32 v126, v126, s24, v237
	v_med3_f32 v127, v127, s24, v237
	v_med3_f32 v128, v128, s24, v237
	v_med3_f32 v129, v129, s24, v237
	v_cvt_pk_fp8_f32 v66, v66, v70
	v_cvt_pk_fp8_f32 v66, v74, v78 op_sel:[0,0,1]
	v_cvt_pk_fp8_f32 v70, v67, v71
	v_cvt_pk_fp8_f32 v70, v75, v79 op_sel:[0,0,1]
	v_cvt_pk_fp8_f32 v74, v68, v72
	v_cvt_pk_fp8_f32 v74, v76, v80 op_sel:[0,0,1]
	v_cvt_pk_fp8_f32 v78, v69, v73
	v_cvt_pk_fp8_f32 v78, v77, v81 op_sel:[0,0,1]
	v_cvt_pk_fp8_f32 v67, v82, v86
	v_cvt_pk_fp8_f32 v67, v90, v94 op_sel:[0,0,1]
	v_cvt_pk_fp8_f32 v71, v83, v87
	v_cvt_pk_fp8_f32 v71, v91, v95 op_sel:[0,0,1]
	v_cvt_pk_fp8_f32 v75, v84, v88
	v_cvt_pk_fp8_f32 v75, v92, v96 op_sel:[0,0,1]
	v_cvt_pk_fp8_f32 v79, v85, v89
	v_cvt_pk_fp8_f32 v79, v93, v97 op_sel:[0,0,1]
	v_cvt_pk_fp8_f32 v68, v98, v102
	v_cvt_pk_fp8_f32 v68, v106, v110 op_sel:[0,0,1]
	v_cvt_pk_fp8_f32 v72, v99, v103
	v_cvt_pk_fp8_f32 v72, v107, v111 op_sel:[0,0,1]
	v_cvt_pk_fp8_f32 v76, v100, v104
	v_cvt_pk_fp8_f32 v76, v108, v112 op_sel:[0,0,1]
	v_cvt_pk_fp8_f32 v80, v101, v105
	v_cvt_pk_fp8_f32 v80, v109, v113 op_sel:[0,0,1]
	v_cvt_pk_fp8_f32 v69, v114, v118
	v_cvt_pk_fp8_f32 v69, v122, v126 op_sel:[0,0,1]
	v_cvt_pk_fp8_f32 v73, v115, v119
	v_cvt_pk_fp8_f32 v73, v123, v127 op_sel:[0,0,1]
	v_cvt_pk_fp8_f32 v77, v116, v120
	v_cvt_pk_fp8_f32 v77, v124, v128 op_sel:[0,0,1]
	v_cvt_pk_fp8_f32 v81, v117, v121
	v_cvt_pk_fp8_f32 v81, v125, v129 op_sel:[0,0,1]
	global_store_dwordx4 v250, v[66:69], s[42:43] nt
	global_store_dwordx4 v250, v[70:73], s[42:43] offset:2048 nt
	global_store_dwordx4 v251, v[74:77], s[42:43] nt
	global_store_dwordx4 v251, v[78:81], s[42:43] offset:2048 nt
	s_add_u32 s42, s42, 0x800000
	s_addc_u32 s43, s43, 0
	global_load_dwordx4 v[66:69], v246, s[4:5] nt
	global_load_dwordx4 v[70:73], v247, s[4:5] nt
	global_load_dwordx4 v[74:77], v248, s[4:5] nt
	global_load_dwordx4 v[78:81], v249, s[4:5] nt
	global_load_dwordx4 v[82:85], v246, s[6:7] nt
	global_load_dwordx4 v[86:89], v247, s[6:7] nt
	global_load_dwordx4 v[90:93], v248, s[6:7] nt
	global_load_dwordx4 v[94:97], v249, s[6:7] nt
	global_load_dwordx4 v[98:101], v246, s[8:9] nt
	global_load_dwordx4 v[102:105], v247, s[8:9] nt
	global_load_dwordx4 v[106:109], v248, s[8:9] nt
	global_load_dwordx4 v[110:113], v249, s[8:9] nt
	global_load_dwordx4 v[114:117], v246, s[38:39] nt
	global_load_dwordx4 v[118:121], v247, s[38:39] nt
	global_load_dwordx4 v[122:125], v248, s[38:39] nt
	global_load_dwordx4 v[126:129], v249, s[38:39] nt
	s_add_u32 s4, s4, 0x2000000
	s_addc_u32 s5, s5, 0
	s_add_u32 s6, s6, 0x2000000
	s_addc_u32 s7, s7, 0
	s_add_u32 s8, s8, 0x2000000
	s_addc_u32 s9, s9, 0
	s_add_u32 s38, s38, 0x2000000
	s_addc_u32 s39, s39, 0
	s_waitcnt vmcnt(40)
; #define GAS __attribute__((address_space(1)))
; template <bool GAIN, bool NT = false> __device__ __forceinline__ void titem8_load(const TItem& d, int lane, f32x4 (&r)[16], f32x4 (&g)[4]) {
;     const int q = lane & 7, kg = lane >> 3; const unsigned lo = (unsigned)((16 * kg) * d.N + 4 * q) * 4u;
;     const GAS char* base = (const GAS char*)d.src;
; #pragma unroll
;     for (int j = 0; j < 16; ++j) { const GAS f32x4* p = (const GAS f32x4*)(base + (size_t)j * (size_t)d.N * 4 + lo); r[j] = NT ? __builtin_nontemporal_load(p) : *p; }
; template <bool GAIN, bool NT = false> __device__ __forceinline__ void titem8_store(const TItem& d, int lane, const f32x4 (&r)[16], const f32x4 (&g)[4]) {
;     const int q = lane & 7, kg = lane >> 3; const unsigned lo = (unsigned)((4 * q) * d.ldk + 16 * kg);
;     GAS char* base = (GAS char*)d.dst;
;     f32x4 s[16];
; #pragma unroll
;     for (int j = 0; j < 16; ++j) s[j] = r[j] * ((GAIN ? g[j >> 2][j & 3] : 1.0f) * W8_SCALE);
; #pragma unroll
;     for (int i = 0; i < 4; ++i) { v4u w;
;         w.x = pk4_fp8w(s[0][i], s[1][i], s[2][i], s[3][i]); w.y = pk4_fp8w(s[4][i], s[5][i], s[6][i], s[7][i]);
;         w.z = pk4_fp8w(s[8][i], s[9][i], s[10][i], s[11][i]); w.w = pk4_fp8w(s[12][i], s[13][i], s[14][i], s[15][i]);
;         GAS v4u* p = (GAS v4u*)(base + (size_t)i * (size_t)d.ldk + lo);
;         if (NT) __builtin_nontemporal_store(w, p); else *p = w; }
	v_pk_mul_f32 v[130:131], v[130:131], s[30:31] op_sel_hi:[1,0]
	v_pk_mul_f32 v[132:133], v[132:133], s[30:31] op_sel_hi:[1,0]
	v_pk_mul_f32 v[134:135], v[134:135], s[30:31] op_sel_hi:[1,0]
	v_pk_mul_f32 v[136:137], v[136:137], s[30:31] op_sel_hi:[1,0]
	v_pk_mul_f32 v[138:139], v[138:139], s[30:31] op_sel_hi:[1,0]
	v_pk_mul_f32 v[140:141], v[140:141], s[30:31] op_sel_hi:[1,0]
	v_pk_mul_f32 v[142:143], v[142:143], s[30:31] op_sel_hi:[1,0]
	v_pk_mul_f32 v[144:145], v[144:145], s[30:31] op_sel_hi:[1,0]
	v_pk_mul_f32 v[146:147], v[146:147], s[30:31] op_sel_hi:[1,0]
	v_pk_mul_f32 v[148:149], v[148:149], s[30:31] op_sel_hi:[1,0]
	v_pk_mul_f32 v[150:151], v[150:151], s[30:31] op_sel_hi:[1,0]
	v_pk_mul_f32 v[152:153], v[152:153], s[30:31] op_sel_hi:[1,0]
	v_pk_mul_f32 v[154:155], v[154:155], s[30:31] op_sel_hi:[1,0]
	v_pk_mul_f32 v[156:157], v[156:157], s[30:31] op_sel_hi:[1,0]
	v_pk_mul_f32 v[158:159], v[158:159], s[30:31] op_sel_hi:[1,0]
	v_pk_mul_f32 v[160:161], v[160:161], s[30:31] op_sel_hi:[1,0]
	v_pk_mul_f32 v[162:163], v[162:163], s[30:31] op_sel_hi:[1,0]
	v_pk_mul_f32 v[164:165], v[164:165], s[30:31] op_sel_hi:[1,0]
	v_pk_mul_f32 v[166:167], v[166:167], s[30:31] op_sel_hi:[1,0]
	v_pk_mul_f32 v[168:169], v[168:169], s[30:31] op_sel_hi:[1,0]
	v_pk_mul_f32 v[170:171], v[170:171], s[30:31] op_sel_hi:[1,0]
	v_pk_mul_f32 v[172:173], v[172:173], s[30:31] op_sel_hi:[1,0]
	v_pk_mul_f32 v[174:175], v[174:175], s[30:31] op_sel_hi:[1,0]
	v_pk_mul_f32 v[176:177], v[176:177], s[30:31] op_sel_hi:[1,0]
	v_pk_mul_f32 v[178:179], v[178:179], s[30:31] op_sel_hi:[1,0]
	v_pk_mul_f32 v[180:181], v[180:181], s[30:31] op_sel_hi:[1,0]
	v_pk_mul_f32 v[182:183], v[182:183], s[30:31] op_sel_hi:[1,0]
	v_pk_mul_f32 v[184:185], v[184:185], s[30:31] op_sel_hi:[1,0]
	v_pk_mul_f32 v[186:187], v[186:187], s[30:31] op_sel_hi:[1,0]
	v_pk_mul_f32 v[188:189], v[188:189], s[30:31] op_sel_hi:[1,0]
	v_pk_mul_f32 v[190:191], v[190:191], s[30:31] op_sel_hi:[1,0]
	v_pk_mul_f32 v[192:193], v[192:193], s[30:31] op_sel_hi:[1,0]
	v_med3_f32 v130, v130, s24, v237
	v_med3_f32 v131, v131, s24, v237
	v_med3_f32 v132, v132, s24, v237
	v_med3_f32 v133, v133, s24, v237
	v_med3_f32 v134, v134, s24, v237
	v_med3_f32 v135, v135, s24, v237
	v_med3_f32 v136, v136, s24, v237
	v_med3_f32 v137, v137, s24, v237
	v_med3_f32 v138, v138, s24, v237
	v_med3_f32 v139, v139, s24, v237
	v_med3_f32 v140, v140, s24, v237
	v_med3_f32 v141, v141, s24, v237
	v_med3_f32 v142, v142, s24, v237
	v_med3_f32 v143, v143, s24, v237
	v_med3_f32 v144, v144, s24, v237
	v_med3_f32 v145, v145, s24, v237
	v_med3_f32 v146, v146, s24, v237
	v_med3_f32 v147, v147, s24, v237
	v_med3_f32 v148, v148, s24, v237
	v_med3_f32 v149, v149, s24, v237
	v_med3_f32 v150, v150, s24, v237
	v_med3_f32 v151, v151, s24, v237
	v_med3_f32 v152, v152, s24, v237
	v_med3_f32 v153, v153, s24, v237
	v_med3_f32 v154, v154, s24, v237
	v_med3_f32 v155, v155, s24, v237
	v_med3_f32 v156, v156, s24, v237
	v_med3_f32 v157, v157, s24, v237
	v_med3_f32 v158, v158, s24, v237
	v_med3_f32 v159, v159, s24, v237
	v_med3_f32 v160, v160, s24, v237
	v_med3_f32 v161, v161, s24, v237
	v_med3_f32 v162, v162, s24, v237
	v_med3_f32 v163, v163, s24, v237
	v_med3_f32 v164, v164, s24, v237
	v_med3_f32 v165, v165, s24, v237
	v_med3_f32 v166, v166, s24, v237
	v_med3_f32 v167, v167, s24, v237
	v_med3_f32 v168, v168, s24, v237
	v_med3_f32 v169, v169, s24, v237
	v_med3_f32 v170, v170, s24, v237
	v_med3_f32 v171, v171, s24, v237
	v_med3_f32 v172, v172, s24, v237
	v_med3_f32 v173, v173, s24, v237
	v_med3_f32 v174, v174, s24, v237
	v_med3_f32 v175, v175, s24, v237
	v_med3_f32 v176, v176, s24, v237
	v_med3_f32 v177, v177, s24, v237
	v_med3_f32 v178, v178, s24, v237
	v_med3_f32 v179, v179, s24, v237
	v_med3_f32 v180, v180, s24, v237
	v_med3_f32 v181, v181, s24, v237
	v_med3_f32 v182, v182, s24, v237
	v_med3_f32 v183, v183, s24, v237
	v_med3_f32 v184, v184, s24, v237
	v_med3_f32 v185, v185, s24, v237
	v_med3_f32 v186, v186, s24, v237
	v_med3_f32 v187, v187, s24, v237
	v_med3_f32 v188, v188, s24, v237
	v_med3_f32 v189, v189, s24, v237
	v_med3_f32 v190, v190, s24, v237
	v_med3_f32 v191, v191, s24, v237
	v_med3_f32 v192, v192, s24, v237
	v_med3_f32 v193, v193, s24, v237
	v_cvt_pk_fp8_f32 v130, v130, v134
	v_cvt_pk_fp8_f32 v130, v138, v142 op_sel:[0,0,1]
	v_cvt_pk_fp8_f32 v134, v131, v135
	v_cvt_pk_fp8_f32 v134, v139, v143 op_sel:[0,0,1]
	v_cvt_pk_fp8_f32 v138, v132, v136
	v_cvt_pk_fp8_f32 v138, v140, v144 op_sel:[0,0,1]
	v_cvt_pk_fp8_f32 v142, v133, v137
	v_cvt_pk_fp8_f32 v142, v141, v145 op_sel:[0,0,1]
	v_cvt_pk_fp8_f32 v131, v146, v150
	v_cvt_pk_fp8_f32 v131, v154, v158 op_sel:[0,0,1]
	v_cvt_pk_fp8_f32 v135, v147, v151
	v_cvt_pk_fp8_f32 v135, v155, v159 op_sel:[0,0,1]
	v_cvt_pk_fp8_f32 v139, v148, v152
	v_cvt_pk_fp8_f32 v139, v156, v160 op_sel:[0,0,1]
	v_cvt_pk_fp8_f32 v143, v149, v153
	v_cvt_pk_fp8_f32 v143, v157, v161 op_sel:[0,0,1]
	v_cvt_pk_fp8_f32 v132, v162, v166
	v_cvt_pk_fp8_f32 v132, v170, v174 op_sel:[0,0,1]
	v_cvt_pk_fp8_f32 v136, v163, v167
	v_cvt_pk_fp8_f32 v136, v171, v175 op_sel:[0,0,1]
	v_cvt_pk_fp8_f32 v140, v164, v168
	v_cvt_pk_fp8_f32 v140, v172, v176 op_sel:[0,0,1]
	v_cvt_pk_fp8_f32 v144, v165, v169
	v_cvt_pk_fp8_f32 v144, v173, v177 op_sel:[0,0,1]
	v_cvt_pk_fp8_f32 v133, v178, v182
	v_cvt_pk_fp8_f32 v133, v186, v190 op_sel:[0,0,1]
	v_cvt_pk_fp8_f32 v137, v179, v183
	v_cvt_pk_fp8_f32 v137, v187, v191 op_sel:[0,0,1]
	v_cvt_pk_fp8_f32 v141, v180, v184
	v_cvt_pk_fp8_f32 v141, v188, v192 op_sel:[0,0,1]
	v_cvt_pk_fp8_f32 v145, v181, v185
	v_cvt_pk_fp8_f32 v145, v189, v193 op_sel:[0,0,1]
	global_store_dwordx4 v250, v[130:133], s[42:43] nt
	global_store_dwordx4 v250, v[134:137], s[42:43] offset:2048 nt
	global_store_dwordx4 v251, v[138:141], s[42:43] nt
	global_store_dwordx4 v251, v[142:145], s[42:43] offset:2048 nt
	s_add_u32 s42, s42, 0x800000
	s_addc_u32 s43, s43, 0
	global_load_dwordx4 v[130:133], v246, s[4:5] nt
	global_load_dwordx4 v[134:137], v247, s[4:5] nt
	global_load_dwordx4 v[138:141], v248, s[4:5] nt
	global_load_dwordx4 v[142:145], v249, s[4:5] nt
	global_load_dwordx4 v[146:149], v246, s[6:7] nt
	global_load_dwordx4 v[150:153], v247, s[6:7] nt
	global_load_dwordx4 v[154:157], v248, s[6:7] nt
	global_load_dwordx4 v[158:161], v249, s[6:7] nt
	global_load_dwordx4 v[162:165], v246, s[8:9] nt
	global_load_dwordx4 v[166:169], v247, s[8:9] nt
	global_load_dwordx4 v[170:173], v248, s[8:9] nt
	global_load_dwordx4 v[174:177], v249, s[8:9] nt
	global_load_dwordx4 v[178:181], v246, s[38:39] nt
	global_load_dwordx4 v[182:185], v247, s[38:39] nt
	global_load_dwordx4 v[186:189], v248, s[38:39] nt
	global_load_dwordx4 v[190:193], v249, s[38:39] nt
	s_add_u32 s4, s4, 0x2000000
	s_addc_u32 s5, s5, 0
	s_add_u32 s6, s6, 0x2000000
	s_addc_u32 s7, s7, 0
	s_add_u32 s8, s8, 0x2000000
	s_addc_u32 s9, s9, 0
	s_add_u32 s38, s38, 0x2000000
	s_addc_u32 s39, s39, 0
	s_waitcnt vmcnt(40)
; #define GAS __attribute__((address_space(1)))
; template <bool GAIN, bool NT = false> __device__ __forceinline__ void titem8_load(const TItem& d, int lane, f32x4 (&r)[16], f32x4 (&g)[4]) {
;     const int q = lane & 7, kg = lane >> 3; const unsigned lo = (unsigned)((16 * kg) * d.N + 4 * q) * 4u;
;     const GAS char* base = (const GAS char*)d.src;
; #pragma unroll
;     for (int j = 0; j < 16; ++j) { const GAS f32x4* p = (const GAS f32x4*)(base + (size_t)j * (size_t)d.N * 4 + lo); r[j] = NT ? __builtin_nontemporal_load(p) : *p; }
; template <bool GAIN, bool NT = false> __device__ __forceinline__ void titem8_store(const TItem& d, int lane, const f32x4 (&r)[16], const f32x4 (&g)[4]) {
;     const int q = lane & 7, kg = lane >> 3; const unsigned lo = (unsigned)((4 * q) * d.ldk + 16 * kg);
;     GAS char* base = (GAS char*)d.dst;
;     f32x4 s[16];
; #pragma unroll
;     for (int j = 0; j < 16; ++j) s[j] = r[j] * ((GAIN ? g[j >> 2][j & 3] : 1.0f) * W8_SCALE);
; #pragma unroll
;     for (int i = 0; i < 4; ++i) { v4u w;
;         w.x = pk4_fp8w(s[0][i], s[1][i], s[2][i], s[3][i]); w.y = pk4_fp8w(s[4][i], s[5][i], s[6][i], s[7][i]);
;         w.z = pk4_fp8w(s[8][i], s[9][i], s[10][i], s[11][i]); w.w = pk4_fp8w(s[12][i], s[13][i], s[14][i], s[15][i]);
;         GAS v4u* p = (GAS v4u*)(base + (size_t)i * (size_t)d.ldk + lo);
;         if (NT) __builtin_nontemporal_store(w, p); else *p = w; }
	v_pk_mul_f32 v[0:1], v[0:1], s[30:31] op_sel_hi:[1,0]
	v_pk_mul_f32 v[2:3], v[2:3], s[30:31] op_sel_hi:[1,0]
	v_pk_mul_f32 v[4:5], v[4:5], s[30:31] op_sel_hi:[1,0]
	v_pk_mul_f32 v[6:7], v[6:7], s[30:31] op_sel_hi:[1,0]
	v_pk_mul_f32 v[8:9], v[8:9], s[30:31] op_sel_hi:[1,0]
	v_pk_mul_f32 v[10:11], v[10:11], s[30:31] op_sel_hi:[1,0]
	v_pk_mul_f32 v[12:13], v[12:13], s[30:31] op_sel_hi:[1,0]
	v_pk_mul_f32 v[14:15], v[14:15], s[30:31] op_sel_hi:[1,0]
	v_pk_mul_f32 v[16:17], v[16:17], s[30:31] op_sel_hi:[1,0]
	v_pk_mul_f32 v[18:19], v[18:19], s[30:31] op_sel_hi:[1,0]
	v_pk_mul_f32 v[20:21], v[20:21], s[30:31] op_sel_hi:[1,0]
	v_pk_mul_f32 v[22:23], v[22:23], s[30:31] op_sel_hi:[1,0]
	v_pk_mul_f32 v[24:25], v[24:25], s[30:31] op_sel_hi:[1,0]
	v_pk_mul_f32 v[26:27], v[26:27], s[30:31] op_sel_hi:[1,0]
	v_pk_mul_f32 v[28:29], v[28:29], s[30:31] op_sel_hi:[1,0]
	v_pk_mul_f32 v[30:31], v[30:31], s[30:31] op_sel_hi:[1,0]
	v_pk_mul_f32 v[32:33], v[32:33], s[30:31] op_sel_hi:[1,0]
	v_pk_mul_f32 v[34:35], v[34:35], s[30:31] op_sel_hi:[1,0]
	v_pk_mul_f32 v[36:37], v[36:37], s[30:31] op_sel_hi:[1,0]
	v_pk_mul_f32 v[38:39], v[38:39], s[30:31] op_sel_hi:[1,0]
	v_pk_mul_f32 v[40:41], v[40:41], s[30:31] op_sel_hi:[1,0]
	v_pk_mul_f32 v[42:43], v[42:43], s[30:31] op_sel_hi:[1,0]
	v_pk_mul_f32 v[44:45], v[44:45], s[30:31] op_sel_hi:[1,0]
	v_pk_mul_f32 v[46:47], v[46:47], s[30:31] op_sel_hi:[1,0]
	v_pk_mul_f32 v[48:49], v[48:49], s[30:31] op_sel_hi:[1,0]
	v_pk_mul_f32 v[50:51], v[50:51], s[30:31] op_sel_hi:[1,0]
	v_pk_mul_f32 v[52:53], v[52:53], s[30:31] op_sel_hi:[1,0]
	v_pk_mul_f32 v[54:55], v[54:55], s[30:31] op_sel_hi:[1,0]
	v_pk_mul_f32 v[56:57], v[56:57], s[30:31] op_sel_hi:[1,0]
	v_pk_mul_f32 v[58:59], v[58:59], s[30:31] op_sel_hi:[1,0]
	v_pk_mul_f32 v[60:61], v[60:61], s[30:31] op_sel_hi:[1,0]
	v_pk_mul_f32 v[62:63], v[62:63], s[30:31] op_sel_hi:[1,0]
	v_med3_f32 v0, v0, s24, v237
	v_med3_f32 v1, v1, s24, v237
	v_med3_f32 v2, v2, s24, v237
	v_med3_f32 v3, v3, s24, v237
	v_med3_f32 v4, v4, s24, v237
	v_med3_f32 v5, v5, s24, v237
	v_med3_f32 v6, v6, s24, v237
	v_med3_f32 v7, v7, s24, v237
	v_med3_f32 v8, v8, s24, v237
	v_med3_f32 v9, v9, s24, v237
	v_med3_f32 v10, v10, s24, v237
	v_med3_f32 v11, v11, s24, v237
	v_med3_f32 v12, v12, s24, v237
	v_med3_f32 v13, v13, s24, v237
	v_med3_f32 v14, v14, s24, v237
	v_med3_f32 v15, v15, s24, v237
	v_med3_f32 v16, v16, s24, v237
	v_med3_f32 v17, v17, s24, v237
	v_med3_f32 v18, v18, s24, v237
	v_med3_f32 v19, v19, s24, v237
	v_med3_f32 v20, v20, s24, v237
	v_med3_f32 v21, v21, s24, v237
	v_med3_f32 v22, v22, s24, v237
	v_med3_f32 v23, v23, s24, v237
	v_med3_f32 v24, v24, s24, v237
	v_med3_f32 v25, v25, s24, v237
	v_med3_f32 v26, v26, s24, v237
	v_med3_f32 v27, v27, s24, v237
	v_med3_f32 v28, v28, s24, v237
	v_med3_f32 v29, v29, s24, v237
	v_med3_f32 v30, v30, s24, v237
	v_med3_f32 v31, v31, s24, v237
	v_med3_f32 v32, v32, s24, v237
	v_med3_f32 v33, v33, s24, v237
	v_med3_f32 v34, v34, s24, v237
	v_med3_f32 v35, v35, s24, v237
	v_med3_f32 v36, v36, s24, v237
	v_med3_f32 v37, v37, s24, v237
	v_med3_f32 v38, v38, s24, v237
	v_med3_f32 v39, v39, s24, v237
	v_med3_f32 v40, v40, s24, v237
	v_med3_f32 v41, v41, s24, v237
	v_med3_f32 v42, v42, s24, v237
	v_med3_f32 v43, v43, s24, v237
	v_med3_f32 v44, v44, s24, v237
	v_med3_f32 v45, v45, s24, v237
	v_med3_f32 v46, v46, s24, v237
	v_med3_f32 v47, v47, s24, v237
	v_med3_f32 v48, v48, s24, v237
	v_med3_f32 v49, v49, s24, v237
	v_med3_f32 v50, v50, s24, v237
	v_med3_f32 v51, v51, s24, v237
	v_med3_f32 v52, v52, s24, v237
	v_med3_f32 v53, v53, s24, v237
	v_med3_f32 v54, v54, s24, v237
	v_med3_f32 v55, v55, s24, v237
	v_med3_f32 v56, v56, s24, v237
	v_med3_f32 v57, v57, s24, v237
	v_med3_f32 v58, v58, s24, v237
	v_med3_f32 v59, v59, s24, v237
	v_med3_f32 v60, v60, s24, v237
	v_med3_f32 v61, v61, s24, v237
	v_med3_f32 v62, v62, s24, v237
	v_med3_f32 v63, v63, s24, v237
	v_cvt_pk_fp8_f32 v0, v0, v4
	v_cvt_pk_fp8_f32 v0, v8, v12 op_sel:[0,0,1]
	v_cvt_pk_fp8_f32 v4, v1, v5
	v_cvt_pk_fp8_f32 v4, v9, v13 op_sel:[0,0,1]
	v_cvt_pk_fp8_f32 v8, v2, v6
	v_cvt_pk_fp8_f32 v8, v10, v14 op_sel:[0,0,1]
	v_cvt_pk_fp8_f32 v12, v3, v7
	v_cvt_pk_fp8_f32 v12, v11, v15 op_sel:[0,0,1]
	v_cvt_pk_fp8_f32 v1, v16, v20
	v_cvt_pk_fp8_f32 v1, v24, v28 op_sel:[0,0,1]
	v_cvt_pk_fp8_f32 v5, v17, v21
	v_cvt_pk_fp8_f32 v5, v25, v29 op_sel:[0,0,1]
	v_cvt_pk_fp8_f32 v9, v18, v22
	v_cvt_pk_fp8_f32 v9, v26, v30 op_sel:[0,0,1]
	v_cvt_pk_fp8_f32 v13, v19, v23
	v_cvt_pk_fp8_f32 v13, v27, v31 op_sel:[0,0,1]
	v_cvt_pk_fp8_f32 v2, v32, v36
	v_cvt_pk_fp8_f32 v2, v40, v44 op_sel:[0,0,1]
	v_cvt_pk_fp8_f32 v6, v33, v37
	v_cvt_pk_fp8_f32 v6, v41, v45 op_sel:[0,0,1]
	v_cvt_pk_fp8_f32 v10, v34, v38
	v_cvt_pk_fp8_f32 v10, v42, v46 op_sel:[0,0,1]
	v_cvt_pk_fp8_f32 v14, v35, v39
	v_cvt_pk_fp8_f32 v14, v43, v47 op_sel:[0,0,1]
	v_cvt_pk_fp8_f32 v3, v48, v52
	v_cvt_pk_fp8_f32 v3, v56, v60 op_sel:[0,0,1]
	v_cvt_pk_fp8_f32 v7, v49, v53
	v_cvt_pk_fp8_f32 v7, v57, v61 op_sel:[0,0,1]
	v_cvt_pk_fp8_f32 v11, v50, v54
	v_cvt_pk_fp8_f32 v11, v58, v62 op_sel:[0,0,1]
	v_cvt_pk_fp8_f32 v15, v51, v55
	v_cvt_pk_fp8_f32 v15, v59, v63 op_sel:[0,0,1]
	global_store_dwordx4 v250, v[0:3], s[42:43] nt
	global_store_dwordx4 v250, v[4:7], s[42:43] offset:2048 nt
	global_store_dwordx4 v251, v[8:11], s[42:43] nt
	global_store_dwordx4 v251, v[12:15], s[42:43] offset:2048 nt
	s_add_u32 s42, s42, 0x800000
	s_addc_u32 s43, s43, 0
	global_load_dwordx4 v[0:3], v246, s[4:5] nt
	global_load_dwordx4 v[4:7], v247, s[4:5] nt
	global_load_dwordx4 v[8:11], v248, s[4:5] nt
	global_load_dwordx4 v[12:15], v249, s[4:5] nt
	global_load_dwordx4 v[16:19], v246, s[6:7] nt
	global_load_dwordx4 v[20:23], v247, s[6:7] nt
	global_load_dwordx4 v[24:27], v248, s[6:7] nt
	global_load_dwordx4 v[28:31], v249, s[6:7] nt
	global_load_dwordx4 v[32:35], v246, s[8:9] nt
	global_load_dwordx4 v[36:39], v247, s[8:9] nt
	global_load_dwordx4 v[40:43], v248, s[8:9] nt
	global_load_dwordx4 v[44:47], v249, s[8:9] nt
	global_load_dwordx4 v[48:51], v246, s[38:39] nt
	global_load_dwordx4 v[52:55], v247, s[38:39] nt
	global_load_dwordx4 v[56:59], v248, s[38:39] nt
	global_load_dwordx4 v[60:63], v249, s[38:39] nt
	s_add_u32 s4, s4, 0x2000000
	s_addc_u32 s5, s5, 0
	s_add_u32 s6, s6, 0x2000000
	s_addc_u32 s7, s7, 0
	s_add_u32 s8, s8, 0x2000000
	s_addc_u32 s9, s9, 0
	s_add_u32 s38, s38, 0x2000000
	s_addc_u32 s39, s39, 0
	s_waitcnt vmcnt(40)
; #define GAS __attribute__((address_space(1)))
; template <bool GAIN, bool NT = false> __device__ __forceinline__ void titem8_load(const TItem& d, int lane, f32x4 (&r)[16], f32x4 (&g)[4]) {
;     const int q = lane & 7, kg = lane >> 3; const unsigned lo = (unsigned)((16 * kg) * d.N + 4 * q) * 4u;
;     const GAS char* base = (const GAS char*)d.src;
; #pragma unroll
;     for (int j = 0; j < 16; ++j) { const GAS f32x4* p = (const GAS f32x4*)(base + (size_t)j * (size_t)d.N * 4 + lo); r[j] = NT ? __builtin_nontemporal_load(p) : *p; }
; template <bool GAIN, bool NT = false> __device__ __forceinline__ void titem8_store(const TItem& d, int lane, const f32x4 (&r)[16], const f32x4 (&g)[4]) {
;     const int q = lane & 7, kg = lane >> 3; const unsigned lo = (unsigned)((4 * q) * d.ldk + 16 * kg);
;     GAS char* base = (GAS char*)d.dst;
;     f32x4 s[16];
; #pragma unroll
;     for (int j = 0; j < 16; ++j) s[j] = r[j] * ((GAIN ? g[j >> 2][j & 3] : 1.0f) * W8_SCALE);
; #pragma unroll
;     for (int i = 0; i < 4; ++i) { v4u w;
;         w.x = pk4_fp8w(s[0][i], s[1][i], s[2][i], s[3][i]); w.y = pk4_fp8w(s[4][i], s[5][i], s[6][i], s[7][i]);
;         w.z = pk4_fp8w(s[8][i], s[9][i], s[10][i], s[11][i]); w.w = pk4_fp8w(s[12][i], s[13][i], s[14][i], s[15][i]);
;         GAS v4u* p = (GAS v4u*)(base + (size_t)i * (size_t)d.ldk + lo);
;         if (NT) __builtin_nontemporal_store(w, p); else *p = w; }
	v_pk_mul_f32 v[66:67], v[66:67], s[30:31] op_sel_hi:[1,0]
	v_pk_mul_f32 v[68:69], v[68:69], s[30:31] op_sel_hi:[1,0]
	v_pk_mul_f32 v[70:71], v[70:71], s[30:31] op_sel_hi:[1,0]
	v_pk_mul_f32 v[72:73], v[72:73], s[30:31] op_sel_hi:[1,0]
	v_pk_mul_f32 v[74:75], v[74:75], s[30:31] op_sel_hi:[1,0]
	v_pk_mul_f32 v[76:77], v[76:77], s[30:31] op_sel_hi:[1,0]
	v_pk_mul_f32 v[78:79], v[78:79], s[30:31] op_sel_hi:[1,0]
	v_pk_mul_f32 v[80:81], v[80:81], s[30:31] op_sel_hi:[1,0]
	v_pk_mul_f32 v[82:83], v[82:83], s[30:31] op_sel_hi:[1,0]
	v_pk_mul_f32 v[84:85], v[84:85], s[30:31] op_sel_hi:[1,0]
	v_pk_mul_f32 v[86:87], v[86:87], s[30:31] op_sel_hi:[1,0]
	v_pk_mul_f32 v[88:89], v[88:89], s[30:31] op_sel_hi:[1,0]
	v_pk_mul_f32 v[90:91], v[90:91], s[30:31] op_sel_hi:[1,0]
	v_pk_mul_f32 v[92:93], v[92:93], s[30:31] op_sel_hi:[1,0]
	v_pk_mul_f32 v[94:95], v[94:95], s[30:31] op_sel_hi:[1,0]
	v_pk_mul_f32 v[96:97], v[96:97], s[30:31] op_sel_hi:[1,0]
	v_pk_mul_f32 v[98:99], v[98:99], s[30:31] op_sel_hi:[1,0]
	v_pk_mul_f32 v[100:101], v[100:101], s[30:31] op_sel_hi:[1,0]
	v_pk_mul_f32 v[102:103], v[102:103], s[30:31] op_sel_hi:[1,0]
	v_pk_mul_f32 v[104:105], v[104:105], s[30:31] op_sel_hi:[1,0]
	v_pk_mul_f32 v[106:107], v[106:107], s[30:31] op_sel_hi:[1,0]
	v_pk_mul_f32 v[108:109], v[108:109], s[30:31] op_sel_hi:[1,0]
	v_pk_mul_f32 v[110:111], v[110:111], s[30:31] op_sel_hi:[1,0]
	v_pk_mul_f32 v[112:113], v[112:113], s[30:31] op_sel_hi:[1,0]
	v_pk_mul_f32 v[114:115], v[114:115], s[30:31] op_sel_hi:[1,0]
	v_pk_mul_f32 v[116:117], v[116:117], s[30:31] op_sel_hi:[1,0]
	v_pk_mul_f32 v[118:119], v[118:119], s[30:31] op_sel_hi:[1,0]
	v_pk_mul_f32 v[120:121], v[120:121], s[30:31] op_sel_hi:[1,0]
	v_pk_mul_f32 v[122:123], v[122:123], s[30:31] op_sel_hi:[1,0]
	v_pk_mul_f32 v[124:125], v[124:125], s[30:31] op_sel_hi:[1,0]
	v_pk_mul_f32 v[126:127], v[126:127], s[30:31] op_sel_hi:[1,0]
	v_pk_mul_f32 v[128:129], v[128:129], s[30:31] op_sel_hi:[1,0]
	v_med3_f32 v66, v66, s24, v237
	v_med3_f32 v67, v67, s24, v237
	v_med3_f32 v68, v68, s24, v237
	v_med3_f32 v69, v69, s24, v237
	v_med3_f32 v70, v70, s24, v237
	v_med3_f32 v71, v71, s24, v237
	v_med3_f32 v72, v72, s24, v237
	v_med3_f32 v73, v73, s24, v237
	v_med3_f32 v74, v74, s24, v237
	v_med3_f32 v75, v75, s24, v237
	v_med3_f32 v76, v76, s24, v237
	v_med3_f32 v77, v77, s24, v237
	v_med3_f32 v78, v78, s24, v237
	v_med3_f32 v79, v79, s24, v237
	v_med3_f32 v80, v80, s24, v237
	v_med3_f32 v81, v81, s24, v237
	v_med3_f32 v82, v82, s24, v237
	v_med3_f32 v83, v83, s24, v237
	v_med3_f32 v84, v84, s24, v237
	v_med3_f32 v85, v85, s24, v237
	v_med3_f32 v86, v86, s24, v237
	v_med3_f32 v87, v87, s24, v237
	v_med3_f32 v88, v88, s24, v237
	v_med3_f32 v89, v89, s24, v237
	v_med3_f32 v90, v90, s24, v237
	v_med3_f32 v91, v91, s24, v237
	v_med3_f32 v92, v92, s24, v237
	v_med3_f32 v93, v93, s24, v237
	v_med3_f32 v94, v94, s24, v237
	v_med3_f32 v95, v95, s24, v237
	v_med3_f32 v96, v96, s24, v237
	v_med3_f32 v97, v97, s24, v237
	v_med3_f32 v98, v98, s24, v237
	v_med3_f32 v99, v99, s24, v237
	v_med3_f32 v100, v100, s24, v237
	v_med3_f32 v101, v101, s24, v237
	v_med3_f32 v102, v102, s24, v237
	v_med3_f32 v103, v103, s24, v237
	v_med3_f32 v104, v104, s24, v237
	v_med3_f32 v105, v105, s24, v237
	v_med3_f32 v106, v106, s24, v237
	v_med3_f32 v107, v107, s24, v237
	v_med3_f32 v108, v108, s24, v237
	v_med3_f32 v109, v109, s24, v237
	v_med3_f32 v110, v110, s24, v237
	v_med3_f32 v111, v111, s24, v237
	v_med3_f32 v112, v112, s24, v237
	v_med3_f32 v113, v113, s24, v237
	v_med3_f32 v114, v114, s24, v237
	v_med3_f32 v115, v115, s24, v237
	v_med3_f32 v116, v116, s24, v237
	v_med3_f32 v117, v117, s24, v237
	v_med3_f32 v118, v118, s24, v237
	v_med3_f32 v119, v119, s24, v237
	v_med3_f32 v120, v120, s24, v237
	v_med3_f32 v121, v121, s24, v237
	v_med3_f32 v122, v122, s24, v237
	v_med3_f32 v123, v123, s24, v237
	v_med3_f32 v124, v124, s24, v237
	v_med3_f32 v125, v125, s24, v237
	v_med3_f32 v126, v126, s24, v237
	v_med3_f32 v127, v127, s24, v237
	v_med3_f32 v128, v128, s24, v237
	v_med3_f32 v129, v129, s24, v237
	v_cvt_pk_fp8_f32 v66, v66, v70
	v_cvt_pk_fp8_f32 v66, v74, v78 op_sel:[0,0,1]
	v_cvt_pk_fp8_f32 v70, v67, v71
	v_cvt_pk_fp8_f32 v70, v75, v79 op_sel:[0,0,1]
	v_cvt_pk_fp8_f32 v74, v68, v72
	v_cvt_pk_fp8_f32 v74, v76, v80 op_sel:[0,0,1]
	v_cvt_pk_fp8_f32 v78, v69, v73
	v_cvt_pk_fp8_f32 v78, v77, v81 op_sel:[0,0,1]
	v_cvt_pk_fp8_f32 v67, v82, v86
	v_cvt_pk_fp8_f32 v67, v90, v94 op_sel:[0,0,1]
	v_cvt_pk_fp8_f32 v71, v83, v87
	v_cvt_pk_fp8_f32 v71, v91, v95 op_sel:[0,0,1]
	v_cvt_pk_fp8_f32 v75, v84, v88
	v_cvt_pk_fp8_f32 v75, v92, v96 op_sel:[0,0,1]
	v_cvt_pk_fp8_f32 v79, v85, v89
	v_cvt_pk_fp8_f32 v79, v93, v97 op_sel:[0,0,1]
	v_cvt_pk_fp8_f32 v68, v98, v102
	v_cvt_pk_fp8_f32 v68, v106, v110 op_sel:[0,0,1]
	v_cvt_pk_fp8_f32 v72, v99, v103
	v_cvt_pk_fp8_f32 v72, v107, v111 op_sel:[0,0,1]
	v_cvt_pk_fp8_f32 v76, v100, v104
	v_cvt_pk_fp8_f32 v76, v108, v112 op_sel:[0,0,1]
	v_cvt_pk_fp8_f32 v80, v101, v105
	v_cvt_pk_fp8_f32 v80, v109, v113 op_sel:[0,0,1]
	v_cvt_pk_fp8_f32 v69, v114, v118
	v_cvt_pk_fp8_f32 v69, v122, v126 op_sel:[0,0,1]
	v_cvt_pk_fp8_f32 v73, v115, v119
	v_cvt_pk_fp8_f32 v73, v123, v127 op_sel:[0,0,1]
	v_cvt_pk_fp8_f32 v77, v116, v120
	v_cvt_pk_fp8_f32 v77, v124, v128 op_sel:[0,0,1]
	v_cvt_pk_fp8_f32 v81, v117, v121
	v_cvt_pk_fp8_f32 v81, v125, v129 op_sel:[0,0,1]
	global_store_dwordx4 v250, v[66:69], s[42:43] nt
	global_store_dwordx4 v250, v[70:73], s[42:43] offset:2048 nt
	global_store_dwordx4 v251, v[74:77], s[42:43] nt
	global_store_dwordx4 v251, v[78:81], s[42:43] offset:2048 nt
	s_add_u32 s42, s42, 0x800000
	s_addc_u32 s43, s43, 0
	global_load_dwordx4 v[66:69], v246, s[4:5] nt
	global_load_dwordx4 v[70:73], v247, s[4:5] nt
	global_load_dwordx4 v[74:77], v248, s[4:5] nt
	global_load_dwordx4 v[78:81], v249, s[4:5] nt
	global_load_dwordx4 v[82:85], v246, s[6:7] nt
	global_load_dwordx4 v[86:89], v247, s[6:7] nt
	global_load_dwordx4 v[90:93], v248, s[6:7] nt
	global_load_dwordx4 v[94:97], v249, s[6:7] nt
	global_load_dwordx4 v[98:101], v246, s[8:9] nt
	global_load_dwordx4 v[102:105], v247, s[8:9] nt
	global_load_dwordx4 v[106:109], v248, s[8:9] nt
	global_load_dwordx4 v[110:113], v249, s[8:9] nt
	global_load_dwordx4 v[114:117], v246, s[38:39] nt
	global_load_dwordx4 v[118:121], v247, s[38:39] nt
	global_load_dwordx4 v[122:125], v248, s[38:39] nt
	global_load_dwordx4 v[126:129], v249, s[38:39] nt
	s_add_u32 s4, s4, 0x2000000
	s_addc_u32 s5, s5, 0
	s_add_u32 s6, s6, 0x2000000
	s_addc_u32 s7, s7, 0
	s_add_u32 s8, s8, 0x2000000
	s_addc_u32 s9, s9, 0
	s_add_u32 s38, s38, 0x2000000
	s_addc_u32 s39, s39, 0
	s_waitcnt vmcnt(40)
; #define GAS __attribute__((address_space(1)))
; template <bool GAIN, bool NT = false> __device__ __forceinline__ void titem8_load(const TItem& d, int lane, f32x4 (&r)[16], f32x4 (&g)[4]) {
;     const int q = lane & 7, kg = lane >> 3; const unsigned lo = (unsigned)((16 * kg) * d.N + 4 * q) * 4u;
;     const GAS char* base = (const GAS char*)d.src;
; #pragma unroll
;     for (int j = 0; j < 16; ++j) { const GAS f32x4* p = (const GAS f32x4*)(base + (size_t)j * (size_t)d.N * 4 + lo); r[j] = NT ? __builtin_nontemporal_load(p) : *p; }
; template <bool GAIN, bool NT = false> __device__ __forceinline__ void titem8_store(const TItem& d, int lane, const f32x4 (&r)[16], const f32x4 (&g)[4]) {
;     const int q = lane & 7, kg = lane >> 3; const unsigned lo = (unsigned)((4 * q) * d.ldk + 16 * kg);
;     GAS char* base = (GAS char*)d.dst;
;     f32x4 s[16];
; #pragma unroll
;     for (int j = 0; j < 16; ++j) s[j] = r[j] * ((GAIN ? g[j >> 2][j & 3] : 1.0f) * W8_SCALE);
; #pragma unroll
;     for (int i = 0; i < 4; ++i) { v4u w;
;         w.x = pk4_fp8w(s[0][i], s[1][i], s[2][i], s[3][i]); w.y = pk4_fp8w(s[4][i], s[5][i], s[6][i], s[7][i]);
;         w.z = pk4_fp8w(s[8][i], s[9][i], s[10][i], s[11][i]); w.w = pk4_fp8w(s[12][i], s[13][i], s[14][i], s[15][i]);
;         GAS v4u* p = (GAS v4u*)(base + (size_t)i * (size_t)d.ldk + lo);
;         if (NT) __builtin_nontemporal_store(w, p); else *p = w; }
	v_pk_mul_f32 v[130:131], v[130:131], s[30:31] op_sel_hi:[1,0]
	v_pk_mul_f32 v[132:133], v[132:133], s[30:31] op_sel_hi:[1,0]
	v_pk_mul_f32 v[134:135], v[134:135], s[30:31] op_sel_hi:[1,0]
	v_pk_mul_f32 v[136:137], v[136:137], s[30:31] op_sel_hi:[1,0]
	v_pk_mul_f32 v[138:139], v[138:139], s[30:31] op_sel_hi:[1,0]
	v_pk_mul_f32 v[140:141], v[140:141], s[30:31] op_sel_hi:[1,0]
	v_pk_mul_f32 v[142:143], v[142:143], s[30:31] op_sel_hi:[1,0]
	v_pk_mul_f32 v[144:145], v[144:145], s[30:31] op_sel_hi:[1,0]
	v_pk_mul_f32 v[146:147], v[146:147], s[30:31] op_sel_hi:[1,0]
	v_pk_mul_f32 v[148:149], v[148:149], s[30:31] op_sel_hi:[1,0]
	v_pk_mul_f32 v[150:151], v[150:151], s[30:31] op_sel_hi:[1,0]
	v_pk_mul_f32 v[152:153], v[152:153], s[30:31] op_sel_hi:[1,0]
	v_pk_mul_f32 v[154:155], v[154:155], s[30:31] op_sel_hi:[1,0]
	v_pk_mul_f32 v[156:157], v[156:157], s[30:31] op_sel_hi:[1,0]
	v_pk_mul_f32 v[158:159], v[158:159], s[30:31] op_sel_hi:[1,0]
	v_pk_mul_f32 v[160:161], v[160:161], s[30:31] op_sel_hi:[1,0]
	v_pk_mul_f32 v[162:163], v[162:163], s[30:31] op_sel_hi:[1,0]
	v_pk_mul_f32 v[164:165], v[164:165], s[30:31] op_sel_hi:[1,0]
	v_pk_mul_f32 v[166:167], v[166:167], s[30:31] op_sel_hi:[1,0]
	v_pk_mul_f32 v[168:169], v[168:169], s[30:31] op_sel_hi:[1,0]
	v_pk_mul_f32 v[170:171], v[170:171], s[30:31] op_sel_hi:[1,0]
	v_pk_mul_f32 v[172:173], v[172:173], s[30:31] op_sel_hi:[1,0]
	v_pk_mul_f32 v[174:175], v[174:175], s[30:31] op_sel_hi:[1,0]
	v_pk_mul_f32 v[176:177], v[176:177], s[30:31] op_sel_hi:[1,0]
	v_pk_mul_f32 v[178:179], v[178:179], s[30:31] op_sel_hi:[1,0]
	v_pk_mul_f32 v[180:181], v[180:181], s[30:31] op_sel_hi:[1,0]
	v_pk_mul_f32 v[182:183], v[182:183], s[30:31] op_sel_hi:[1,0]
	v_pk_mul_f32 v[184:185], v[184:185], s[30:31] op_sel_hi:[1,0]
	v_pk_mul_f32 v[186:187], v[186:187], s[30:31] op_sel_hi:[1,0]
	v_pk_mul_f32 v[188:189], v[188:189], s[30:31] op_sel_hi:[1,0]
	v_pk_mul_f32 v[190:191], v[190:191], s[30:31] op_sel_hi:[1,0]
	v_pk_mul_f32 v[192:193], v[192:193], s[30:31] op_sel_hi:[1,0]
	v_med3_f32 v130, v130, s24, v237
	v_med3_f32 v131, v131, s24, v237
	v_med3_f32 v132, v132, s24, v237
	v_med3_f32 v133, v133, s24, v237
	v_med3_f32 v134, v134, s24, v237
	v_med3_f32 v135, v135, s24, v237
	v_med3_f32 v136, v136, s24, v237
	v_med3_f32 v137, v137, s24, v237
	v_med3_f32 v138, v138, s24, v237
	v_med3_f32 v139, v139, s24, v237
	v_med3_f32 v140, v140, s24, v237
	v_med3_f32 v141, v141, s24, v237
	v_med3_f32 v142, v142, s24, v237
	v_med3_f32 v143, v143, s24, v237
	v_med3_f32 v144, v144, s24, v237
	v_med3_f32 v145, v145, s24, v237
	v_med3_f32 v146, v146, s24, v237
	v_med3_f32 v147, v147, s24, v237
	v_med3_f32 v148, v148, s24, v237
	v_med3_f32 v149, v149, s24, v237
	v_med3_f32 v150, v150, s24, v237
	v_med3_f32 v151, v151, s24, v237
	v_med3_f32 v152, v152, s24, v237
	v_med3_f32 v153, v153, s24, v237
	v_med3_f32 v154, v154, s24, v237
	v_med3_f32 v155, v155, s24, v237
	v_med3_f32 v156, v156, s24, v237
	v_med3_f32 v157, v157, s24, v237
	v_med3_f32 v158, v158, s24, v237
	v_med3_f32 v159, v159, s24, v237
	v_med3_f32 v160, v160, s24, v237
	v_med3_f32 v161, v161, s24, v237
	v_med3_f32 v162, v162, s24, v237
	v_med3_f32 v163, v163, s24, v237
	v_med3_f32 v164, v164, s24, v237
	v_med3_f32 v165, v165, s24, v237
	v_med3_f32 v166, v166, s24, v237
	v_med3_f32 v167, v167, s24, v237
	v_med3_f32 v168, v168, s24, v237
	v_med3_f32 v169, v169, s24, v237
	v_med3_f32 v170, v170, s24, v237
	v_med3_f32 v171, v171, s24, v237
	v_med3_f32 v172, v172, s24, v237
	v_med3_f32 v173, v173, s24, v237
	v_med3_f32 v174, v174, s24, v237
	v_med3_f32 v175, v175, s24, v237
	v_med3_f32 v176, v176, s24, v237
	v_med3_f32 v177, v177, s24, v237
	v_med3_f32 v178, v178, s24, v237
	v_med3_f32 v179, v179, s24, v237
	v_med3_f32 v180, v180, s24, v237
	v_med3_f32 v181, v181, s24, v237
	v_med3_f32 v182, v182, s24, v237
	v_med3_f32 v183, v183, s24, v237
	v_med3_f32 v184, v184, s24, v237
	v_med3_f32 v185, v185, s24, v237
	v_med3_f32 v186, v186, s24, v237
	v_med3_f32 v187, v187, s24, v237
	v_med3_f32 v188, v188, s24, v237
	v_med3_f32 v189, v189, s24, v237
	v_med3_f32 v190, v190, s24, v237
	v_med3_f32 v191, v191, s24, v237
	v_med3_f32 v192, v192, s24, v237
	v_med3_f32 v193, v193, s24, v237
	v_cvt_pk_fp8_f32 v130, v130, v134
	v_cvt_pk_fp8_f32 v130, v138, v142 op_sel:[0,0,1]
	v_cvt_pk_fp8_f32 v134, v131, v135
	v_cvt_pk_fp8_f32 v134, v139, v143 op_sel:[0,0,1]
	v_cvt_pk_fp8_f32 v138, v132, v136
	v_cvt_pk_fp8_f32 v138, v140, v144 op_sel:[0,0,1]
	v_cvt_pk_fp8_f32 v142, v133, v137
	v_cvt_pk_fp8_f32 v142, v141, v145 op_sel:[0,0,1]
	v_cvt_pk_fp8_f32 v131, v146, v150
	v_cvt_pk_fp8_f32 v131, v154, v158 op_sel:[0,0,1]
	v_cvt_pk_fp8_f32 v135, v147, v151
	v_cvt_pk_fp8_f32 v135, v155, v159 op_sel:[0,0,1]
	v_cvt_pk_fp8_f32 v139, v148, v152
	v_cvt_pk_fp8_f32 v139, v156, v160 op_sel:[0,0,1]
	v_cvt_pk_fp8_f32 v143, v149, v153
	v_cvt_pk_fp8_f32 v143, v157, v161 op_sel:[0,0,1]
	v_cvt_pk_fp8_f32 v132, v162, v166
	v_cvt_pk_fp8_f32 v132, v170, v174 op_sel:[0,0,1]
	v_cvt_pk_fp8_f32 v136, v163, v167
	v_cvt_pk_fp8_f32 v136, v171, v175 op_sel:[0,0,1]
	v_cvt_pk_fp8_f32 v140, v164, v168
	v_cvt_pk_fp8_f32 v140, v172, v176 op_sel:[0,0,1]
	v_cvt_pk_fp8_f32 v144, v165, v169
	v_cvt_pk_fp8_f32 v144, v173, v177 op_sel:[0,0,1]
	v_cvt_pk_fp8_f32 v133, v178, v182
	v_cvt_pk_fp8_f32 v133, v186, v190 op_sel:[0,0,1]
	v_cvt_pk_fp8_f32 v137, v179, v183
	v_cvt_pk_fp8_f32 v137, v187, v191 op_sel:[0,0,1]
	v_cvt_pk_fp8_f32 v141, v180, v184
	v_cvt_pk_fp8_f32 v141, v188, v192 op_sel:[0,0,1]
	v_cvt_pk_fp8_f32 v145, v181, v185
	v_cvt_pk_fp8_f32 v145, v189, v193 op_sel:[0,0,1]
	global_store_dwordx4 v250, v[130:133], s[42:43] nt
	global_store_dwordx4 v250, v[134:137], s[42:43] offset:2048 nt
	global_store_dwordx4 v251, v[138:141], s[42:43] nt
	global_store_dwordx4 v251, v[142:145], s[42:43] offset:2048 nt
	s_add_u32 s42, s42, 0x800000
	s_addc_u32 s43, s43, 0
	global_load_dwordx4 v[130:133], v246, s[4:5] nt
	global_load_dwordx4 v[134:137], v247, s[4:5] nt
	global_load_dwordx4 v[138:141], v248, s[4:5] nt
	global_load_dwordx4 v[142:145], v249, s[4:5] nt
	global_load_dwordx4 v[146:149], v246, s[6:7] nt
	global_load_dwordx4 v[150:153], v247, s[6:7] nt
	global_load_dwordx4 v[154:157], v248, s[6:7] nt
	global_load_dwordx4 v[158:161], v249, s[6:7] nt
	global_load_dwordx4 v[162:165], v246, s[8:9] nt
	global_load_dwordx4 v[166:169], v247, s[8:9] nt
	global_load_dwordx4 v[170:173], v248, s[8:9] nt
	global_load_dwordx4 v[174:177], v249, s[8:9] nt
	global_load_dwordx4 v[178:181], v246, s[38:39] nt
	global_load_dwordx4 v[182:185], v247, s[38:39] nt
	global_load_dwordx4 v[186:189], v248, s[38:39] nt
	global_load_dwordx4 v[190:193], v249, s[38:39] nt
	s_add_u32 s4, s4, 0x2000000
	s_addc_u32 s5, s5, 0
	s_add_u32 s6, s6, 0x2000000
	s_addc_u32 s7, s7, 0
	s_add_u32 s8, s8, 0x2000000
	s_addc_u32 s9, s9, 0
	s_add_u32 s38, s38, 0x2000000
	s_addc_u32 s39, s39, 0
	s_waitcnt vmcnt(40)
; #define GAS __attribute__((address_space(1)))
; template <bool GAIN, bool NT = false> __device__ __forceinline__ void titem8_load(const TItem& d, int lane, f32x4 (&r)[16], f32x4 (&g)[4]) {
;     const int q = lane & 7, kg = lane >> 3; const unsigned lo = (unsigned)((16 * kg) * d.N + 4 * q) * 4u;
;     const GAS char* base = (const GAS char*)d.src;
; #pragma unroll
;     for (int j = 0; j < 16; ++j) { const GAS f32x4* p = (const GAS f32x4*)(base + (size_t)j * (size_t)d.N * 4 + lo); r[j] = NT ? __builtin_nontemporal_load(p) : *p; }
; template <bool GAIN, bool NT = false> __device__ __forceinline__ void titem8_store(const TItem& d, int lane, const f32x4 (&r)[16], const f32x4 (&g)[4]) {
;     const int q = lane & 7, kg = lane >> 3; const unsigned lo = (unsigned)((4 * q) * d.ldk + 16 * kg);
;     GAS char* base = (GAS char*)d.dst;
;     f32x4 s[16];
; #pragma unroll
;     for (int j = 0; j < 16; ++j) s[j] = r[j] * ((GAIN ? g[j >> 2][j & 3] : 1.0f) * W8_SCALE);
; #pragma unroll
;     for (int i = 0; i < 4; ++i) { v4u w;
;         w.x = pk4_fp8w(s[0][i], s[1][i], s[2][i], s[3][i]); w.y = pk4_fp8w(s[4][i], s[5][i], s[6][i], s[7][i]);
;         w.z = pk4_fp8w(s[8][i], s[9][i], s[10][i], s[11][i]); w.w = pk4_fp8w(s[12][i], s[13][i], s[14][i], s[15][i]);
;         GAS v4u* p = (GAS v4u*)(base + (size_t)i * (size_t)d.ldk + lo);
;         if (NT) __builtin_nontemporal_store(w, p); else *p = w; }
	v_pk_mul_f32 v[0:1], v[0:1], s[30:31] op_sel_hi:[1,0]
	v_pk_mul_f32 v[2:3], v[2:3], s[30:31] op_sel_hi:[1,0]
	v_pk_mul_f32 v[4:5], v[4:5], s[30:31] op_sel_hi:[1,0]
	v_pk_mul_f32 v[6:7], v[6:7], s[30:31] op_sel_hi:[1,0]
	v_pk_mul_f32 v[8:9], v[8:9], s[30:31] op_sel_hi:[1,0]
	v_pk_mul_f32 v[10:11], v[10:11], s[30:31] op_sel_hi:[1,0]
	v_pk_mul_f32 v[12:13], v[12:13], s[30:31] op_sel_hi:[1,0]
	v_pk_mul_f32 v[14:15], v[14:15], s[30:31] op_sel_hi:[1,0]
	v_pk_mul_f32 v[16:17], v[16:17], s[30:31] op_sel_hi:[1,0]
	v_pk_mul_f32 v[18:19], v[18:19], s[30:31] op_sel_hi:[1,0]
	v_pk_mul_f32 v[20:21], v[20:21], s[30:31] op_sel_hi:[1,0]
	v_pk_mul_f32 v[22:23], v[22:23], s[30:31] op_sel_hi:[1,0]
	v_pk_mul_f32 v[24:25], v[24:25], s[30:31] op_sel_hi:[1,0]
	v_pk_mul_f32 v[26:27], v[26:27], s[30:31] op_sel_hi:[1,0]
	v_pk_mul_f32 v[28:29], v[28:29], s[30:31] op_sel_hi:[1,0]
	v_pk_mul_f32 v[30:31], v[30:31], s[30:31] op_sel_hi:[1,0]
	v_pk_mul_f32 v[32:33], v[32:33], s[30:31] op_sel_hi:[1,0]
	v_pk_mul_f32 v[34:35], v[34:35], s[30:31] op_sel_hi:[1,0]
	v_pk_mul_f32 v[36:37], v[36:37], s[30:31] op_sel_hi:[1,0]
	v_pk_mul_f32 v[38:39], v[38:39], s[30:31] op_sel_hi:[1,0]
	v_pk_mul_f32 v[40:41], v[40:41], s[30:31] op_sel_hi:[1,0]
	v_pk_mul_f32 v[42:43], v[42:43], s[30:31] op_sel_hi:[1,0]
	v_pk_mul_f32 v[44:45], v[44:45], s[30:31] op_sel_hi:[1,0]
	v_pk_mul_f32 v[46:47], v[46:47], s[30:31] op_sel_hi:[1,0]
	v_pk_mul_f32 v[48:49], v[48:49], s[30:31] op_sel_hi:[1,0]
	v_pk_mul_f32 v[50:51], v[50:51], s[30:31] op_sel_hi:[1,0]
	v_pk_mul_f32 v[52:53], v[52:53], s[30:31] op_sel_hi:[1,0]
	v_pk_mul_f32 v[54:55], v[54:55], s[30:31] op_sel_hi:[1,0]
	v_pk_mul_f32 v[56:57], v[56:57], s[30:31] op_sel_hi:[1,0]
	v_pk_mul_f32 v[58:59], v[58:59], s[30:31] op_sel_hi:[1,0]
	v_pk_mul_f32 v[60:61], v[60:61], s[30:31] op_sel_hi:[1,0]
	v_pk_mul_f32 v[62:63], v[62:63], s[30:31] op_sel_hi:[1,0]
	v_med3_f32 v0, v0, s24, v237
	v_med3_f32 v1, v1, s24, v237
	v_med3_f32 v2, v2, s24, v237
	v_med3_f32 v3, v3, s24, v237
	v_med3_f32 v4, v4, s24, v237
	v_med3_f32 v5, v5, s24, v237
	v_med3_f32 v6, v6, s24, v237
	v_med3_f32 v7, v7, s24, v237
	v_med3_f32 v8, v8, s24, v237
	v_med3_f32 v9, v9, s24, v237
	v_med3_f32 v10, v10, s24, v237
	v_med3_f32 v11, v11, s24, v237
	v_med3_f32 v12, v12, s24, v237
	v_med3_f32 v13, v13, s24, v237
	v_med3_f32 v14, v14, s24, v237
	v_med3_f32 v15, v15, s24, v237
	v_med3_f32 v16, v16, s24, v237
	v_med3_f32 v17, v17, s24, v237
	v_med3_f32 v18, v18, s24, v237
	v_med3_f32 v19, v19, s24, v237
	v_med3_f32 v20, v20, s24, v237
	v_med3_f32 v21, v21, s24, v237
	v_med3_f32 v22, v22, s24, v237
	v_med3_f32 v23, v23, s24, v237
	v_med3_f32 v24, v24, s24, v237
	v_med3_f32 v25, v25, s24, v237
	v_med3_f32 v26, v26, s24, v237
	v_med3_f32 v27, v27, s24, v237
	v_med3_f32 v28, v28, s24, v237
	v_med3_f32 v29, v29, s24, v237
	v_med3_f32 v30, v30, s24, v237
	v_med3_f32 v31, v31, s24, v237
	v_med3_f32 v32, v32, s24, v237
	v_med3_f32 v33, v33, s24, v237
	v_med3_f32 v34, v34, s24, v237
	v_med3_f32 v35, v35, s24, v237
	v_med3_f32 v36, v36, s24, v237
	v_med3_f32 v37, v37, s24, v237
	v_med3_f32 v38, v38, s24, v237
	v_med3_f32 v39, v39, s24, v237
	v_med3_f32 v40, v40, s24, v237
	v_med3_f32 v41, v41, s24, v237
	v_med3_f32 v42, v42, s24, v237
	v_med3_f32 v43, v43, s24, v237
	v_med3_f32 v44, v44, s24, v237
	v_med3_f32 v45, v45, s24, v237
	v_med3_f32 v46, v46, s24, v237
	v_med3_f32 v47, v47, s24, v237
	v_med3_f32 v48, v48, s24, v237
	v_med3_f32 v49, v49, s24, v237
	v_med3_f32 v50, v50, s24, v237
	v_med3_f32 v51, v51, s24, v237
	v_med3_f32 v52, v52, s24, v237
	v_med3_f32 v53, v53, s24, v237
	v_med3_f32 v54, v54, s24, v237
	v_med3_f32 v55, v55, s24, v237
	v_med3_f32 v56, v56, s24, v237
	v_med3_f32 v57, v57, s24, v237
	v_med3_f32 v58, v58, s24, v237
	v_med3_f32 v59, v59, s24, v237
	v_med3_f32 v60, v60, s24, v237
	v_med3_f32 v61, v61, s24, v237
	v_med3_f32 v62, v62, s24, v237
	v_med3_f32 v63, v63, s24, v237
	v_cvt_pk_fp8_f32 v0, v0, v4
	v_cvt_pk_fp8_f32 v0, v8, v12 op_sel:[0,0,1]
	v_cvt_pk_fp8_f32 v4, v1, v5
	v_cvt_pk_fp8_f32 v4, v9, v13 op_sel:[0,0,1]
	v_cvt_pk_fp8_f32 v8, v2, v6
	v_cvt_pk_fp8_f32 v8, v10, v14 op_sel:[0,0,1]
	v_cvt_pk_fp8_f32 v12, v3, v7
	v_cvt_pk_fp8_f32 v12, v11, v15 op_sel:[0,0,1]
	v_cvt_pk_fp8_f32 v1, v16, v20
	v_cvt_pk_fp8_f32 v1, v24, v28 op_sel:[0,0,1]
	v_cvt_pk_fp8_f32 v5, v17, v21
	v_cvt_pk_fp8_f32 v5, v25, v29 op_sel:[0,0,1]
	v_cvt_pk_fp8_f32 v9, v18, v22
	v_cvt_pk_fp8_f32 v9, v26, v30 op_sel:[0,0,1]
	v_cvt_pk_fp8_f32 v13, v19, v23
	v_cvt_pk_fp8_f32 v13, v27, v31 op_sel:[0,0,1]
	v_cvt_pk_fp8_f32 v2, v32, v36
	v_cvt_pk_fp8_f32 v2, v40, v44 op_sel:[0,0,1]
	v_cvt_pk_fp8_f32 v6, v33, v37
	v_cvt_pk_fp8_f32 v6, v41, v45 op_sel:[0,0,1]
	v_cvt_pk_fp8_f32 v10, v34, v38
	v_cvt_pk_fp8_f32 v10, v42, v46 op_sel:[0,0,1]
	v_cvt_pk_fp8_f32 v14, v35, v39
	v_cvt_pk_fp8_f32 v14, v43, v47 op_sel:[0,0,1]
	v_cvt_pk_fp8_f32 v3, v48, v52
	v_cvt_pk_fp8_f32 v3, v56, v60 op_sel:[0,0,1]
	v_cvt_pk_fp8_f32 v7, v49, v53
	v_cvt_pk_fp8_f32 v7, v57, v61 op_sel:[0,0,1]
	v_cvt_pk_fp8_f32 v11, v50, v54
	v_cvt_pk_fp8_f32 v11, v58, v62 op_sel:[0,0,1]
	v_cvt_pk_fp8_f32 v15, v51, v55
	v_cvt_pk_fp8_f32 v15, v59, v63 op_sel:[0,0,1]
	global_store_dwordx4 v250, v[0:3], s[42:43] nt
	global_store_dwordx4 v250, v[4:7], s[42:43] offset:2048 nt
	global_store_dwordx4 v251, v[8:11], s[42:43] nt
	global_store_dwordx4 v251, v[12:15], s[42:43] offset:2048 nt
	s_add_u32 s42, s42, 0x800000
	s_addc_u32 s43, s43, 0
	global_load_dwordx4 v[0:3], v246, s[4:5] nt
	global_load_dwordx4 v[4:7], v247, s[4:5] nt
	global_load_dwordx4 v[8:11], v248, s[4:5] nt
	global_load_dwordx4 v[12:15], v249, s[4:5] nt
	global_load_dwordx4 v[16:19], v246, s[6:7] nt
	global_load_dwordx4 v[20:23], v247, s[6:7] nt
	global_load_dwordx4 v[24:27], v248, s[6:7] nt
	global_load_dwordx4 v[28:31], v249, s[6:7] nt
	global_load_dwordx4 v[32:35], v246, s[8:9] nt
	global_load_dwordx4 v[36:39], v247, s[8:9] nt
	global_load_dwordx4 v[40:43], v248, s[8:9] nt
	global_load_dwordx4 v[44:47], v249, s[8:9] nt
	global_load_dwordx4 v[48:51], v246, s[38:39] nt
	global_load_dwordx4 v[52:55], v247, s[38:39] nt
	global_load_dwordx4 v[56:59], v248, s[38:39] nt
	global_load_dwordx4 v[60:63], v249, s[38:39] nt
	s_add_u32 s4, s4, 0x2000000
	s_addc_u32 s5, s5, 0
	s_add_u32 s6, s6, 0x2000000
	s_addc_u32 s7, s7, 0
	s_add_u32 s8, s8, 0x2000000
	s_addc_u32 s9, s9, 0
	s_add_u32 s38, s38, 0x2000000
	s_addc_u32 s39, s39, 0
	s_waitcnt vmcnt(40)
; #define GAS __attribute__((address_space(1)))
; template <bool GAIN, bool NT = false> __device__ __forceinline__ void titem8_load(const TItem& d, int lane, f32x4 (&r)[16], f32x4 (&g)[4]) {
;     const int q = lane & 7, kg = lane >> 3; const unsigned lo = (unsigned)((16 * kg) * d.N + 4 * q) * 4u;
;     const GAS char* base = (const GAS char*)d.src;
; #pragma unroll
;     for (int j = 0; j < 16; ++j) { const GAS f32x4* p = (const GAS f32x4*)(base + (size_t)j * (size_t)d.N * 4 + lo); r[j] = NT ? __builtin_nontemporal_load(p) : *p; }
; template <bool GAIN, bool NT = false> __device__ __forceinline__ void titem8_store(const TItem& d, int lane, const f32x4 (&r)[16], const f32x4 (&g)[4]) {
;     const int q = lane & 7, kg = lane >> 3; const unsigned lo = (unsigned)((4 * q) * d.ldk + 16 * kg);
;     GAS char* base = (GAS char*)d.dst;
;     f32x4 s[16];
; #pragma unroll
;     for (int j = 0; j < 16; ++j) s[j] = r[j] * ((GAIN ? g[j >> 2][j & 3] : 1.0f) * W8_SCALE);
; #pragma unroll
;     for (int i = 0; i < 4; ++i) { v4u w;
;         w.x = pk4_fp8w(s[0][i], s[1][i], s[2][i], s[3][i]); w.y = pk4_fp8w(s[4][i], s[5][i], s[6][i], s[7][i]);
;         w.z = pk4_fp8w(s[8][i], s[9][i], s[10][i], s[11][i]); w.w = pk4_fp8w(s[12][i], s[13][i], s[14][i], s[15][i]);
;         GAS v4u* p = (GAS v4u*)(base + (size_t)i * (size_t)d.ldk + lo);
;         if (NT) __builtin_nontemporal_store(w, p); else *p = w; }
	v_pk_mul_f32 v[66:67], v[66:67], s[30:31] op_sel_hi:[1,0]
	v_pk_mul_f32 v[68:69], v[68:69], s[30:31] op_sel_hi:[1,0]
	v_pk_mul_f32 v[70:71], v[70:71], s[30:31] op_sel_hi:[1,0]
	v_pk_mul_f32 v[72:73], v[72:73], s[30:31] op_sel_hi:[1,0]
	v_pk_mul_f32 v[74:75], v[74:75], s[30:31] op_sel_hi:[1,0]
	v_pk_mul_f32 v[76:77], v[76:77], s[30:31] op_sel_hi:[1,0]
	v_pk_mul_f32 v[78:79], v[78:79], s[30:31] op_sel_hi:[1,0]
	v_pk_mul_f32 v[80:81], v[80:81], s[30:31] op_sel_hi:[1,0]
	v_pk_mul_f32 v[82:83], v[82:83], s[30:31] op_sel_hi:[1,0]
	v_pk_mul_f32 v[84:85], v[84:85], s[30:31] op_sel_hi:[1,0]
	v_pk_mul_f32 v[86:87], v[86:87], s[30:31] op_sel_hi:[1,0]
	v_pk_mul_f32 v[88:89], v[88:89], s[30:31] op_sel_hi:[1,0]
	v_pk_mul_f32 v[90:91], v[90:91], s[30:31] op_sel_hi:[1,0]
	v_pk_mul_f32 v[92:93], v[92:93], s[30:31] op_sel_hi:[1,0]
	v_pk_mul_f32 v[94:95], v[94:95], s[30:31] op_sel_hi:[1,0]
	v_pk_mul_f32 v[96:97], v[96:97], s[30:31] op_sel_hi:[1,0]
	v_pk_mul_f32 v[98:99], v[98:99], s[30:31] op_sel_hi:[1,0]
	v_pk_mul_f32 v[100:101], v[100:101], s[30:31] op_sel_hi:[1,0]
	v_pk_mul_f32 v[102:103], v[102:103], s[30:31] op_sel_hi:[1,0]
	v_pk_mul_f32 v[104:105], v[104:105], s[30:31] op_sel_hi:[1,0]
	v_pk_mul_f32 v[106:107], v[106:107], s[30:31] op_sel_hi:[1,0]
	v_pk_mul_f32 v[108:109], v[108:109], s[30:31] op_sel_hi:[1,0]
	v_pk_mul_f32 v[110:111], v[110:111], s[30:31] op_sel_hi:[1,0]
	v_pk_mul_f32 v[112:113], v[112:113], s[30:31] op_sel_hi:[1,0]
	v_pk_mul_f32 v[114:115], v[114:115], s[30:31] op_sel_hi:[1,0]
	v_pk_mul_f32 v[116:117], v[116:117], s[30:31] op_sel_hi:[1,0]
	v_pk_mul_f32 v[118:119], v[118:119], s[30:31] op_sel_hi:[1,0]
	v_pk_mul_f32 v[120:121], v[120:121], s[30:31] op_sel_hi:[1,0]
	v_pk_mul_f32 v[122:123], v[122:123], s[30:31] op_sel_hi:[1,0]
	v_pk_mul_f32 v[124:125], v[124:125], s[30:31] op_sel_hi:[1,0]
	v_pk_mul_f32 v[126:127], v[126:127], s[30:31] op_sel_hi:[1,0]
	v_pk_mul_f32 v[128:129], v[128:129], s[30:31] op_sel_hi:[1,0]
	v_med3_f32 v66, v66, s24, v237
	v_med3_f32 v67, v67, s24, v237
	v_med3_f32 v68, v68, s24, v237
	v_med3_f32 v69, v69, s24, v237
	v_med3_f32 v70, v70, s24, v237
	v_med3_f32 v71, v71, s24, v237
	v_med3_f32 v72, v72, s24, v237
	v_med3_f32 v73, v73, s24, v237
	v_med3_f32 v74, v74, s24, v237
	v_med3_f32 v75, v75, s24, v237
	v_med3_f32 v76, v76, s24, v237
	v_med3_f32 v77, v77, s24, v237
	v_med3_f32 v78, v78, s24, v237
	v_med3_f32 v79, v79, s24, v237
	v_med3_f32 v80, v80, s24, v237
	v_med3_f32 v81, v81, s24, v237
	v_med3_f32 v82, v82, s24, v237
	v_med3_f32 v83, v83, s24, v237
	v_med3_f32 v84, v84, s24, v237
	v_med3_f32 v85, v85, s24, v237
	v_med3_f32 v86, v86, s24, v237
	v_med3_f32 v87, v87, s24, v237
	v_med3_f32 v88, v88, s24, v237
	v_med3_f32 v89, v89, s24, v237
	v_med3_f32 v90, v90, s24, v237
	v_med3_f32 v91, v91, s24, v237
	v_med3_f32 v92, v92, s24, v237
	v_med3_f32 v93, v93, s24, v237
	v_med3_f32 v94, v94, s24, v237
	v_med3_f32 v95, v95, s24, v237
	v_med3_f32 v96, v96, s24, v237
	v_med3_f32 v97, v97, s24, v237
	v_med3_f32 v98, v98, s24, v237
	v_med3_f32 v99, v99, s24, v237
	v_med3_f32 v100, v100, s24, v237
	v_med3_f32 v101, v101, s24, v237
	v_med3_f32 v102, v102, s24, v237
	v_med3_f32 v103, v103, s24, v237
	v_med3_f32 v104, v104, s24, v237
	v_med3_f32 v105, v105, s24, v237
	v_med3_f32 v106, v106, s24, v237
	v_med3_f32 v107, v107, s24, v237
	v_med3_f32 v108, v108, s24, v237
	v_med3_f32 v109, v109, s24, v237
	v_med3_f32 v110, v110, s24, v237
	v_med3_f32 v111, v111, s24, v237
	v_med3_f32 v112, v112, s24, v237
	v_med3_f32 v113, v113, s24, v237
	v_med3_f32 v114, v114, s24, v237
	v_med3_f32 v115, v115, s24, v237
	v_med3_f32 v116, v116, s24, v237
	v_med3_f32 v117, v117, s24, v237
	v_med3_f32 v118, v118, s24, v237
	v_med3_f32 v119, v119, s24, v237
	v_med3_f32 v120, v120, s24, v237
	v_med3_f32 v121, v121, s24, v237
	v_med3_f32 v122, v122, s24, v237
	v_med3_f32 v123, v123, s24, v237
	v_med3_f32 v124, v124, s24, v237
	v_med3_f32 v125, v125, s24, v237
	v_med3_f32 v126, v126, s24, v237
	v_med3_f32 v127, v127, s24, v237
	v_med3_f32 v128, v128, s24, v237
	v_med3_f32 v129, v129, s24, v237
	v_cvt_pk_fp8_f32 v66, v66, v70
	v_cvt_pk_fp8_f32 v66, v74, v78 op_sel:[0,0,1]
	v_cvt_pk_fp8_f32 v70, v67, v71
	v_cvt_pk_fp8_f32 v70, v75, v79 op_sel:[0,0,1]
	v_cvt_pk_fp8_f32 v74, v68, v72
	v_cvt_pk_fp8_f32 v74, v76, v80 op_sel:[0,0,1]
	v_cvt_pk_fp8_f32 v78, v69, v73
	v_cvt_pk_fp8_f32 v78, v77, v81 op_sel:[0,0,1]
	v_cvt_pk_fp8_f32 v67, v82, v86
	v_cvt_pk_fp8_f32 v67, v90, v94 op_sel:[0,0,1]
	v_cvt_pk_fp8_f32 v71, v83, v87
	v_cvt_pk_fp8_f32 v71, v91, v95 op_sel:[0,0,1]
	v_cvt_pk_fp8_f32 v75, v84, v88
	v_cvt_pk_fp8_f32 v75, v92, v96 op_sel:[0,0,1]
	v_cvt_pk_fp8_f32 v79, v85, v89
	v_cvt_pk_fp8_f32 v79, v93, v97 op_sel:[0,0,1]
	v_cvt_pk_fp8_f32 v68, v98, v102
	v_cvt_pk_fp8_f32 v68, v106, v110 op_sel:[0,0,1]
	v_cvt_pk_fp8_f32 v72, v99, v103
	v_cvt_pk_fp8_f32 v72, v107, v111 op_sel:[0,0,1]
	v_cvt_pk_fp8_f32 v76, v100, v104
	v_cvt_pk_fp8_f32 v76, v108, v112 op_sel:[0,0,1]
	v_cvt_pk_fp8_f32 v80, v101, v105
	v_cvt_pk_fp8_f32 v80, v109, v113 op_sel:[0,0,1]
	v_cvt_pk_fp8_f32 v69, v114, v118
	v_cvt_pk_fp8_f32 v69, v122, v126 op_sel:[0,0,1]
	v_cvt_pk_fp8_f32 v73, v115, v119
	v_cvt_pk_fp8_f32 v73, v123, v127 op_sel:[0,0,1]
	v_cvt_pk_fp8_f32 v77, v116, v120
	v_cvt_pk_fp8_f32 v77, v124, v128 op_sel:[0,0,1]
	v_cvt_pk_fp8_f32 v81, v117, v121
	v_cvt_pk_fp8_f32 v81, v125, v129 op_sel:[0,0,1]
	global_store_dwordx4 v250, v[66:69], s[42:43] nt
	global_store_dwordx4 v250, v[70:73], s[42:43] offset:2048 nt
	global_store_dwordx4 v251, v[74:77], s[42:43] nt
	global_store_dwordx4 v251, v[78:81], s[42:43] offset:2048 nt
	s_add_u32 s42, s42, 0x800000
	s_addc_u32 s43, s43, 0
	global_load_dwordx4 v[66:69], v246, s[4:5] nt
	global_load_dwordx4 v[70:73], v247, s[4:5] nt
	global_load_dwordx4 v[74:77], v248, s[4:5] nt
	global_load_dwordx4 v[78:81], v249, s[4:5] nt
	global_load_dwordx4 v[82:85], v246, s[6:7] nt
	global_load_dwordx4 v[86:89], v247, s[6:7] nt
	global_load_dwordx4 v[90:93], v248, s[6:7] nt
	global_load_dwordx4 v[94:97], v249, s[6:7] nt
	global_load_dwordx4 v[98:101], v246, s[8:9] nt
	global_load_dwordx4 v[102:105], v247, s[8:9] nt
	global_load_dwordx4 v[106:109], v248, s[8:9] nt
	global_load_dwordx4 v[110:113], v249, s[8:9] nt
	global_load_dwordx4 v[114:117], v246, s[38:39] nt
	global_load_dwordx4 v[118:121], v247, s[38:39] nt
	global_load_dwordx4 v[122:125], v248, s[38:39] nt
	global_load_dwordx4 v[126:129], v249, s[38:39] nt
	s_add_u32 s4, s4, 0x2000000
	s_addc_u32 s5, s5, 0
	s_add_u32 s6, s6, 0x2000000
	s_addc_u32 s7, s7, 0
	s_add_u32 s8, s8, 0x2000000
	s_addc_u32 s9, s9, 0
	s_add_u32 s38, s38, 0x2000000
	s_addc_u32 s39, s39, 0
	s_waitcnt vmcnt(40)
; #define GAS __attribute__((address_space(1)))
; template <bool GAIN, bool NT = false> __device__ __forceinline__ void titem8_load(const TItem& d, int lane, f32x4 (&r)[16], f32x4 (&g)[4]) {
;     const int q = lane & 7, kg = lane >> 3; const unsigned lo = (unsigned)((16 * kg) * d.N + 4 * q) * 4u;
;     const GAS char* base = (const GAS char*)d.src;
; #pragma unroll
;     for (int j = 0; j < 16; ++j) { const GAS f32x4* p = (const GAS f32x4*)(base + (size_t)j * (size_t)d.N * 4 + lo); r[j] = NT ? __builtin_nontemporal_load(p) : *p; }
; template <bool GAIN, bool NT = false> __device__ __forceinline__ void titem8_store(const TItem& d, int lane, const f32x4 (&r)[16], const f32x4 (&g)[4]) {
;     const int q = lane & 7, kg = lane >> 3; const unsigned lo = (unsigned)((4 * q) * d.ldk + 16 * kg);
;     GAS char* base = (GAS char*)d.dst;
;     f32x4 s[16];
; #pragma unroll
;     for (int j = 0; j < 16; ++j) s[j] = r[j] * ((GAIN ? g[j >> 2][j & 3] : 1.0f) * W8_SCALE);
; #pragma unroll
;     for (int i = 0; i < 4; ++i) { v4u w;
;         w.x = pk4_fp8w(s[0][i], s[1][i], s[2][i], s[3][i]); w.y = pk4_fp8w(s[4][i], s[5][i], s[6][i], s[7][i]);
;         w.z = pk4_fp8w(s[8][i], s[9][i], s[10][i], s[11][i]); w.w = pk4_fp8w(s[12][i], s[13][i], s[14][i], s[15][i]);
;         GAS v4u* p = (GAS v4u*)(base + (size_t)i * (size_t)d.ldk + lo);
;         if (NT) __builtin_nontemporal_store(w, p); else *p = w; }
	v_pk_mul_f32 v[130:131], v[130:131], s[30:31] op_sel_hi:[1,0]
	v_pk_mul_f32 v[132:133], v[132:133], s[30:31] op_sel_hi:[1,0]
	v_pk_mul_f32 v[134:135], v[134:135], s[30:31] op_sel_hi:[1,0]
	v_pk_mul_f32 v[136:137], v[136:137], s[30:31] op_sel_hi:[1,0]
	v_pk_mul_f32 v[138:139], v[138:139], s[30:31] op_sel_hi:[1,0]
	v_pk_mul_f32 v[140:141], v[140:141], s[30:31] op_sel_hi:[1,0]
	v_pk_mul_f32 v[142:143], v[142:143], s[30:31] op_sel_hi:[1,0]
	v_pk_mul_f32 v[144:145], v[144:145], s[30:31] op_sel_hi:[1,0]
	v_pk_mul_f32 v[146:147], v[146:147], s[30:31] op_sel_hi:[1,0]
	v_pk_mul_f32 v[148:149], v[148:149], s[30:31] op_sel_hi:[1,0]
	v_pk_mul_f32 v[150:151], v[150:151], s[30:31] op_sel_hi:[1,0]
	v_pk_mul_f32 v[152:153], v[152:153], s[30:31] op_sel_hi:[1,0]
	v_pk_mul_f32 v[154:155], v[154:155], s[30:31] op_sel_hi:[1,0]
	v_pk_mul_f32 v[156:157], v[156:157], s[30:31] op_sel_hi:[1,0]
	v_pk_mul_f32 v[158:159], v[158:159], s[30:31] op_sel_hi:[1,0]
	v_pk_mul_f32 v[160:161], v[160:161], s[30:31] op_sel_hi:[1,0]
	v_pk_mul_f32 v[162:163], v[162:163], s[30:31] op_sel_hi:[1,0]
	v_pk_mul_f32 v[164:165], v[164:165], s[30:31] op_sel_hi:[1,0]
	v_pk_mul_f32 v[166:167], v[166:167], s[30:31] op_sel_hi:[1,0]
	v_pk_mul_f32 v[168:169], v[168:169], s[30:31] op_sel_hi:[1,0]
	v_pk_mul_f32 v[170:171], v[170:171], s[30:31] op_sel_hi:[1,0]
	v_pk_mul_f32 v[172:173], v[172:173], s[30:31] op_sel_hi:[1,0]
	v_pk_mul_f32 v[174:175], v[174:175], s[30:31] op_sel_hi:[1,0]
	v_pk_mul_f32 v[176:177], v[176:177], s[30:31] op_sel_hi:[1,0]
	v_pk_mul_f32 v[178:179], v[178:179], s[30:31] op_sel_hi:[1,0]
	v_pk_mul_f32 v[180:181], v[180:181], s[30:31] op_sel_hi:[1,0]
	v_pk_mul_f32 v[182:183], v[182:183], s[30:31] op_sel_hi:[1,0]
	v_pk_mul_f32 v[184:185], v[184:185], s[30:31] op_sel_hi:[1,0]
	v_pk_mul_f32 v[186:187], v[186:187], s[30:31] op_sel_hi:[1,0]
	v_pk_mul_f32 v[188:189], v[188:189], s[30:31] op_sel_hi:[1,0]
	v_pk_mul_f32 v[190:191], v[190:191], s[30:31] op_sel_hi:[1,0]
	v_pk_mul_f32 v[192:193], v[192:193], s[30:31] op_sel_hi:[1,0]
	v_med3_f32 v130, v130, s24, v237
	v_med3_f32 v131, v131, s24, v237
	v_med3_f32 v132, v132, s24, v237
	v_med3_f32 v133, v133, s24, v237
	v_med3_f32 v134, v134, s24, v237
	v_med3_f32 v135, v135, s24, v237
	v_med3_f32 v136, v136, s24, v237
	v_med3_f32 v137, v137, s24, v237
	v_med3_f32 v138, v138, s24, v237
	v_med3_f32 v139, v139, s24, v237
	v_med3_f32 v140, v140, s24, v237
	v_med3_f32 v141, v141, s24, v237
	v_med3_f32 v142, v142, s24, v237
	v_med3_f32 v143, v143, s24, v237
	v_med3_f32 v144, v144, s24, v237
	v_med3_f32 v145, v145, s24, v237
	v_med3_f32 v146, v146, s24, v237
	v_med3_f32 v147, v147, s24, v237
	v_med3_f32 v148, v148, s24, v237
	v_med3_f32 v149, v149, s24, v237
	v_med3_f32 v150, v150, s24, v237
	v_med3_f32 v151, v151, s24, v237
	v_med3_f32 v152, v152, s24, v237
	v_med3_f32 v153, v153, s24, v237
	v_med3_f32 v154, v154, s24, v237
	v_med3_f32 v155, v155, s24, v237
	v_med3_f32 v156, v156, s24, v237
	v_med3_f32 v157, v157, s24, v237
	v_med3_f32 v158, v158, s24, v237
	v_med3_f32 v159, v159, s24, v237
	v_med3_f32 v160, v160, s24, v237
	v_med3_f32 v161, v161, s24, v237
	v_med3_f32 v162, v162, s24, v237
	v_med3_f32 v163, v163, s24, v237
	v_med3_f32 v164, v164, s24, v237
	v_med3_f32 v165, v165, s24, v237
	v_med3_f32 v166, v166, s24, v237
	v_med3_f32 v167, v167, s24, v237
	v_med3_f32 v168, v168, s24, v237
	v_med3_f32 v169, v169, s24, v237
	v_med3_f32 v170, v170, s24, v237
	v_med3_f32 v171, v171, s24, v237
	v_med3_f32 v172, v172, s24, v237
	v_med3_f32 v173, v173, s24, v237
	v_med3_f32 v174, v174, s24, v237
	v_med3_f32 v175, v175, s24, v237
	v_med3_f32 v176, v176, s24, v237
	v_med3_f32 v177, v177, s24, v237
	v_med3_f32 v178, v178, s24, v237
	v_med3_f32 v179, v179, s24, v237
	v_med3_f32 v180, v180, s24, v237
	v_med3_f32 v181, v181, s24, v237
	v_med3_f32 v182, v182, s24, v237
	v_med3_f32 v183, v183, s24, v237
	v_med3_f32 v184, v184, s24, v237
	v_med3_f32 v185, v185, s24, v237
	v_med3_f32 v186, v186, s24, v237
	v_med3_f32 v187, v187, s24, v237
	v_med3_f32 v188, v188, s24, v237
	v_med3_f32 v189, v189, s24, v237
	v_med3_f32 v190, v190, s24, v237
	v_med3_f32 v191, v191, s24, v237
	v_med3_f32 v192, v192, s24, v237
	v_med3_f32 v193, v193, s24, v237
	v_cvt_pk_fp8_f32 v130, v130, v134
	v_cvt_pk_fp8_f32 v130, v138, v142 op_sel:[0,0,1]
	v_cvt_pk_fp8_f32 v134, v131, v135
	v_cvt_pk_fp8_f32 v134, v139, v143 op_sel:[0,0,1]
	v_cvt_pk_fp8_f32 v138, v132, v136
	v_cvt_pk_fp8_f32 v138, v140, v144 op_sel:[0,0,1]
	v_cvt_pk_fp8_f32 v142, v133, v137
	v_cvt_pk_fp8_f32 v142, v141, v145 op_sel:[0,0,1]
	v_cvt_pk_fp8_f32 v131, v146, v150
	v_cvt_pk_fp8_f32 v131, v154, v158 op_sel:[0,0,1]
	v_cvt_pk_fp8_f32 v135, v147, v151
	v_cvt_pk_fp8_f32 v135, v155, v159 op_sel:[0,0,1]
	v_cvt_pk_fp8_f32 v139, v148, v152
	v_cvt_pk_fp8_f32 v139, v156, v160 op_sel:[0,0,1]
	v_cvt_pk_fp8_f32 v143, v149, v153
	v_cvt_pk_fp8_f32 v143, v157, v161 op_sel:[0,0,1]
	v_cvt_pk_fp8_f32 v132, v162, v166
	v_cvt_pk_fp8_f32 v132, v170, v174 op_sel:[0,0,1]
	v_cvt_pk_fp8_f32 v136, v163, v167
	v_cvt_pk_fp8_f32 v136, v171, v175 op_sel:[0,0,1]
	v_cvt_pk_fp8_f32 v140, v164, v168
	v_cvt_pk_fp8_f32 v140, v172, v176 op_sel:[0,0,1]
	v_cvt_pk_fp8_f32 v144, v165, v169
	v_cvt_pk_fp8_f32 v144, v173, v177 op_sel:[0,0,1]
	v_cvt_pk_fp8_f32 v133, v178, v182
	v_cvt_pk_fp8_f32 v133, v186, v190 op_sel:[0,0,1]
	v_cvt_pk_fp8_f32 v137, v179, v183
	v_cvt_pk_fp8_f32 v137, v187, v191 op_sel:[0,0,1]
	v_cvt_pk_fp8_f32 v141, v180, v184
	v_cvt_pk_fp8_f32 v141, v188, v192 op_sel:[0,0,1]
	v_cvt_pk_fp8_f32 v145, v181, v185
	v_cvt_pk_fp8_f32 v145, v189, v193 op_sel:[0,0,1]
	global_store_dwordx4 v250, v[130:133], s[42:43] nt
	global_store_dwordx4 v250, v[134:137], s[42:43] offset:2048 nt
	global_store_dwordx4 v251, v[138:141], s[42:43] nt
	global_store_dwordx4 v251, v[142:145], s[42:43] offset:2048 nt
	s_add_u32 s42, s42, 0x800000
	s_addc_u32 s43, s43, 0
	global_load_dwordx4 v[130:133], v246, s[4:5] nt
	global_load_dwordx4 v[134:137], v247, s[4:5] nt
	global_load_dwordx4 v[138:141], v248, s[4:5] nt
	global_load_dwordx4 v[142:145], v249, s[4:5] nt
	global_load_dwordx4 v[146:149], v246, s[6:7] nt
	global_load_dwordx4 v[150:153], v247, s[6:7] nt
	global_load_dwordx4 v[154:157], v248, s[6:7] nt
	global_load_dwordx4 v[158:161], v249, s[6:7] nt
	global_load_dwordx4 v[162:165], v246, s[8:9] nt
	global_load_dwordx4 v[166:169], v247, s[8:9] nt
	global_load_dwordx4 v[170:173], v248, s[8:9] nt
	global_load_dwordx4 v[174:177], v249, s[8:9] nt
	global_load_dwordx4 v[178:181], v246, s[38:39] nt
	global_load_dwordx4 v[182:185], v247, s[38:39] nt
	global_load_dwordx4 v[186:189], v248, s[38:39] nt
	global_load_dwordx4 v[190:193], v249, s[38:39] nt
	s_add_u32 s4, s4, 0x2000000
	s_addc_u32 s5, s5, 0
	s_add_u32 s6, s6, 0x2000000
	s_addc_u32 s7, s7, 0
	s_add_u32 s8, s8, 0x2000000
	s_addc_u32 s9, s9, 0
	s_add_u32 s38, s38, 0x2000000
	s_addc_u32 s39, s39, 0
	s_waitcnt vmcnt(40)
; #define GAS __attribute__((address_space(1)))
; template <bool GAIN, bool NT = false> __device__ __forceinline__ void titem8_load(const TItem& d, int lane, f32x4 (&r)[16], f32x4 (&g)[4]) {
;     const int q = lane & 7, kg = lane >> 3; const unsigned lo = (unsigned)((16 * kg) * d.N + 4 * q) * 4u;
;     const GAS char* base = (const GAS char*)d.src;
; #pragma unroll
;     for (int j = 0; j < 16; ++j) { const GAS f32x4* p = (const GAS f32x4*)(base + (size_t)j * (size_t)d.N * 4 + lo); r[j] = NT ? __builtin_nontemporal_load(p) : *p; }
; template <bool GAIN, bool NT = false> __device__ __forceinline__ void titem8_store(const TItem& d, int lane, const f32x4 (&r)[16], const f32x4 (&g)[4]) {
;     const int q = lane & 7, kg = lane >> 3; const unsigned lo = (unsigned)((4 * q) * d.ldk + 16 * kg);
;     GAS char* base = (GAS char*)d.dst;
;     f32x4 s[16];
; #pragma unroll
;     for (int j = 0; j < 16; ++j) s[j] = r[j] * ((GAIN ? g[j >> 2][j & 3] : 1.0f) * W8_SCALE);
; #pragma unroll
;     for (int i = 0; i < 4; ++i) { v4u w;
;         w.x = pk4_fp8w(s[0][i], s[1][i], s[2][i], s[3][i]); w.y = pk4_fp8w(s[4][i], s[5][i], s[6][i], s[7][i]);
;         w.z = pk4_fp8w(s[8][i], s[9][i], s[10][i], s[11][i]); w.w = pk4_fp8w(s[12][i], s[13][i], s[14][i], s[15][i]);
;         GAS v4u* p = (GAS v4u*)(base + (size_t)i * (size_t)d.ldk + lo);
;         if (NT) __builtin_nontemporal_store(w, p); else *p = w; }
	v_pk_mul_f32 v[0:1], v[0:1], s[30:31] op_sel_hi:[1,0]
	v_pk_mul_f32 v[2:3], v[2:3], s[30:31] op_sel_hi:[1,0]
	v_pk_mul_f32 v[4:5], v[4:5], s[30:31] op_sel_hi:[1,0]
	v_pk_mul_f32 v[6:7], v[6:7], s[30:31] op_sel_hi:[1,0]
	v_pk_mul_f32 v[8:9], v[8:9], s[30:31] op_sel_hi:[1,0]
	v_pk_mul_f32 v[10:11], v[10:11], s[30:31] op_sel_hi:[1,0]
	v_pk_mul_f32 v[12:13], v[12:13], s[30:31] op_sel_hi:[1,0]
	v_pk_mul_f32 v[14:15], v[14:15], s[30:31] op_sel_hi:[1,0]
	v_pk_mul_f32 v[16:17], v[16:17], s[30:31] op_sel_hi:[1,0]
	v_pk_mul_f32 v[18:19], v[18:19], s[30:31] op_sel_hi:[1,0]
	v_pk_mul_f32 v[20:21], v[20:21], s[30:31] op_sel_hi:[1,0]
	v_pk_mul_f32 v[22:23], v[22:23], s[30:31] op_sel_hi:[1,0]
	v_pk_mul_f32 v[24:25], v[24:25], s[30:31] op_sel_hi:[1,0]
	v_pk_mul_f32 v[26:27], v[26:27], s[30:31] op_sel_hi:[1,0]
	v_pk_mul_f32 v[28:29], v[28:29], s[30:31] op_sel_hi:[1,0]
	v_pk_mul_f32 v[30:31], v[30:31], s[30:31] op_sel_hi:[1,0]
	v_pk_mul_f32 v[32:33], v[32:33], s[30:31] op_sel_hi:[1,0]
	v_pk_mul_f32 v[34:35], v[34:35], s[30:31] op_sel_hi:[1,0]
	v_pk_mul_f32 v[36:37], v[36:37], s[30:31] op_sel_hi:[1,0]
	v_pk_mul_f32 v[38:39], v[38:39], s[30:31] op_sel_hi:[1,0]
	v_pk_mul_f32 v[40:41], v[40:41], s[30:31] op_sel_hi:[1,0]
	v_pk_mul_f32 v[42:43], v[42:43], s[30:31] op_sel_hi:[1,0]
	v_pk_mul_f32 v[44:45], v[44:45], s[30:31] op_sel_hi:[1,0]
	v_pk_mul_f32 v[46:47], v[46:47], s[30:31] op_sel_hi:[1,0]
	v_pk_mul_f32 v[48:49], v[48:49], s[30:31] op_sel_hi:[1,0]
	v_pk_mul_f32 v[50:51], v[50:51], s[30:31] op_sel_hi:[1,0]
	v_pk_mul_f32 v[52:53], v[52:53], s[30:31] op_sel_hi:[1,0]
	v_pk_mul_f32 v[54:55], v[54:55], s[30:31] op_sel_hi:[1,0]
	v_pk_mul_f32 v[56:57], v[56:57], s[30:31] op_sel_hi:[1,0]
	v_pk_mul_f32 v[58:59], v[58:59], s[30:31] op_sel_hi:[1,0]
	v_pk_mul_f32 v[60:61], v[60:61], s[30:31] op_sel_hi:[1,0]
	v_pk_mul_f32 v[62:63], v[62:63], s[30:31] op_sel_hi:[1,0]
	v_med3_f32 v0, v0, s24, v237
	v_med3_f32 v1, v1, s24, v237
	v_med3_f32 v2, v2, s24, v237
	v_med3_f32 v3, v3, s24, v237
	v_med3_f32 v4, v4, s24, v237
	v_med3_f32 v5, v5, s24, v237
	v_med3_f32 v6, v6, s24, v237
	v_med3_f32 v7, v7, s24, v237
	v_med3_f32 v8, v8, s24, v237
	v_med3_f32 v9, v9, s24, v237
	v_med3_f32 v10, v10, s24, v237
	v_med3_f32 v11, v11, s24, v237
	v_med3_f32 v12, v12, s24, v237
	v_med3_f32 v13, v13, s24, v237
	v_med3_f32 v14, v14, s24, v237
	v_med3_f32 v15, v15, s24, v237
	v_med3_f32 v16, v16, s24, v237
	v_med3_f32 v17, v17, s24, v237
	v_med3_f32 v18, v18, s24, v237
	v_med3_f32 v19, v19, s24, v237
	v_med3_f32 v20, v20, s24, v237
	v_med3_f32 v21, v21, s24, v237
	v_med3_f32 v22, v22, s24, v237
	v_med3_f32 v23, v23, s24, v237
	v_med3_f32 v24, v24, s24, v237
	v_med3_f32 v25, v25, s24, v237
	v_med3_f32 v26, v26, s24, v237
	v_med3_f32 v27, v27, s24, v237
	v_med3_f32 v28, v28, s24, v237
	v_med3_f32 v29, v29, s24, v237
	v_med3_f32 v30, v30, s24, v237
	v_med3_f32 v31, v31, s24, v237
	v_med3_f32 v32, v32, s24, v237
	v_med3_f32 v33, v33, s24, v237
	v_med3_f32 v34, v34, s24, v237
	v_med3_f32 v35, v35, s24, v237
	v_med3_f32 v36, v36, s24, v237
	v_med3_f32 v37, v37, s24, v237
	v_med3_f32 v38, v38, s24, v237
	v_med3_f32 v39, v39, s24, v237
	v_med3_f32 v40, v40, s24, v237
	v_med3_f32 v41, v41, s24, v237
	v_med3_f32 v42, v42, s24, v237
	v_med3_f32 v43, v43, s24, v237
	v_med3_f32 v44, v44, s24, v237
	v_med3_f32 v45, v45, s24, v237
	v_med3_f32 v46, v46, s24, v237
	v_med3_f32 v47, v47, s24, v237
	v_med3_f32 v48, v48, s24, v237
	v_med3_f32 v49, v49, s24, v237
	v_med3_f32 v50, v50, s24, v237
	v_med3_f32 v51, v51, s24, v237
	v_med3_f32 v52, v52, s24, v237
	v_med3_f32 v53, v53, s24, v237
	v_med3_f32 v54, v54, s24, v237
	v_med3_f32 v55, v55, s24, v237
	v_med3_f32 v56, v56, s24, v237
	v_med3_f32 v57, v57, s24, v237
	v_med3_f32 v58, v58, s24, v237
	v_med3_f32 v59, v59, s24, v237
	v_med3_f32 v60, v60, s24, v237
	v_med3_f32 v61, v61, s24, v237
	v_med3_f32 v62, v62, s24, v237
	v_med3_f32 v63, v63, s24, v237
	v_cvt_pk_fp8_f32 v0, v0, v4
	v_cvt_pk_fp8_f32 v0, v8, v12 op_sel:[0,0,1]
	v_cvt_pk_fp8_f32 v4, v1, v5
	v_cvt_pk_fp8_f32 v4, v9, v13 op_sel:[0,0,1]
	v_cvt_pk_fp8_f32 v8, v2, v6
	v_cvt_pk_fp8_f32 v8, v10, v14 op_sel:[0,0,1]
	v_cvt_pk_fp8_f32 v12, v3, v7
	v_cvt_pk_fp8_f32 v12, v11, v15 op_sel:[0,0,1]
	v_cvt_pk_fp8_f32 v1, v16, v20
	v_cvt_pk_fp8_f32 v1, v24, v28 op_sel:[0,0,1]
	v_cvt_pk_fp8_f32 v5, v17, v21
	v_cvt_pk_fp8_f32 v5, v25, v29 op_sel:[0,0,1]
	v_cvt_pk_fp8_f32 v9, v18, v22
	v_cvt_pk_fp8_f32 v9, v26, v30 op_sel:[0,0,1]
	v_cvt_pk_fp8_f32 v13, v19, v23
	v_cvt_pk_fp8_f32 v13, v27, v31 op_sel:[0,0,1]
	v_cvt_pk_fp8_f32 v2, v32, v36
	v_cvt_pk_fp8_f32 v2, v40, v44 op_sel:[0,0,1]
	v_cvt_pk_fp8_f32 v6, v33, v37
	v_cvt_pk_fp8_f32 v6, v41, v45 op_sel:[0,0,1]
	v_cvt_pk_fp8_f32 v10, v34, v38
	v_cvt_pk_fp8_f32 v10, v42, v46 op_sel:[0,0,1]
	v_cvt_pk_fp8_f32 v14, v35, v39
	v_cvt_pk_fp8_f32 v14, v43, v47 op_sel:[0,0,1]
	v_cvt_pk_fp8_f32 v3, v48, v52
	v_cvt_pk_fp8_f32 v3, v56, v60 op_sel:[0,0,1]
	v_cvt_pk_fp8_f32 v7, v49, v53
	v_cvt_pk_fp8_f32 v7, v57, v61 op_sel:[0,0,1]
	v_cvt_pk_fp8_f32 v11, v50, v54
	v_cvt_pk_fp8_f32 v11, v58, v62 op_sel:[0,0,1]
	v_cvt_pk_fp8_f32 v15, v51, v55
	v_cvt_pk_fp8_f32 v15, v59, v63 op_sel:[0,0,1]
	global_store_dwordx4 v250, v[0:3], s[42:43] nt
	global_store_dwordx4 v250, v[4:7], s[42:43] offset:2048 nt
	global_store_dwordx4 v251, v[8:11], s[42:43] nt
	global_store_dwordx4 v251, v[12:15], s[42:43] offset:2048 nt
	s_add_u32 s42, s42, 0x800000
	s_addc_u32 s43, s43, 0
	global_load_dwordx4 v[0:3], v246, s[4:5] nt
	global_load_dwordx4 v[4:7], v247, s[4:5] nt
	global_load_dwordx4 v[8:11], v248, s[4:5] nt
	global_load_dwordx4 v[12:15], v249, s[4:5] nt
	global_load_dwordx4 v[16:19], v246, s[6:7] nt
	global_load_dwordx4 v[20:23], v247, s[6:7] nt
	global_load_dwordx4 v[24:27], v248, s[6:7] nt
	global_load_dwordx4 v[28:31], v249, s[6:7] nt
	global_load_dwordx4 v[32:35], v246, s[8:9] nt
	global_load_dwordx4 v[36:39], v247, s[8:9] nt
	global_load_dwordx4 v[40:43], v248, s[8:9] nt
	global_load_dwordx4 v[44:47], v249, s[8:9] nt
	global_load_dwordx4 v[48:51], v246, s[38:39] nt
	global_load_dwordx4 v[52:55], v247, s[38:39] nt
	global_load_dwordx4 v[56:59], v248, s[38:39] nt
	global_load_dwordx4 v[60:63], v249, s[38:39] nt
	s_add_u32 s4, s4, 0x2000000
	s_addc_u32 s5, s5, 0
	s_add_u32 s6, s6, 0x2000000
	s_addc_u32 s7, s7, 0
	s_add_u32 s8, s8, 0x2000000
	s_addc_u32 s9, s9, 0
	s_add_u32 s38, s38, 0x2000000
	s_addc_u32 s39, s39, 0
	s_waitcnt vmcnt(40)
; #define GAS __attribute__((address_space(1)))
; template <bool GAIN, bool NT = false> __device__ __forceinline__ void titem8_store(const TItem& d, int lane, const f32x4 (&r)[16], const f32x4 (&g)[4]) {
;     const int q = lane & 7, kg = lane >> 3; const unsigned lo = (unsigned)((4 * q) * d.ldk + 16 * kg);
;     GAS char* base = (GAS char*)d.dst;
;     f32x4 s[16];
; #pragma unroll
;     for (int j = 0; j < 16; ++j) s[j] = r[j] * ((GAIN ? g[j >> 2][j & 3] : 1.0f) * W8_SCALE);
; #pragma unroll
;     for (int i = 0; i < 4; ++i) { v4u w;
;         w.x = pk4_fp8w(s[0][i], s[1][i], s[2][i], s[3][i]); w.y = pk4_fp8w(s[4][i], s[5][i], s[6][i], s[7][i]);
;         w.z = pk4_fp8w(s[8][i], s[9][i], s[10][i], s[11][i]); w.w = pk4_fp8w(s[12][i], s[13][i], s[14][i], s[15][i]);
;         GAS v4u* p = (GAS v4u*)(base + (size_t)i * (size_t)d.ldk + lo);
;         if (NT) __builtin_nontemporal_store(w, p); else *p = w; }
	v_pk_mul_f32 v[66:67], v[66:67], s[30:31] op_sel_hi:[1,0]
	v_pk_mul_f32 v[68:69], v[68:69], s[30:31] op_sel_hi:[1,0]
	v_pk_mul_f32 v[70:71], v[70:71], s[30:31] op_sel_hi:[1,0]
	v_pk_mul_f32 v[72:73], v[72:73], s[30:31] op_sel_hi:[1,0]
	v_pk_mul_f32 v[74:75], v[74:75], s[30:31] op_sel_hi:[1,0]
	v_pk_mul_f32 v[76:77], v[76:77], s[30:31] op_sel_hi:[1,0]
	v_pk_mul_f32 v[78:79], v[78:79], s[30:31] op_sel_hi:[1,0]
	v_pk_mul_f32 v[80:81], v[80:81], s[30:31] op_sel_hi:[1,0]
	v_pk_mul_f32 v[82:83], v[82:83], s[30:31] op_sel_hi:[1,0]
	v_pk_mul_f32 v[84:85], v[84:85], s[30:31] op_sel_hi:[1,0]
	v_pk_mul_f32 v[86:87], v[86:87], s[30:31] op_sel_hi:[1,0]
	v_pk_mul_f32 v[88:89], v[88:89], s[30:31] op_sel_hi:[1,0]
	v_pk_mul_f32 v[90:91], v[90:91], s[30:31] op_sel_hi:[1,0]
	v_pk_mul_f32 v[92:93], v[92:93], s[30:31] op_sel_hi:[1,0]
	v_pk_mul_f32 v[94:95], v[94:95], s[30:31] op_sel_hi:[1,0]
	v_pk_mul_f32 v[96:97], v[96:97], s[30:31] op_sel_hi:[1,0]
	v_pk_mul_f32 v[98:99], v[98:99], s[30:31] op_sel_hi:[1,0]
	v_pk_mul_f32 v[100:101], v[100:101], s[30:31] op_sel_hi:[1,0]
	v_pk_mul_f32 v[102:103], v[102:103], s[30:31] op_sel_hi:[1,0]
	v_pk_mul_f32 v[104:105], v[104:105], s[30:31] op_sel_hi:[1,0]
	v_pk_mul_f32 v[106:107], v[106:107], s[30:31] op_sel_hi:[1,0]
	v_pk_mul_f32 v[108:109], v[108:109], s[30:31] op_sel_hi:[1,0]
	v_pk_mul_f32 v[110:111], v[110:111], s[30:31] op_sel_hi:[1,0]
	v_pk_mul_f32 v[112:113], v[112:113], s[30:31] op_sel_hi:[1,0]
	v_pk_mul_f32 v[114:115], v[114:115], s[30:31] op_sel_hi:[1,0]
	v_pk_mul_f32 v[116:117], v[116:117], s[30:31] op_sel_hi:[1,0]
	v_pk_mul_f32 v[118:119], v[118:119], s[30:31] op_sel_hi:[1,0]
	v_pk_mul_f32 v[120:121], v[120:121], s[30:31] op_sel_hi:[1,0]
	v_pk_mul_f32 v[122:123], v[122:123], s[30:31] op_sel_hi:[1,0]
	v_pk_mul_f32 v[124:125], v[124:125], s[30:31] op_sel_hi:[1,0]
	v_pk_mul_f32 v[126:127], v[126:127], s[30:31] op_sel_hi:[1,0]
	v_pk_mul_f32 v[128:129], v[128:129], s[30:31] op_sel_hi:[1,0]
	v_med3_f32 v66, v66, s24, v237
	v_med3_f32 v67, v67, s24, v237
	v_med3_f32 v68, v68, s24, v237
	v_med3_f32 v69, v69, s24, v237
	v_med3_f32 v70, v70, s24, v237
	v_med3_f32 v71, v71, s24, v237
	v_med3_f32 v72, v72, s24, v237
	v_med3_f32 v73, v73, s24, v237
	v_med3_f32 v74, v74, s24, v237
	v_med3_f32 v75, v75, s24, v237
	v_med3_f32 v76, v76, s24, v237
	v_med3_f32 v77, v77, s24, v237
	v_med3_f32 v78, v78, s24, v237
	v_med3_f32 v79, v79, s24, v237
	v_med3_f32 v80, v80, s24, v237
	v_med3_f32 v81, v81, s24, v237
	v_med3_f32 v82, v82, s24, v237
	v_med3_f32 v83, v83, s24, v237
	v_med3_f32 v84, v84, s24, v237
	v_med3_f32 v85, v85, s24, v237
	v_med3_f32 v86, v86, s24, v237
	v_med3_f32 v87, v87, s24, v237
	v_med3_f32 v88, v88, s24, v237
	v_med3_f32 v89, v89, s24, v237
	v_med3_f32 v90, v90, s24, v237
	v_med3_f32 v91, v91, s24, v237
	v_med3_f32 v92, v92, s24, v237
	v_med3_f32 v93, v93, s24, v237
	v_med3_f32 v94, v94, s24, v237
	v_med3_f32 v95, v95, s24, v237
	v_med3_f32 v96, v96, s24, v237
	v_med3_f32 v97, v97, s24, v237
	v_med3_f32 v98, v98, s24, v237
	v_med3_f32 v99, v99, s24, v237
	v_med3_f32 v100, v100, s24, v237
	v_med3_f32 v101, v101, s24, v237
	v_med3_f32 v102, v102, s24, v237
	v_med3_f32 v103, v103, s24, v237
	v_med3_f32 v104, v104, s24, v237
	v_med3_f32 v105, v105, s24, v237
	v_med3_f32 v106, v106, s24, v237
	v_med3_f32 v107, v107, s24, v237
	v_med3_f32 v108, v108, s24, v237
	v_med3_f32 v109, v109, s24, v237
	v_med3_f32 v110, v110, s24, v237
	v_med3_f32 v111, v111, s24, v237
	v_med3_f32 v112, v112, s24, v237
	v_med3_f32 v113, v113, s24, v237
	v_med3_f32 v114, v114, s24, v237
	v_med3_f32 v115, v115, s24, v237
	v_med3_f32 v116, v116, s24, v237
	v_med3_f32 v117, v117, s24, v237
	v_med3_f32 v118, v118, s24, v237
	v_med3_f32 v119, v119, s24, v237
	v_med3_f32 v120, v120, s24, v237
	v_med3_f32 v121, v121, s24, v237
	v_med3_f32 v122, v122, s24, v237
	v_med3_f32 v123, v123, s24, v237
	v_med3_f32 v124, v124, s24, v237
	v_med3_f32 v125, v125, s24, v237
	v_med3_f32 v126, v126, s24, v237
	v_med3_f32 v127, v127, s24, v237
	v_med3_f32 v128, v128, s24, v237
	v_med3_f32 v129, v129, s24, v237
	v_cvt_pk_fp8_f32 v66, v66, v70
	v_cvt_pk_fp8_f32 v66, v74, v78 op_sel:[0,0,1]
	v_cvt_pk_fp8_f32 v70, v67, v71
	v_cvt_pk_fp8_f32 v70, v75, v79 op_sel:[0,0,1]
	v_cvt_pk_fp8_f32 v74, v68, v72
	v_cvt_pk_fp8_f32 v74, v76, v80 op_sel:[0,0,1]
	v_cvt_pk_fp8_f32 v78, v69, v73
	v_cvt_pk_fp8_f32 v78, v77, v81 op_sel:[0,0,1]
	v_cvt_pk_fp8_f32 v67, v82, v86
	v_cvt_pk_fp8_f32 v67, v90, v94 op_sel:[0,0,1]
	v_cvt_pk_fp8_f32 v71, v83, v87
	v_cvt_pk_fp8_f32 v71, v91, v95 op_sel:[0,0,1]
	v_cvt_pk_fp8_f32 v75, v84, v88
	v_cvt_pk_fp8_f32 v75, v92, v96 op_sel:[0,0,1]
	v_cvt_pk_fp8_f32 v79, v85, v89
	v_cvt_pk_fp8_f32 v79, v93, v97 op_sel:[0,0,1]
	v_cvt_pk_fp8_f32 v68, v98, v102
	v_cvt_pk_fp8_f32 v68, v106, v110 op_sel:[0,0,1]
	v_cvt_pk_fp8_f32 v72, v99, v103
	v_cvt_pk_fp8_f32 v72, v107, v111 op_sel:[0,0,1]
	v_cvt_pk_fp8_f32 v76, v100, v104
	v_cvt_pk_fp8_f32 v76, v108, v112 op_sel:[0,0,1]
	v_cvt_pk_fp8_f32 v80, v101, v105
	v_cvt_pk_fp8_f32 v80, v109, v113 op_sel:[0,0,1]
	v_cvt_pk_fp8_f32 v69, v114, v118
	v_cvt_pk_fp8_f32 v69, v122, v126 op_sel:[0,0,1]
	v_cvt_pk_fp8_f32 v73, v115, v119
	v_cvt_pk_fp8_f32 v73, v123, v127 op_sel:[0,0,1]
	v_cvt_pk_fp8_f32 v77, v116, v120
	v_cvt_pk_fp8_f32 v77, v124, v128 op_sel:[0,0,1]
	v_cvt_pk_fp8_f32 v81, v117, v121
	v_cvt_pk_fp8_f32 v81, v125, v129 op_sel:[0,0,1]
	global_store_dwordx4 v250, v[66:69], s[42:43] nt
	global_store_dwordx4 v250, v[70:73], s[42:43] offset:2048 nt
	global_store_dwordx4 v251, v[74:77], s[42:43] nt
	global_store_dwordx4 v251, v[78:81], s[42:43] offset:2048 nt
	s_add_u32 s42, s42, 0x800000
	s_addc_u32 s43, s43, 0
	s_waitcnt vmcnt(24)
; #define GAS __attribute__((address_space(1)))
; template <bool GAIN, bool NT = false> __device__ __forceinline__ void titem8_store(const TItem& d, int lane, const f32x4 (&r)[16], const f32x4 (&g)[4]) {
;     const int q = lane & 7, kg = lane >> 3; const unsigned lo = (unsigned)((4 * q) * d.ldk + 16 * kg);
;     GAS char* base = (GAS char*)d.dst;
;     f32x4 s[16];
; #pragma unroll
;     for (int j = 0; j < 16; ++j) s[j] = r[j] * ((GAIN ? g[j >> 2][j & 3] : 1.0f) * W8_SCALE);
; #pragma unroll
;     for (int i = 0; i < 4; ++i) { v4u w;
;         w.x = pk4_fp8w(s[0][i], s[1][i], s[2][i], s[3][i]); w.y = pk4_fp8w(s[4][i], s[5][i], s[6][i], s[7][i]);
;         w.z = pk4_fp8w(s[8][i], s[9][i], s[10][i], s[11][i]); w.w = pk4_fp8w(s[12][i], s[13][i], s[14][i], s[15][i]);
;         GAS v4u* p = (GAS v4u*)(base + (size_t)i * (size_t)d.ldk + lo);
;         if (NT) __builtin_nontemporal_store(w, p); else *p = w; }
	v_pk_mul_f32 v[130:131], v[130:131], s[30:31] op_sel_hi:[1,0]
	v_pk_mul_f32 v[132:133], v[132:133], s[30:31] op_sel_hi:[1,0]
	v_pk_mul_f32 v[134:135], v[134:135], s[30:31] op_sel_hi:[1,0]
	v_pk_mul_f32 v[136:137], v[136:137], s[30:31] op_sel_hi:[1,0]
	v_pk_mul_f32 v[138:139], v[138:139], s[30:31] op_sel_hi:[1,0]
	v_pk_mul_f32 v[140:141], v[140:141], s[30:31] op_sel_hi:[1,0]
	v_pk_mul_f32 v[142:143], v[142:143], s[30:31] op_sel_hi:[1,0]
	v_pk_mul_f32 v[144:145], v[144:145], s[30:31] op_sel_hi:[1,0]
	v_pk_mul_f32 v[146:147], v[146:147], s[30:31] op_sel_hi:[1,0]
	v_pk_mul_f32 v[148:149], v[148:149], s[30:31] op_sel_hi:[1,0]
	v_pk_mul_f32 v[150:151], v[150:151], s[30:31] op_sel_hi:[1,0]
	v_pk_mul_f32 v[152:153], v[152:153], s[30:31] op_sel_hi:[1,0]
	v_pk_mul_f32 v[154:155], v[154:155], s[30:31] op_sel_hi:[1,0]
	v_pk_mul_f32 v[156:157], v[156:157], s[30:31] op_sel_hi:[1,0]
	v_pk_mul_f32 v[158:159], v[158:159], s[30:31] op_sel_hi:[1,0]
	v_pk_mul_f32 v[160:161], v[160:161], s[30:31] op_sel_hi:[1,0]
	v_pk_mul_f32 v[162:163], v[162:163], s[30:31] op_sel_hi:[1,0]
	v_pk_mul_f32 v[164:165], v[164:165], s[30:31] op_sel_hi:[1,0]
	v_pk_mul_f32 v[166:167], v[166:167], s[30:31] op_sel_hi:[1,0]
	v_pk_mul_f32 v[168:169], v[168:169], s[30:31] op_sel_hi:[1,0]
	v_pk_mul_f32 v[170:171], v[170:171], s[30:31] op_sel_hi:[1,0]
	v_pk_mul_f32 v[172:173], v[172:173], s[30:31] op_sel_hi:[1,0]
	v_pk_mul_f32 v[174:175], v[174:175], s[30:31] op_sel_hi:[1,0]
	v_pk_mul_f32 v[176:177], v[176:177], s[30:31] op_sel_hi:[1,0]
	v_pk_mul_f32 v[178:179], v[178:179], s[30:31] op_sel_hi:[1,0]
	v_pk_mul_f32 v[180:181], v[180:181], s[30:31] op_sel_hi:[1,0]
	v_pk_mul_f32 v[182:183], v[182:183], s[30:31] op_sel_hi:[1,0]
	v_pk_mul_f32 v[184:185], v[184:185], s[30:31] op_sel_hi:[1,0]
	v_pk_mul_f32 v[186:187], v[186:187], s[30:31] op_sel_hi:[1,0]
	v_pk_mul_f32 v[188:189], v[188:189], s[30:31] op_sel_hi:[1,0]
	v_pk_mul_f32 v[190:191], v[190:191], s[30:31] op_sel_hi:[1,0]
	v_pk_mul_f32 v[192:193], v[192:193], s[30:31] op_sel_hi:[1,0]
	v_med3_f32 v130, v130, s24, v237
	v_med3_f32 v131, v131, s24, v237
	v_med3_f32 v132, v132, s24, v237
	v_med3_f32 v133, v133, s24, v237
	v_med3_f32 v134, v134, s24, v237
	v_med3_f32 v135, v135, s24, v237
	v_med3_f32 v136, v136, s24, v237
	v_med3_f32 v137, v137, s24, v237
	v_med3_f32 v138, v138, s24, v237
	v_med3_f32 v139, v139, s24, v237
	v_med3_f32 v140, v140, s24, v237
	v_med3_f32 v141, v141, s24, v237
	v_med3_f32 v142, v142, s24, v237
	v_med3_f32 v143, v143, s24, v237
	v_med3_f32 v144, v144, s24, v237
	v_med3_f32 v145, v145, s24, v237
	v_med3_f32 v146, v146, s24, v237
	v_med3_f32 v147, v147, s24, v237
	v_med3_f32 v148, v148, s24, v237
	v_med3_f32 v149, v149, s24, v237
	v_med3_f32 v150, v150, s24, v237
	v_med3_f32 v151, v151, s24, v237
	v_med3_f32 v152, v152, s24, v237
	v_med3_f32 v153, v153, s24, v237
	v_med3_f32 v154, v154, s24, v237
	v_med3_f32 v155, v155, s24, v237
	v_med3_f32 v156, v156, s24, v237
	v_med3_f32 v157, v157, s24, v237
	v_med3_f32 v158, v158, s24, v237
	v_med3_f32 v159, v159, s24, v237
	v_med3_f32 v160, v160, s24, v237
	v_med3_f32 v161, v161, s24, v237
	v_med3_f32 v162, v162, s24, v237
	v_med3_f32 v163, v163, s24, v237
	v_med3_f32 v164, v164, s24, v237
	v_med3_f32 v165, v165, s24, v237
	v_med3_f32 v166, v166, s24, v237
	v_med3_f32 v167, v167, s24, v237
	v_med3_f32 v168, v168, s24, v237
	v_med3_f32 v169, v169, s24, v237
	v_med3_f32 v170, v170, s24, v237
	v_med3_f32 v171, v171, s24, v237
	v_med3_f32 v172, v172, s24, v237
	v_med3_f32 v173, v173, s24, v237
	v_med3_f32 v174, v174, s24, v237
	v_med3_f32 v175, v175, s24, v237
	v_med3_f32 v176, v176, s24, v237
	v_med3_f32 v177, v177, s24, v237
	v_med3_f32 v178, v178, s24, v237
	v_med3_f32 v179, v179, s24, v237
	v_med3_f32 v180, v180, s24, v237
	v_med3_f32 v181, v181, s24, v237
	v_med3_f32 v182, v182, s24, v237
	v_med3_f32 v183, v183, s24, v237
	v_med3_f32 v184, v184, s24, v237
	v_med3_f32 v185, v185, s24, v237
	v_med3_f32 v186, v186, s24, v237
	v_med3_f32 v187, v187, s24, v237
	v_med3_f32 v188, v188, s24, v237
	v_med3_f32 v189, v189, s24, v237
	v_med3_f32 v190, v190, s24, v237
	v_med3_f32 v191, v191, s24, v237
	v_med3_f32 v192, v192, s24, v237
	v_med3_f32 v193, v193, s24, v237
	v_cvt_pk_fp8_f32 v130, v130, v134
	v_cvt_pk_fp8_f32 v130, v138, v142 op_sel:[0,0,1]
	v_cvt_pk_fp8_f32 v134, v131, v135
	v_cvt_pk_fp8_f32 v134, v139, v143 op_sel:[0,0,1]
	v_cvt_pk_fp8_f32 v138, v132, v136
	v_cvt_pk_fp8_f32 v138, v140, v144 op_sel:[0,0,1]
	v_cvt_pk_fp8_f32 v142, v133, v137
	v_cvt_pk_fp8_f32 v142, v141, v145 op_sel:[0,0,1]
	v_cvt_pk_fp8_f32 v131, v146, v150
	v_cvt_pk_fp8_f32 v131, v154, v158 op_sel:[0,0,1]
	v_cvt_pk_fp8_f32 v135, v147, v151
	v_cvt_pk_fp8_f32 v135, v155, v159 op_sel:[0,0,1]
	v_cvt_pk_fp8_f32 v139, v148, v152
	v_cvt_pk_fp8_f32 v139, v156, v160 op_sel:[0,0,1]
	v_cvt_pk_fp8_f32 v143, v149, v153
	v_cvt_pk_fp8_f32 v143, v157, v161 op_sel:[0,0,1]
	v_cvt_pk_fp8_f32 v132, v162, v166
	v_cvt_pk_fp8_f32 v132, v170, v174 op_sel:[0,0,1]
	v_cvt_pk_fp8_f32 v136, v163, v167
	v_cvt_pk_fp8_f32 v136, v171, v175 op_sel:[0,0,1]
	v_cvt_pk_fp8_f32 v140, v164, v168
	v_cvt_pk_fp8_f32 v140, v172, v176 op_sel:[0,0,1]
	v_cvt_pk_fp8_f32 v144, v165, v169
	v_cvt_pk_fp8_f32 v144, v173, v177 op_sel:[0,0,1]
	v_cvt_pk_fp8_f32 v133, v178, v182
	v_cvt_pk_fp8_f32 v133, v186, v190 op_sel:[0,0,1]
	v_cvt_pk_fp8_f32 v137, v179, v183
	v_cvt_pk_fp8_f32 v137, v187, v191 op_sel:[0,0,1]
	v_cvt_pk_fp8_f32 v141, v180, v184
	v_cvt_pk_fp8_f32 v141, v188, v192 op_sel:[0,0,1]
	v_cvt_pk_fp8_f32 v145, v181, v185
	v_cvt_pk_fp8_f32 v145, v189, v193 op_sel:[0,0,1]
	global_store_dwordx4 v250, v[130:133], s[42:43] nt
	global_store_dwordx4 v250, v[134:137], s[42:43] offset:2048 nt
	global_store_dwordx4 v251, v[138:141], s[42:43] nt
	global_store_dwordx4 v251, v[142:145], s[42:43] offset:2048 nt
	s_add_u32 s42, s42, 0x800000
	s_addc_u32 s43, s43, 0
	s_waitcnt vmcnt(8)
; #define GAS __attribute__((address_space(1)))
; template <bool GAIN, bool NT = false> __device__ __forceinline__ void titem8_store(const TItem& d, int lane, const f32x4 (&r)[16], const f32x4 (&g)[4]) {
;     const int q = lane & 7, kg = lane >> 3; const unsigned lo = (unsigned)((4 * q) * d.ldk + 16 * kg);
;     GAS char* base = (GAS char*)d.dst;
;     f32x4 s[16];
; #pragma unroll
;     for (int j = 0; j < 16; ++j) s[j] = r[j] * ((GAIN ? g[j >> 2][j & 3] : 1.0f) * W8_SCALE);
; #pragma unroll
;     for (int i = 0; i < 4; ++i) { v4u w;
;         w.x = pk4_fp8w(s[0][i], s[1][i], s[2][i], s[3][i]); w.y = pk4_fp8w(s[4][i], s[5][i], s[6][i], s[7][i]);
;         w.z = pk4_fp8w(s[8][i], s[9][i], s[10][i], s[11][i]); w.w = pk4_fp8w(s[12][i], s[13][i], s[14][i], s[15][i]);
;         GAS v4u* p = (GAS v4u*)(base + (size_t)i * (size_t)d.ldk + lo);
;         if (NT) __builtin_nontemporal_store(w, p); else *p = w; }
;     __device__ __forceinline__ void done(const Unit& u) const { if (u.pm == (c & 7)) convert_share(); }
	v_pk_mul_f32 v[0:1], v[0:1], s[30:31] op_sel_hi:[1,0]
	v_pk_mul_f32 v[2:3], v[2:3], s[30:31] op_sel_hi:[1,0]
	v_pk_mul_f32 v[4:5], v[4:5], s[30:31] op_sel_hi:[1,0]
	v_pk_mul_f32 v[6:7], v[6:7], s[30:31] op_sel_hi:[1,0]
	v_pk_mul_f32 v[8:9], v[8:9], s[30:31] op_sel_hi:[1,0]
	v_pk_mul_f32 v[10:11], v[10:11], s[30:31] op_sel_hi:[1,0]
	v_pk_mul_f32 v[12:13], v[12:13], s[30:31] op_sel_hi:[1,0]
	v_pk_mul_f32 v[14:15], v[14:15], s[30:31] op_sel_hi:[1,0]
	v_pk_mul_f32 v[16:17], v[16:17], s[30:31] op_sel_hi:[1,0]
	v_pk_mul_f32 v[18:19], v[18:19], s[30:31] op_sel_hi:[1,0]
	v_pk_mul_f32 v[20:21], v[20:21], s[30:31] op_sel_hi:[1,0]
	v_pk_mul_f32 v[22:23], v[22:23], s[30:31] op_sel_hi:[1,0]
	v_pk_mul_f32 v[24:25], v[24:25], s[30:31] op_sel_hi:[1,0]
	v_pk_mul_f32 v[26:27], v[26:27], s[30:31] op_sel_hi:[1,0]
	v_pk_mul_f32 v[28:29], v[28:29], s[30:31] op_sel_hi:[1,0]
	v_pk_mul_f32 v[30:31], v[30:31], s[30:31] op_sel_hi:[1,0]
	v_pk_mul_f32 v[32:33], v[32:33], s[30:31] op_sel_hi:[1,0]
	v_pk_mul_f32 v[34:35], v[34:35], s[30:31] op_sel_hi:[1,0]
	v_pk_mul_f32 v[36:37], v[36:37], s[30:31] op_sel_hi:[1,0]
	v_pk_mul_f32 v[38:39], v[38:39], s[30:31] op_sel_hi:[1,0]
	v_pk_mul_f32 v[40:41], v[40:41], s[30:31] op_sel_hi:[1,0]
	v_pk_mul_f32 v[42:43], v[42:43], s[30:31] op_sel_hi:[1,0]
	v_pk_mul_f32 v[44:45], v[44:45], s[30:31] op_sel_hi:[1,0]
	v_pk_mul_f32 v[46:47], v[46:47], s[30:31] op_sel_hi:[1,0]
	v_pk_mul_f32 v[48:49], v[48:49], s[30:31] op_sel_hi:[1,0]
	v_pk_mul_f32 v[50:51], v[50:51], s[30:31] op_sel_hi:[1,0]
	v_pk_mul_f32 v[52:53], v[52:53], s[30:31] op_sel_hi:[1,0]
	v_pk_mul_f32 v[54:55], v[54:55], s[30:31] op_sel_hi:[1,0]
	v_pk_mul_f32 v[56:57], v[56:57], s[30:31] op_sel_hi:[1,0]
	v_pk_mul_f32 v[58:59], v[58:59], s[30:31] op_sel_hi:[1,0]
	v_pk_mul_f32 v[60:61], v[60:61], s[30:31] op_sel_hi:[1,0]
	v_pk_mul_f32 v[62:63], v[62:63], s[30:31] op_sel_hi:[1,0]
	v_med3_f32 v0, v0, s24, v237
	v_med3_f32 v1, v1, s24, v237
	v_med3_f32 v2, v2, s24, v237
	v_med3_f32 v3, v3, s24, v237
	v_med3_f32 v4, v4, s24, v237
	v_med3_f32 v5, v5, s24, v237
	v_med3_f32 v6, v6, s24, v237
	v_med3_f32 v7, v7, s24, v237
	v_med3_f32 v8, v8, s24, v237
	v_med3_f32 v9, v9, s24, v237
	v_med3_f32 v10, v10, s24, v237
	v_med3_f32 v11, v11, s24, v237
	v_med3_f32 v12, v12, s24, v237
	v_med3_f32 v13, v13, s24, v237
	v_med3_f32 v14, v14, s24, v237
	v_med3_f32 v15, v15, s24, v237
	v_med3_f32 v16, v16, s24, v237
	v_med3_f32 v17, v17, s24, v237
	v_med3_f32 v18, v18, s24, v237
	v_med3_f32 v19, v19, s24, v237
	v_med3_f32 v20, v20, s24, v237
	v_med3_f32 v21, v21, s24, v237
	v_med3_f32 v22, v22, s24, v237
	v_med3_f32 v23, v23, s24, v237
	v_med3_f32 v24, v24, s24, v237
	v_med3_f32 v25, v25, s24, v237
	v_med3_f32 v26, v26, s24, v237
	v_med3_f32 v27, v27, s24, v237
	v_med3_f32 v28, v28, s24, v237
	v_med3_f32 v29, v29, s24, v237
	v_med3_f32 v30, v30, s24, v237
	v_med3_f32 v31, v31, s24, v237
	v_med3_f32 v32, v32, s24, v237
	v_med3_f32 v33, v33, s24, v237
	v_med3_f32 v34, v34, s24, v237
	v_med3_f32 v35, v35, s24, v237
	v_med3_f32 v36, v36, s24, v237
	v_med3_f32 v37, v37, s24, v237
	v_med3_f32 v38, v38, s24, v237
	v_med3_f32 v39, v39, s24, v237
	v_med3_f32 v40, v40, s24, v237
	v_med3_f32 v41, v41, s24, v237
	v_med3_f32 v42, v42, s24, v237
	v_med3_f32 v43, v43, s24, v237
	v_med3_f32 v44, v44, s24, v237
	v_med3_f32 v45, v45, s24, v237
	v_med3_f32 v46, v46, s24, v237
	v_med3_f32 v47, v47, s24, v237
	v_med3_f32 v48, v48, s24, v237
	v_med3_f32 v49, v49, s24, v237
	v_med3_f32 v50, v50, s24, v237
	v_med3_f32 v51, v51, s24, v237
	v_med3_f32 v52, v52, s24, v237
	v_med3_f32 v53, v53, s24, v237
	v_med3_f32 v54, v54, s24, v237
	v_med3_f32 v55, v55, s24, v237
	v_med3_f32 v56, v56, s24, v237
	v_med3_f32 v57, v57, s24, v237
	v_med3_f32 v58, v58, s24, v237
	v_med3_f32 v59, v59, s24, v237
	v_med3_f32 v60, v60, s24, v237
	v_med3_f32 v61, v61, s24, v237
	v_med3_f32 v62, v62, s24, v237
	v_med3_f32 v63, v63, s24, v237
	v_cvt_pk_fp8_f32 v0, v0, v4
	v_cvt_pk_fp8_f32 v0, v8, v12 op_sel:[0,0,1]
	v_cvt_pk_fp8_f32 v4, v1, v5
	v_cvt_pk_fp8_f32 v4, v9, v13 op_sel:[0,0,1]
	v_cvt_pk_fp8_f32 v8, v2, v6
	v_cvt_pk_fp8_f32 v8, v10, v14 op_sel:[0,0,1]
	v_cvt_pk_fp8_f32 v12, v3, v7
	v_cvt_pk_fp8_f32 v12, v11, v15 op_sel:[0,0,1]
	v_cvt_pk_fp8_f32 v1, v16, v20
	v_cvt_pk_fp8_f32 v1, v24, v28 op_sel:[0,0,1]
	v_cvt_pk_fp8_f32 v5, v17, v21
	v_cvt_pk_fp8_f32 v5, v25, v29 op_sel:[0,0,1]
	v_cvt_pk_fp8_f32 v9, v18, v22
	v_cvt_pk_fp8_f32 v9, v26, v30 op_sel:[0,0,1]
	v_cvt_pk_fp8_f32 v13, v19, v23
	v_cvt_pk_fp8_f32 v13, v27, v31 op_sel:[0,0,1]
	v_cvt_pk_fp8_f32 v2, v32, v36
	v_cvt_pk_fp8_f32 v2, v40, v44 op_sel:[0,0,1]
	v_cvt_pk_fp8_f32 v6, v33, v37
	v_cvt_pk_fp8_f32 v6, v41, v45 op_sel:[0,0,1]
	v_cvt_pk_fp8_f32 v10, v34, v38
	v_cvt_pk_fp8_f32 v10, v42, v46 op_sel:[0,0,1]
	v_cvt_pk_fp8_f32 v14, v35, v39
	v_cvt_pk_fp8_f32 v14, v43, v47 op_sel:[0,0,1]
	v_cvt_pk_fp8_f32 v3, v48, v52
	v_cvt_pk_fp8_f32 v3, v56, v60 op_sel:[0,0,1]
	v_cvt_pk_fp8_f32 v7, v49, v53
	v_cvt_pk_fp8_f32 v7, v57, v61 op_sel:[0,0,1]
	v_cvt_pk_fp8_f32 v11, v50, v54
	v_cvt_pk_fp8_f32 v11, v58, v62 op_sel:[0,0,1]
	v_cvt_pk_fp8_f32 v15, v51, v55
	v_cvt_pk_fp8_f32 v15, v59, v63 op_sel:[0,0,1]
	global_store_dwordx4 v250, v[0:3], s[42:43] nt
	global_store_dwordx4 v250, v[4:7], s[42:43] offset:2048 nt
	global_store_dwordx4 v251, v[8:11], s[42:43] nt
	global_store_dwordx4 v251, v[12:15], s[42:43] offset:2048 nt
	s_add_u32 s42, s42, 0x800000
	s_addc_u32 s43, s43, 0
	v_mov_b32_e32 v65, 0
